# YI loads of the S5 state-output GEMM epilogue kept in flight (rolling prefetch) under the gelu math
# speedup vs baseline: 1.0023x; 1.0023x over previous
; __device__ __forceinline__ float gelu_tanh(float x) { return x * sigmoidf_(1.5957691216057308f * (x + 0.044715f * x * x * x)); }
; __device__ __forceinline__ unsigned cvt_pk_bf16(float lo, float hi) { const f32x2c v = {lo, hi}; const bf16x2c b = __builtin_convertvector(v, bf16x2c); return __builtin_bit_cast(unsigned, b); }
;     __device__ __forceinline__ void operator()(const f32x4 (&acc)[2][2][4][2], const Unit& u, int wr, int wc, int fr, int fq) const {
;         const int row0 = u.pm * BM + wr * 64 + fr, col0 = u.pn * BM + wc * 32 + 8 * fq;
; #pragma unroll
;         for (int ai = 0; ai < 2; ++ai)
; #pragma unroll
;             for (int m = 0; m < 4; ++m) { const int row = row0 + ai * HALF + m * 16; const int g = row / S5R, rl = row % S5R;
; #pragma unroll
;                 for (int bj = 0; bj < 2; ++bj) { const int col = col0 + bj * HALF;
;                     const u32x4 yi = *(const u32x4*)(YI + (size_t)row * 512 + col);
;                     const unsigned yw[4] = {yi.x, yi.y, yi.z, yi.w};
;                     const f32x4 v0 = acc[ai][bj][m][0], v1 = acc[ai][bj][m][1];
;                     float o[8];
; #pragma unroll
;                     for (int q = 0; q < 4; ++q) { const float al = (q < 2) ? v0[2 * q] : v1[2 * q - 4], ah = (q < 2) ? v0[2 * q + 1] : v1[2 * q - 3];
;                         o[2 * q] = gelu_tanh(al + __builtin_bit_cast(float, yw[q] << 16)); o[2 * q + 1] = gelu_tanh(ah + __builtin_bit_cast(float, yw[q] & 0xffff0000u)); }
;                     u32x4 w; w.x = cvt_pk_bf16(o[0], o[1]); w.y = cvt_pk_bf16(o[2], o[3]); w.z = cvt_pk_bf16(o[4], o[5]); w.w = cvt_pk_bf16(o[6], o[7]);
;                     const size_t tok = (size_t)rl * S5L + (col >> 4);
;                     *(u32x4*)(Z + tok * 512 + g * 16 + (col & 15)) = w; } }
.LBB0_1895:
	v_lshl_add_u32 v142, s33, 8, v154
	v_ashrrev_i32_e32 v143, 31, v142
	v_lshrrev_b32_e32 v160, 21, v143
	v_add_u32_e32 v128, v142, v160
	v_ashrrev_i32_e32 v144, 11, v128
	v_mul_i32_i24_e32 v128, 0x800, v144
	v_lshl_or_b32 v146, s46, 8, v156
	v_sub_u32_e32 v128, v142, v128
	v_lshlrev_b64 v[130:131], 10, v[142:143]
	v_ashrrev_i32_e32 v129, 31, v128
	v_ashrrev_i32_e32 v147, 31, v146
	v_lshlrev_b64 v[150:151], 15, v[128:129]
	v_lshlrev_b32_e32 v148, 4, v144
	v_lshl_add_u64 v[128:129], s[30:31], 0, v[130:131]
	v_lshlrev_b64 v[144:145], 1, v[146:147]
	v_lshl_add_u64 v[152:153], v[128:129], 0, v[144:145]
	v_mov_b32_e32 v166, v152
	v_mov_b32_e32 v167, v153
	global_load_dwordx4 v[170:173], v[166:167], off
	global_load_dwordx4 v[174:177], v[166:167], off offset:256
	s_mov_b64 s[98:99], 0x4000
	v_lshl_add_u64 v[168:169], v[166:167], 0, s[98:99]
	global_load_dwordx4 v[178:181], v[168:169], off
	global_load_dwordx4 v[182:185], v[168:169], off offset:256
	s_mov_b64 s[98:99], 0x8000
	v_lshl_add_u64 v[168:169], v[166:167], 0, s[98:99]
	global_load_dwordx4 v[186:189], v[168:169], off
	global_load_dwordx4 v[190:193], v[168:169], off offset:256
	s_mov_b64 s[98:99], 0xc000
	v_lshl_add_u64 v[168:169], v[166:167], 0, s[98:99]
	global_load_dwordx4 v[194:197], v[168:169], off
	global_load_dwordx4 v[198:201], v[168:169], off offset:256
	s_mov_b64 s[98:99], 0x20000
	v_lshl_add_u64 v[168:169], v[166:167], 0, s[98:99]
	global_load_dwordx4 v[202:205], v[168:169], off
	v_ashrrev_i32_e32 v149, 31, v148
	v_readlane_b32 s86, v243, 25
	s_waitcnt vmcnt(8)
	v_mov_b32_e32 v128, v170
	v_mov_b32_e32 v129, v171
	v_mov_b32_e32 v130, v172
	v_mov_b32_e32 v131, v173
	global_load_dwordx4 v[170:173], v[168:169], off offset:256
	v_lshlrev_b32_e32 v162, 16, v128
	v_and_b32_e32 v163, 0xffff0000, v128
	v_pk_add_f32 v[124:125], v[124:125], v[162:163]
	s_nop 0
	v_mul_f32_e32 v128, 0x3d372713, v124
	v_mul_f32_e32 v128, v124, v128
	v_fma_f32 v128, v124, v128, v124
	v_mul_f32_e32 v128, 0x3fcc422a, v128
	v_mul_f32_e32 v128, 0xbfb8aa3b, v128
	v_exp_f32_e32 v162, v128
	v_mul_f32_e32 v128, 0x3d372713, v125
	v_mul_f32_e32 v128, v125, v128
	v_fma_f32 v128, v125, v128, v125
	v_mul_f32_e32 v128, 0x3fcc422a, v128
	v_mul_f32_e32 v128, 0xbfb8aa3b, v128
	v_exp_f32_e32 v163, v128
	s_nop 0
	v_pk_add_f32 v[162:163], v[162:163], 1.0 op_sel_hi:[1,0]
	s_nop 0
	v_div_scale_f32 v128, s[46:47], v163, v163, 1.0
	v_rcp_f32_e32 v143, v128
	s_nop 0
	v_fma_f32 v147, -v128, v143, 1.0
	v_fmac_f32_e32 v143, v147, v143
	v_div_scale_f32 v147, vcc, 1.0, v163, 1.0
	v_mul_f32_e32 v161, v147, v143
	v_fma_f32 v164, -v128, v161, v147
	v_fmac_f32_e32 v161, v164, v143
	v_fma_f32 v128, -v128, v161, v147
	v_div_fmas_f32 v128, v128, v143, v161
	v_div_fixup_f32 v163, v128, v163, 1.0
	v_div_scale_f32 v128, s[46:47], v162, v162, 1.0
	v_rcp_f32_e32 v143, v128
	s_nop 0
	v_fma_f32 v147, -v128, v143, 1.0
	v_fmac_f32_e32 v143, v147, v143
	v_div_scale_f32 v147, vcc, 1.0, v162, 1.0
	v_mul_f32_e32 v161, v147, v143
	v_fma_f32 v164, -v128, v161, v147
	v_fmac_f32_e32 v161, v164, v143
	v_fma_f32 v128, -v128, v161, v147
	v_div_fmas_f32 v128, v128, v143, v161
	v_div_fixup_f32 v162, v128, v162, 1.0
	v_lshlrev_b32_e32 v128, 16, v129
	v_and_b32_e32 v129, 0xffff0000, v129
	v_pk_add_f32 v[126:127], v[126:127], v[128:129]
	v_pk_mul_f32 v[124:125], v[124:125], v[162:163]
	v_mul_f32_e32 v128, 0x3d372713, v126
	v_mul_f32_e32 v129, 0x3d372713, v127
	v_mul_f32_e32 v128, v126, v128
	v_mul_f32_e32 v129, v127, v129
	v_fma_f32 v128, v126, v128, v126
	v_fma_f32 v129, v127, v129, v127
	v_mul_f32_e32 v128, 0x3fcc422a, v128
	v_mul_f32_e32 v129, 0x3fcc422a, v129
	v_mul_f32_e32 v128, 0xbfb8aa3b, v128
	v_mul_f32_e32 v129, 0xbfb8aa3b, v129
	v_exp_f32_e32 v128, v128
	v_exp_f32_e32 v129, v129
	s_nop 0
	v_pk_add_f32 v[128:129], v[128:129], 1.0 op_sel_hi:[1,0]
	s_nop 0
	v_div_scale_f32 v143, s[46:47], v129, v129, 1.0
	v_rcp_f32_e32 v147, v143
	s_nop 0
	v_fma_f32 v161, -v143, v147, 1.0
	v_fmac_f32_e32 v147, v161, v147
	v_div_scale_f32 v161, vcc, 1.0, v129, 1.0
	v_mul_f32_e32 v162, v161, v147
	v_fma_f32 v163, -v143, v162, v161
	v_fmac_f32_e32 v162, v163, v147
	v_fma_f32 v143, -v143, v162, v161
	v_div_fmas_f32 v143, v143, v147, v162
	v_div_fixup_f32 v129, v143, v129, 1.0
	v_div_scale_f32 v143, s[46:47], v128, v128, 1.0
	v_rcp_f32_e32 v147, v143
	s_nop 0
	v_fma_f32 v161, -v143, v147, 1.0
	v_fmac_f32_e32 v147, v161, v147
	v_div_scale_f32 v161, vcc, 1.0, v128, 1.0
	v_mul_f32_e32 v162, v161, v147
	v_fma_f32 v163, -v143, v162, v161
	v_fmac_f32_e32 v162, v163, v147
	v_fma_f32 v143, -v143, v162, v161
	v_div_fmas_f32 v143, v143, v147, v162
	v_div_fixup_f32 v128, v143, v128, 1.0
	v_pk_mul_f32 v[126:127], v[126:127], v[128:129]
	v_lshlrev_b32_e32 v128, 16, v130
	v_and_b32_e32 v129, 0xffff0000, v130
	v_pk_add_f32 v[120:121], v[120:121], v[128:129]
	s_nop 0
	v_mul_f32_e32 v128, 0x3d372713, v120
	v_mul_f32_e32 v129, 0x3d372713, v121
	v_mul_f32_e32 v128, v120, v128
	v_mul_f32_e32 v129, v121, v129
	v_fma_f32 v128, v120, v128, v120
	v_fma_f32 v129, v121, v129, v121
	v_mul_f32_e32 v128, 0x3fcc422a, v128
	v_mul_f32_e32 v129, 0x3fcc422a, v129
	v_mul_f32_e32 v128, 0xbfb8aa3b, v128
	v_mul_f32_e32 v129, 0xbfb8aa3b, v129
	v_exp_f32_e32 v128, v128
	v_exp_f32_e32 v129, v129
	s_nop 0
	v_pk_add_f32 v[128:129], v[128:129], 1.0 op_sel_hi:[1,0]
	s_nop 0
	v_div_scale_f32 v130, s[46:47], v129, v129, 1.0
	v_rcp_f32_e32 v143, v130
	s_nop 0
	v_fma_f32 v147, -v130, v143, 1.0
	v_fmac_f32_e32 v143, v147, v143
	v_div_scale_f32 v147, vcc, 1.0, v129, 1.0
	v_mul_f32_e32 v161, v147, v143
	v_fma_f32 v162, -v130, v161, v147
	v_fmac_f32_e32 v161, v162, v143
	v_fma_f32 v130, -v130, v161, v147
; __device__ __forceinline__ float gelu_tanh(float x) { return x * sigmoidf_(1.5957691216057308f * (x + 0.044715f * x * x * x)); }
; __device__ __forceinline__ unsigned cvt_pk_bf16(float lo, float hi) { const f32x2c v = {lo, hi}; const bf16x2c b = __builtin_convertvector(v, bf16x2c); return __builtin_bit_cast(unsigned, b); }
;     __device__ __forceinline__ void operator()(const f32x4 (&acc)[2][2][4][2], const Unit& u, int wr, int wc, int fr, int fq) const {
;     ...
;             for (int m = 0; m < 4; ++m) { const int row = row0 + ai * HALF + m * 16; const int g = row / S5R, rl = row % S5R;
; #pragma unroll
;                 for (int bj = 0; bj < 2; ++bj) { const int col = col0 + bj * HALF;
;                     const u32x4 yi = *(const u32x4*)(YI + (size_t)row * 512 + col);
;                     const unsigned yw[4] = {yi.x, yi.y, yi.z, yi.w};
;                     const f32x4 v0 = acc[ai][bj][m][0], v1 = acc[ai][bj][m][1];
;                     float o[8];
; #pragma unroll
;                     for (int q = 0; q < 4; ++q) { const float al = (q < 2) ? v0[2 * q] : v1[2 * q - 4], ah = (q < 2) ? v0[2 * q + 1] : v1[2 * q - 3];
;                         o[2 * q] = gelu_tanh(al + __builtin_bit_cast(float, yw[q] << 16)); o[2 * q + 1] = gelu_tanh(ah + __builtin_bit_cast(float, yw[q] & 0xffff0000u)); }
;                     u32x4 w; w.x = cvt_pk_bf16(o[0], o[1]); w.y = cvt_pk_bf16(o[2], o[3]); w.z = cvt_pk_bf16(o[4], o[5]); w.w = cvt_pk_bf16(o[6], o[7]);
;                     const size_t tok = (size_t)rl * S5L + (col >> 4);
;                     *(u32x4*)(Z + tok * 512 + g * 16 + (col & 15)) = w; } }
	v_div_fmas_f32 v130, v130, v143, v161
	v_div_fixup_f32 v129, v130, v129, 1.0
	v_div_scale_f32 v130, s[46:47], v128, v128, 1.0
	v_rcp_f32_e32 v143, v130
	s_nop 0
	v_fma_f32 v147, -v130, v143, 1.0
	v_fmac_f32_e32 v143, v147, v143
	v_div_scale_f32 v147, vcc, 1.0, v128, 1.0
	v_mul_f32_e32 v161, v147, v143
	v_fma_f32 v162, -v130, v161, v147
	v_fmac_f32_e32 v161, v162, v143
	v_fma_f32 v130, -v130, v161, v147
	v_div_fmas_f32 v130, v130, v143, v161
	v_div_fixup_f32 v128, v130, v128, 1.0
	v_pk_mul_f32 v[128:129], v[120:121], v[128:129]
	v_lshlrev_b32_e32 v120, 16, v131
	v_and_b32_e32 v121, 0xffff0000, v131
	v_pk_add_f32 v[120:121], v[122:123], v[120:121]
	s_nop 0
	v_mul_f32_e32 v122, 0x3d372713, v120
	v_mul_f32_e32 v123, 0x3d372713, v121
	v_mul_f32_e32 v122, v120, v122
	v_mul_f32_e32 v123, v121, v123
	v_fma_f32 v122, v120, v122, v120
	v_fma_f32 v123, v121, v123, v121
	v_mul_f32_e32 v122, 0x3fcc422a, v122
	v_mul_f32_e32 v123, 0x3fcc422a, v123
	v_mul_f32_e32 v122, 0xbfb8aa3b, v122
	v_mul_f32_e32 v123, 0xbfb8aa3b, v123
	v_exp_f32_e32 v122, v122
	v_exp_f32_e32 v123, v123
	s_nop 0
	v_pk_add_f32 v[122:123], v[122:123], 1.0 op_sel_hi:[1,0]
	s_nop 0
	v_div_scale_f32 v130, s[46:47], v123, v123, 1.0
	v_rcp_f32_e32 v131, v130
	s_nop 0
	v_fma_f32 v143, -v130, v131, 1.0
	v_fmac_f32_e32 v131, v143, v131
	v_div_scale_f32 v143, vcc, 1.0, v123, 1.0
	v_mul_f32_e32 v147, v143, v131
	v_fma_f32 v161, -v130, v147, v143
	v_fmac_f32_e32 v147, v161, v131
	v_fma_f32 v130, -v130, v147, v143
	v_div_fmas_f32 v130, v130, v131, v147
	v_div_fixup_f32 v123, v130, v123, 1.0
	v_div_scale_f32 v130, s[46:47], v122, v122, 1.0
	v_rcp_f32_e32 v131, v130
	s_nop 0
	v_fma_f32 v143, -v130, v131, 1.0
	v_fmac_f32_e32 v131, v143, v131
	v_div_scale_f32 v143, vcc, 1.0, v122, 1.0
	v_mul_f32_e32 v147, v143, v131
	v_fma_f32 v161, -v130, v147, v143
	v_fmac_f32_e32 v147, v161, v131
	v_fma_f32 v130, -v130, v147, v143
	v_div_fmas_f32 v130, v130, v131, v147
	v_div_fixup_f32 v122, v130, v122, 1.0
	v_pk_mul_f32 v[130:131], v[120:121], v[122:123]
	v_cvt_pk_bf16_f32 v120, v124, v125
	v_ashrrev_i32_e32 v124, 4, v146
	v_ashrrev_i32_e32 v125, 31, v124
	v_cvt_pk_bf16_f32 v121, v126, v127
	v_lshl_add_u64 v[126:127], s[36:37], 0, v[150:151]
	v_lshlrev_b64 v[124:125], 10, v[124:125]
	v_cvt_pk_bf16_f32 v122, v128, v129
	v_cvt_pk_bf16_f32 v123, v130, v131
	v_lshl_add_u64 v[130:131], v[126:127], 0, v[124:125]
	v_lshlrev_b64 v[128:129], 1, v[148:149]
	v_lshl_add_u64 v[130:131], v[130:131], 0, v[128:129]
	v_lshl_add_u64 v[130:131], v[130:131], 0, v[140:141]
	global_store_dwordx4 v[130:131], v[120:123], off
	s_nop 1
	v_or_b32_e32 v143, 0x80, v146
	s_waitcnt vmcnt(9)
	v_mov_b32_e32 v120, v174
	v_mov_b32_e32 v121, v175
	v_mov_b32_e32 v122, v176
	v_mov_b32_e32 v123, v177
	s_mov_b64 s[98:99], 0x24000
	v_lshl_add_u64 v[168:169], v[166:167], 0, s[98:99]
	global_load_dwordx4 v[174:177], v[168:169], off
	v_lshlrev_b32_e32 v130, 16, v120
	v_and_b32_e32 v131, 0xffff0000, v120
	v_pk_add_f32 v[116:117], v[116:117], v[130:131]
	s_nop 0
	v_mul_f32_e32 v120, 0x3d372713, v116
	v_mul_f32_e32 v120, v116, v120
	v_fma_f32 v120, v116, v120, v116
	v_mul_f32_e32 v120, 0x3fcc422a, v120
	v_mul_f32_e32 v120, 0xbfb8aa3b, v120
	v_exp_f32_e32 v130, v120
	v_mul_f32_e32 v120, 0x3d372713, v117
	v_mul_f32_e32 v120, v117, v120
	v_fma_f32 v120, v117, v120, v117
	v_mul_f32_e32 v120, 0x3fcc422a, v120
	v_mul_f32_e32 v120, 0xbfb8aa3b, v120
	v_exp_f32_e32 v131, v120
	s_nop 0
	v_pk_add_f32 v[130:131], v[130:131], 1.0 op_sel_hi:[1,0]
	s_nop 0
	v_div_scale_f32 v120, s[46:47], v131, v131, 1.0
	v_rcp_f32_e32 v146, v120
	s_nop 0
	v_fma_f32 v147, -v120, v146, 1.0
	v_fmac_f32_e32 v146, v147, v146
	v_div_scale_f32 v147, vcc, 1.0, v131, 1.0
	v_mul_f32_e32 v148, v147, v146
	v_fma_f32 v149, -v120, v148, v147
	v_fmac_f32_e32 v148, v149, v146
	v_fma_f32 v120, -v120, v148, v147
	v_div_fmas_f32 v120, v120, v146, v148
	v_div_fixup_f32 v131, v120, v131, 1.0
	v_div_scale_f32 v120, s[46:47], v130, v130, 1.0
	v_rcp_f32_e32 v146, v120
	s_nop 0
	v_fma_f32 v147, -v120, v146, 1.0
	v_fmac_f32_e32 v146, v147, v146
	v_div_scale_f32 v147, vcc, 1.0, v130, 1.0
	v_mul_f32_e32 v148, v147, v146
	v_fma_f32 v149, -v120, v148, v147
	v_fmac_f32_e32 v148, v149, v146
	v_fma_f32 v120, -v120, v148, v147
	v_div_fmas_f32 v120, v120, v146, v148
	v_div_fixup_f32 v130, v120, v130, 1.0
	v_lshlrev_b32_e32 v120, 16, v121
	v_and_b32_e32 v121, 0xffff0000, v121
	v_pk_add_f32 v[118:119], v[118:119], v[120:121]
	v_pk_mul_f32 v[116:117], v[116:117], v[130:131]
	v_mul_f32_e32 v120, 0x3d372713, v118
	v_mul_f32_e32 v121, 0x3d372713, v119
	v_mul_f32_e32 v120, v118, v120
	v_mul_f32_e32 v121, v119, v121
	v_fma_f32 v120, v118, v120, v118
	v_fma_f32 v121, v119, v121, v119
	v_mul_f32_e32 v120, 0x3fcc422a, v120
	v_mul_f32_e32 v121, 0x3fcc422a, v121
	v_mul_f32_e32 v120, 0xbfb8aa3b, v120
	v_mul_f32_e32 v121, 0xbfb8aa3b, v121
	v_exp_f32_e32 v120, v120
	v_exp_f32_e32 v121, v121
	s_nop 0
	v_pk_add_f32 v[120:121], v[120:121], 1.0 op_sel_hi:[1,0]
	s_nop 0
	v_div_scale_f32 v130, s[46:47], v121, v121, 1.0
	v_rcp_f32_e32 v131, v130
	s_nop 0
	v_fma_f32 v146, -v130, v131, 1.0
	v_fmac_f32_e32 v131, v146, v131
	v_div_scale_f32 v146, vcc, 1.0, v121, 1.0
	v_mul_f32_e32 v147, v146, v131
	v_fma_f32 v148, -v130, v147, v146
	v_fmac_f32_e32 v147, v148, v131
	v_fma_f32 v130, -v130, v147, v146
	v_div_fmas_f32 v130, v130, v131, v147
	v_div_fixup_f32 v121, v130, v121, 1.0
	v_div_scale_f32 v130, s[46:47], v120, v120, 1.0
	v_rcp_f32_e32 v131, v130
	s_nop 0
	v_fma_f32 v146, -v130, v131, 1.0
	v_fmac_f32_e32 v131, v146, v131
	v_div_scale_f32 v146, vcc, 1.0, v120, 1.0
	v_mul_f32_e32 v147, v146, v131
	v_fma_f32 v148, -v130, v147, v146
; __device__ __forceinline__ float gelu_tanh(float x) { return x * sigmoidf_(1.5957691216057308f * (x + 0.044715f * x * x * x)); }
; __device__ __forceinline__ unsigned cvt_pk_bf16(float lo, float hi) { const f32x2c v = {lo, hi}; const bf16x2c b = __builtin_convertvector(v, bf16x2c); return __builtin_bit_cast(unsigned, b); }
;     __device__ __forceinline__ void operator()(const f32x4 (&acc)[2][2][4][2], const Unit& u, int wr, int wc, int fr, int fq) const {
;     ...
;             for (int m = 0; m < 4; ++m) { const int row = row0 + ai * HALF + m * 16; const int g = row / S5R, rl = row % S5R;
; #pragma unroll
;                 for (int bj = 0; bj < 2; ++bj) { const int col = col0 + bj * HALF;
;                     const u32x4 yi = *(const u32x4*)(YI + (size_t)row * 512 + col);
;                     const unsigned yw[4] = {yi.x, yi.y, yi.z, yi.w};
;                     const f32x4 v0 = acc[ai][bj][m][0], v1 = acc[ai][bj][m][1];
;                     float o[8];
; #pragma unroll
;                     for (int q = 0; q < 4; ++q) { const float al = (q < 2) ? v0[2 * q] : v1[2 * q - 4], ah = (q < 2) ? v0[2 * q + 1] : v1[2 * q - 3];
;                         o[2 * q] = gelu_tanh(al + __builtin_bit_cast(float, yw[q] << 16)); o[2 * q + 1] = gelu_tanh(ah + __builtin_bit_cast(float, yw[q] & 0xffff0000u)); }
;                     u32x4 w; w.x = cvt_pk_bf16(o[0], o[1]); w.y = cvt_pk_bf16(o[2], o[3]); w.z = cvt_pk_bf16(o[4], o[5]); w.w = cvt_pk_bf16(o[6], o[7]);
;                     const size_t tok = (size_t)rl * S5L + (col >> 4);
;                     *(u32x4*)(Z + tok * 512 + g * 16 + (col & 15)) = w; } }
	v_fmac_f32_e32 v147, v148, v131
	v_fma_f32 v130, -v130, v147, v146
	v_div_fmas_f32 v130, v130, v131, v147
	v_div_fixup_f32 v120, v130, v120, 1.0
	v_pk_mul_f32 v[118:119], v[118:119], v[120:121]
	v_lshlrev_b32_e32 v120, 16, v122
	v_and_b32_e32 v121, 0xffff0000, v122
	v_pk_add_f32 v[112:113], v[112:113], v[120:121]
	s_nop 0
	v_mul_f32_e32 v120, 0x3d372713, v112
	v_mul_f32_e32 v121, 0x3d372713, v113
	v_mul_f32_e32 v120, v112, v120
	v_mul_f32_e32 v121, v113, v121
	v_fma_f32 v120, v112, v120, v112
	v_fma_f32 v121, v113, v121, v113
	v_mul_f32_e32 v120, 0x3fcc422a, v120
	v_mul_f32_e32 v121, 0x3fcc422a, v121
	v_mul_f32_e32 v120, 0xbfb8aa3b, v120
	v_mul_f32_e32 v121, 0xbfb8aa3b, v121
	v_exp_f32_e32 v120, v120
	v_exp_f32_e32 v121, v121
	s_nop 0
	v_pk_add_f32 v[120:121], v[120:121], 1.0 op_sel_hi:[1,0]
	s_nop 0
	v_div_scale_f32 v122, s[46:47], v121, v121, 1.0
	v_rcp_f32_e32 v130, v122
	s_nop 0
	v_fma_f32 v131, -v122, v130, 1.0
	v_fmac_f32_e32 v130, v131, v130
	v_div_scale_f32 v131, vcc, 1.0, v121, 1.0
	v_mul_f32_e32 v146, v131, v130
	v_fma_f32 v147, -v122, v146, v131
	v_fmac_f32_e32 v146, v147, v130
	v_fma_f32 v122, -v122, v146, v131
	v_div_fmas_f32 v122, v122, v130, v146
	v_div_fixup_f32 v121, v122, v121, 1.0
	v_div_scale_f32 v122, s[46:47], v120, v120, 1.0
	v_rcp_f32_e32 v130, v122
	s_nop 0
	v_fma_f32 v131, -v122, v130, 1.0
	v_fmac_f32_e32 v130, v131, v130
	v_div_scale_f32 v131, vcc, 1.0, v120, 1.0
	v_mul_f32_e32 v146, v131, v130
	v_fma_f32 v147, -v122, v146, v131
	v_fmac_f32_e32 v146, v147, v130
	v_fma_f32 v122, -v122, v146, v131
	v_div_fmas_f32 v122, v122, v130, v146
	v_div_fixup_f32 v120, v122, v120, 1.0
	v_pk_mul_f32 v[120:121], v[112:113], v[120:121]
	v_lshlrev_b32_e32 v112, 16, v123
	v_and_b32_e32 v113, 0xffff0000, v123
	v_pk_add_f32 v[112:113], v[114:115], v[112:113]
	s_nop 0
	v_mul_f32_e32 v114, 0x3d372713, v112
	v_mul_f32_e32 v115, 0x3d372713, v113
	v_mul_f32_e32 v114, v112, v114
	v_mul_f32_e32 v115, v113, v115
	v_fma_f32 v114, v112, v114, v112
	v_fma_f32 v115, v113, v115, v113
	v_mul_f32_e32 v114, 0x3fcc422a, v114
	v_mul_f32_e32 v115, 0x3fcc422a, v115
	v_mul_f32_e32 v114, 0xbfb8aa3b, v114
	v_mul_f32_e32 v115, 0xbfb8aa3b, v115
	v_exp_f32_e32 v114, v114
	v_exp_f32_e32 v115, v115
	s_nop 0
	v_pk_add_f32 v[114:115], v[114:115], 1.0 op_sel_hi:[1,0]
	s_nop 0
	v_div_scale_f32 v122, s[46:47], v115, v115, 1.0
	v_rcp_f32_e32 v123, v122
	s_nop 0
	v_fma_f32 v130, -v122, v123, 1.0
	v_fmac_f32_e32 v123, v130, v123
	v_div_scale_f32 v130, vcc, 1.0, v115, 1.0
	v_mul_f32_e32 v131, v130, v123
	v_fma_f32 v146, -v122, v131, v130
	v_fmac_f32_e32 v131, v146, v123
	v_fma_f32 v122, -v122, v131, v130
	v_div_fmas_f32 v122, v122, v123, v131
	v_div_fixup_f32 v115, v122, v115, 1.0
	v_div_scale_f32 v122, s[46:47], v114, v114, 1.0
	v_rcp_f32_e32 v123, v122
	s_nop 0
	v_fma_f32 v130, -v122, v123, 1.0
	v_fmac_f32_e32 v123, v130, v123
	v_div_scale_f32 v130, vcc, 1.0, v114, 1.0
	v_mul_f32_e32 v131, v130, v123
	v_fma_f32 v146, -v122, v131, v130
	v_fmac_f32_e32 v131, v146, v123
	v_fma_f32 v122, -v122, v131, v130
	v_div_fmas_f32 v122, v122, v123, v131
	v_div_fixup_f32 v114, v122, v114, 1.0
	v_pk_mul_f32 v[122:123], v[112:113], v[114:115]
	v_cvt_pk_bf16_f32 v112, v116, v117
	v_ashrrev_i32_e32 v116, 4, v143
	v_ashrrev_i32_e32 v117, 31, v116
	v_lshlrev_b64 v[116:117], 10, v[116:117]
	v_cvt_pk_bf16_f32 v113, v118, v119
	v_lshl_add_u64 v[118:119], v[126:127], 0, v[116:117]
	v_lshl_add_u64 v[118:119], v[118:119], 0, v[128:129]
	v_cvt_pk_bf16_f32 v114, v120, v121
	v_cvt_pk_bf16_f32 v115, v122, v123
	v_lshl_add_u64 v[118:119], v[118:119], 0, v[140:141]
	global_store_dwordx4 v[118:119], v[112:115], off
	s_nop 1
	v_or_b32_e32 v112, 16, v142
	v_add_u32_e32 v113, v112, v160
	v_ashrrev_i32_e32 v118, 11, v113
	v_mul_i32_i24_e32 v113, 0x800, v118
	v_sub_u32_e32 v114, v112, v113
	v_ashrrev_i32_e32 v113, 31, v112
	v_lshlrev_b64 v[112:113], 10, v[112:113]
	v_lshl_add_u64 v[112:113], s[30:31], 0, v[112:113]
	v_ashrrev_i32_e32 v115, 31, v114
	v_lshl_add_u64 v[122:123], v[112:113], 0, v[144:145]
	v_lshlrev_b64 v[120:121], 15, v[114:115]
	s_nop 1
	v_lshlrev_b32_e32 v118, 4, v118
	v_ashrrev_i32_e32 v119, 31, v118
	s_waitcnt vmcnt(10)
	v_mov_b32_e32 v112, v178
	v_mov_b32_e32 v113, v179
	v_mov_b32_e32 v114, v180
	v_mov_b32_e32 v115, v181
	global_load_dwordx4 v[178:181], v[168:169], off offset:256
	v_lshlrev_b32_e32 v126, 16, v112
	v_and_b32_e32 v127, 0xffff0000, v112
	v_pk_add_f32 v[108:109], v[108:109], v[126:127]
	s_nop 0
	v_mul_f32_e32 v112, 0x3d372713, v108
	v_mul_f32_e32 v112, v108, v112
	v_fma_f32 v112, v108, v112, v108
	v_mul_f32_e32 v112, 0x3fcc422a, v112
	v_mul_f32_e32 v112, 0xbfb8aa3b, v112
	v_exp_f32_e32 v126, v112
	v_mul_f32_e32 v112, 0x3d372713, v109
	v_mul_f32_e32 v112, v109, v112
	v_fma_f32 v112, v109, v112, v109
	v_mul_f32_e32 v112, 0x3fcc422a, v112
	v_mul_f32_e32 v112, 0xbfb8aa3b, v112
	v_exp_f32_e32 v127, v112
	s_nop 0
	v_pk_add_f32 v[126:127], v[126:127], 1.0 op_sel_hi:[1,0]
	s_nop 0
	v_div_scale_f32 v112, s[46:47], v127, v127, 1.0
	v_rcp_f32_e32 v128, v112
	s_nop 0
	v_fma_f32 v129, -v112, v128, 1.0
	v_fmac_f32_e32 v128, v129, v128
	v_div_scale_f32 v129, vcc, 1.0, v127, 1.0
	v_mul_f32_e32 v130, v129, v128
	v_fma_f32 v131, -v112, v130, v129
	v_fmac_f32_e32 v130, v131, v128
	v_fma_f32 v112, -v112, v130, v129
	v_div_fmas_f32 v112, v112, v128, v130
	v_div_fixup_f32 v127, v112, v127, 1.0
	v_div_scale_f32 v112, s[46:47], v126, v126, 1.0
	v_rcp_f32_e32 v128, v112
	s_nop 0
	v_fma_f32 v129, -v112, v128, 1.0
	v_fmac_f32_e32 v128, v129, v128
	v_div_scale_f32 v129, vcc, 1.0, v126, 1.0
	v_mul_f32_e32 v130, v129, v128
	v_fma_f32 v131, -v112, v130, v129
	v_fmac_f32_e32 v130, v131, v128
; __device__ __forceinline__ float gelu_tanh(float x) { return x * sigmoidf_(1.5957691216057308f * (x + 0.044715f * x * x * x)); }
; __device__ __forceinline__ unsigned cvt_pk_bf16(float lo, float hi) { const f32x2c v = {lo, hi}; const bf16x2c b = __builtin_convertvector(v, bf16x2c); return __builtin_bit_cast(unsigned, b); }
;     __device__ __forceinline__ void operator()(const f32x4 (&acc)[2][2][4][2], const Unit& u, int wr, int wc, int fr, int fq) const {
;     ...
;             for (int m = 0; m < 4; ++m) { const int row = row0 + ai * HALF + m * 16; const int g = row / S5R, rl = row % S5R;
; #pragma unroll
;                 for (int bj = 0; bj < 2; ++bj) { const int col = col0 + bj * HALF;
;                     const u32x4 yi = *(const u32x4*)(YI + (size_t)row * 512 + col);
;                     const unsigned yw[4] = {yi.x, yi.y, yi.z, yi.w};
;                     const f32x4 v0 = acc[ai][bj][m][0], v1 = acc[ai][bj][m][1];
;                     float o[8];
; #pragma unroll
;                     for (int q = 0; q < 4; ++q) { const float al = (q < 2) ? v0[2 * q] : v1[2 * q - 4], ah = (q < 2) ? v0[2 * q + 1] : v1[2 * q - 3];
;                         o[2 * q] = gelu_tanh(al + __builtin_bit_cast(float, yw[q] << 16)); o[2 * q + 1] = gelu_tanh(ah + __builtin_bit_cast(float, yw[q] & 0xffff0000u)); }
;                     u32x4 w; w.x = cvt_pk_bf16(o[0], o[1]); w.y = cvt_pk_bf16(o[2], o[3]); w.z = cvt_pk_bf16(o[4], o[5]); w.w = cvt_pk_bf16(o[6], o[7]);
;                     const size_t tok = (size_t)rl * S5L + (col >> 4);
;                     *(u32x4*)(Z + tok * 512 + g * 16 + (col & 15)) = w; } }
	v_fma_f32 v112, -v112, v130, v129
	v_div_fmas_f32 v112, v112, v128, v130
	v_div_fixup_f32 v126, v112, v126, 1.0
	v_lshlrev_b32_e32 v112, 16, v113
	v_and_b32_e32 v113, 0xffff0000, v113
	v_pk_add_f32 v[110:111], v[110:111], v[112:113]
	v_pk_mul_f32 v[108:109], v[108:109], v[126:127]
	v_mul_f32_e32 v112, 0x3d372713, v110
	v_mul_f32_e32 v113, 0x3d372713, v111
	v_mul_f32_e32 v112, v110, v112
	v_mul_f32_e32 v113, v111, v113
	v_fma_f32 v112, v110, v112, v110
	v_fma_f32 v113, v111, v113, v111
	v_mul_f32_e32 v112, 0x3fcc422a, v112
	v_mul_f32_e32 v113, 0x3fcc422a, v113
	v_mul_f32_e32 v112, 0xbfb8aa3b, v112
	v_mul_f32_e32 v113, 0xbfb8aa3b, v113
	v_exp_f32_e32 v112, v112
	v_exp_f32_e32 v113, v113
	s_nop 0
	v_pk_add_f32 v[112:113], v[112:113], 1.0 op_sel_hi:[1,0]
	s_nop 0
	v_div_scale_f32 v126, s[46:47], v113, v113, 1.0
	v_rcp_f32_e32 v127, v126
	s_nop 0
	v_fma_f32 v128, -v126, v127, 1.0
	v_fmac_f32_e32 v127, v128, v127
	v_div_scale_f32 v128, vcc, 1.0, v113, 1.0
	v_mul_f32_e32 v129, v128, v127
	v_fma_f32 v130, -v126, v129, v128
	v_fmac_f32_e32 v129, v130, v127
	v_fma_f32 v126, -v126, v129, v128
	v_div_fmas_f32 v126, v126, v127, v129
	v_div_fixup_f32 v113, v126, v113, 1.0
	v_div_scale_f32 v126, s[46:47], v112, v112, 1.0
	v_rcp_f32_e32 v127, v126
	s_nop 0
	v_fma_f32 v128, -v126, v127, 1.0
	v_fmac_f32_e32 v127, v128, v127
	v_div_scale_f32 v128, vcc, 1.0, v112, 1.0
	v_mul_f32_e32 v129, v128, v127
	v_fma_f32 v130, -v126, v129, v128
	v_fmac_f32_e32 v129, v130, v127
	v_fma_f32 v126, -v126, v129, v128
	v_div_fmas_f32 v126, v126, v127, v129
	v_div_fixup_f32 v112, v126, v112, 1.0
	v_pk_mul_f32 v[110:111], v[110:111], v[112:113]
	v_lshlrev_b32_e32 v112, 16, v114
	v_and_b32_e32 v113, 0xffff0000, v114
	v_pk_add_f32 v[104:105], v[104:105], v[112:113]
	s_nop 0
	v_mul_f32_e32 v112, 0x3d372713, v104
	v_mul_f32_e32 v113, 0x3d372713, v105
	v_mul_f32_e32 v112, v104, v112
	v_mul_f32_e32 v113, v105, v113
	v_fma_f32 v112, v104, v112, v104
	v_fma_f32 v113, v105, v113, v105
	v_mul_f32_e32 v112, 0x3fcc422a, v112
	v_mul_f32_e32 v113, 0x3fcc422a, v113
	v_mul_f32_e32 v112, 0xbfb8aa3b, v112
	v_mul_f32_e32 v113, 0xbfb8aa3b, v113
	v_exp_f32_e32 v112, v112
	v_exp_f32_e32 v113, v113
	s_nop 0
	v_pk_add_f32 v[112:113], v[112:113], 1.0 op_sel_hi:[1,0]
	s_nop 0
	v_div_scale_f32 v114, s[46:47], v113, v113, 1.0
	v_rcp_f32_e32 v126, v114
	s_nop 0
	v_fma_f32 v127, -v114, v126, 1.0
	v_fmac_f32_e32 v126, v127, v126
	v_div_scale_f32 v127, vcc, 1.0, v113, 1.0
	v_mul_f32_e32 v128, v127, v126
	v_fma_f32 v129, -v114, v128, v127
	v_fmac_f32_e32 v128, v129, v126
	v_fma_f32 v114, -v114, v128, v127
	v_div_fmas_f32 v114, v114, v126, v128
	v_div_fixup_f32 v113, v114, v113, 1.0
	v_div_scale_f32 v114, s[46:47], v112, v112, 1.0
	v_rcp_f32_e32 v126, v114
	s_nop 0
	v_fma_f32 v127, -v114, v126, 1.0
	v_fmac_f32_e32 v126, v127, v126
	v_div_scale_f32 v127, vcc, 1.0, v112, 1.0
	v_mul_f32_e32 v128, v127, v126
	v_fma_f32 v129, -v114, v128, v127
	v_fmac_f32_e32 v128, v129, v126
	v_fma_f32 v114, -v114, v128, v127
	v_div_fmas_f32 v114, v114, v126, v128
	v_div_fixup_f32 v112, v114, v112, 1.0
	v_pk_mul_f32 v[112:113], v[104:105], v[112:113]
	v_lshlrev_b32_e32 v104, 16, v115
	v_and_b32_e32 v105, 0xffff0000, v115
	v_pk_add_f32 v[104:105], v[106:107], v[104:105]
	s_nop 0
	v_mul_f32_e32 v106, 0x3d372713, v104
	v_mul_f32_e32 v107, 0x3d372713, v105
	v_mul_f32_e32 v106, v104, v106
	v_mul_f32_e32 v107, v105, v107
	v_fma_f32 v106, v104, v106, v104
	v_fma_f32 v107, v105, v107, v105
	v_mul_f32_e32 v106, 0x3fcc422a, v106
	v_mul_f32_e32 v107, 0x3fcc422a, v107
	v_mul_f32_e32 v106, 0xbfb8aa3b, v106
	v_mul_f32_e32 v107, 0xbfb8aa3b, v107
	v_exp_f32_e32 v106, v106
	v_exp_f32_e32 v107, v107
	s_nop 0
	v_pk_add_f32 v[106:107], v[106:107], 1.0 op_sel_hi:[1,0]
	s_nop 0
	v_div_scale_f32 v114, s[46:47], v107, v107, 1.0
	v_rcp_f32_e32 v115, v114
	s_nop 0
	v_fma_f32 v126, -v114, v115, 1.0
	v_fmac_f32_e32 v115, v126, v115
	v_div_scale_f32 v126, vcc, 1.0, v107, 1.0
	v_mul_f32_e32 v127, v126, v115
	v_fma_f32 v128, -v114, v127, v126
	v_fmac_f32_e32 v127, v128, v115
	v_fma_f32 v114, -v114, v127, v126
	v_div_fmas_f32 v114, v114, v115, v127
	v_div_fixup_f32 v107, v114, v107, 1.0
	v_div_scale_f32 v114, s[46:47], v106, v106, 1.0
	v_rcp_f32_e32 v115, v114
	s_nop 0
	v_fma_f32 v126, -v114, v115, 1.0
	v_fmac_f32_e32 v115, v126, v115
	v_div_scale_f32 v126, vcc, 1.0, v106, 1.0
	v_mul_f32_e32 v127, v126, v115
	v_fma_f32 v128, -v114, v127, v126
	v_fmac_f32_e32 v127, v128, v115
	v_fma_f32 v114, -v114, v127, v126
	v_div_fmas_f32 v114, v114, v115, v127
	v_div_fixup_f32 v106, v114, v106, 1.0
	v_pk_mul_f32 v[114:115], v[104:105], v[106:107]
	v_cvt_pk_bf16_f32 v104, v108, v109
	v_lshl_add_u64 v[108:109], s[36:37], 0, v[120:121]
	v_cvt_pk_bf16_f32 v105, v110, v111
	v_cvt_pk_bf16_f32 v106, v112, v113
	v_lshl_add_u64 v[112:113], v[108:109], 0, v[124:125]
	v_lshlrev_b64 v[110:111], 1, v[118:119]
	v_lshl_add_u64 v[112:113], v[112:113], 0, v[110:111]
	v_cvt_pk_bf16_f32 v107, v114, v115
	v_lshl_add_u64 v[112:113], v[112:113], 0, v[140:141]
	global_store_dwordx4 v[112:113], v[104:107], off
	s_nop 1
	s_waitcnt vmcnt(11)
; __device__ __forceinline__ float gelu_tanh(float x) { return x * sigmoidf_(1.5957691216057308f * (x + 0.044715f * x * x * x)); }
; __device__ __forceinline__ unsigned cvt_pk_bf16(float lo, float hi) { const f32x2c v = {lo, hi}; const bf16x2c b = __builtin_convertvector(v, bf16x2c); return __builtin_bit_cast(unsigned, b); }
;     __device__ __forceinline__ void operator()(const f32x4 (&acc)[2][2][4][2], const Unit& u, int wr, int wc, int fr, int fq) const {
;     ...
;             for (int m = 0; m < 4; ++m) { const int row = row0 + ai * HALF + m * 16; const int g = row / S5R, rl = row % S5R;
; #pragma unroll
;                 for (int bj = 0; bj < 2; ++bj) { const int col = col0 + bj * HALF;
;                     const u32x4 yi = *(const u32x4*)(YI + (size_t)row * 512 + col);
;                     const unsigned yw[4] = {yi.x, yi.y, yi.z, yi.w};
;                     const f32x4 v0 = acc[ai][bj][m][0], v1 = acc[ai][bj][m][1];
;                     float o[8];
; #pragma unroll
;                     for (int q = 0; q < 4; ++q) { const float al = (q < 2) ? v0[2 * q] : v1[2 * q - 4], ah = (q < 2) ? v0[2 * q + 1] : v1[2 * q - 3];
;                         o[2 * q] = gelu_tanh(al + __builtin_bit_cast(float, yw[q] << 16)); o[2 * q + 1] = gelu_tanh(ah + __builtin_bit_cast(float, yw[q] & 0xffff0000u)); }
;                     u32x4 w; w.x = cvt_pk_bf16(o[0], o[1]); w.y = cvt_pk_bf16(o[2], o[3]); w.z = cvt_pk_bf16(o[4], o[5]); w.w = cvt_pk_bf16(o[6], o[7]);
;                     const size_t tok = (size_t)rl * S5L + (col >> 4);
;                     *(u32x4*)(Z + tok * 512 + g * 16 + (col & 15)) = w; } }
	v_mov_b32_e32 v104, v182
	v_mov_b32_e32 v105, v183
	v_mov_b32_e32 v106, v184
	v_mov_b32_e32 v107, v185
	s_mov_b64 s[98:99], 0x28000
	v_lshl_add_u64 v[168:169], v[166:167], 0, s[98:99]
	global_load_dwordx4 v[182:185], v[168:169], off
	v_lshlrev_b32_e32 v112, 16, v104
	v_and_b32_e32 v113, 0xffff0000, v104
	v_pk_add_f32 v[100:101], v[100:101], v[112:113]
	s_nop 0
	v_mul_f32_e32 v104, 0x3d372713, v100
	v_mul_f32_e32 v104, v100, v104
	v_fma_f32 v104, v100, v104, v100
	v_mul_f32_e32 v104, 0x3fcc422a, v104
	v_mul_f32_e32 v104, 0xbfb8aa3b, v104
	v_exp_f32_e32 v112, v104
	v_mul_f32_e32 v104, 0x3d372713, v101
	v_mul_f32_e32 v104, v101, v104
	v_fma_f32 v104, v101, v104, v101
	v_mul_f32_e32 v104, 0x3fcc422a, v104
	v_mul_f32_e32 v104, 0xbfb8aa3b, v104
	v_exp_f32_e32 v113, v104
	s_nop 0
	v_pk_add_f32 v[112:113], v[112:113], 1.0 op_sel_hi:[1,0]
	s_nop 0
	v_div_scale_f32 v104, s[46:47], v113, v113, 1.0
	v_rcp_f32_e32 v114, v104
	s_nop 0
	v_fma_f32 v115, -v104, v114, 1.0
	v_fmac_f32_e32 v114, v115, v114
	v_div_scale_f32 v115, vcc, 1.0, v113, 1.0
	v_mul_f32_e32 v118, v115, v114
	v_fma_f32 v119, -v104, v118, v115
	v_fmac_f32_e32 v118, v119, v114
	v_fma_f32 v104, -v104, v118, v115
	v_div_fmas_f32 v104, v104, v114, v118
	v_div_fixup_f32 v113, v104, v113, 1.0
	v_div_scale_f32 v104, s[46:47], v112, v112, 1.0
	v_rcp_f32_e32 v114, v104
	s_nop 0
	v_fma_f32 v115, -v104, v114, 1.0
	v_fmac_f32_e32 v114, v115, v114
	v_div_scale_f32 v115, vcc, 1.0, v112, 1.0
	v_mul_f32_e32 v118, v115, v114
	v_fma_f32 v119, -v104, v118, v115
	v_fmac_f32_e32 v118, v119, v114
	v_fma_f32 v104, -v104, v118, v115
	v_div_fmas_f32 v104, v104, v114, v118
	v_div_fixup_f32 v112, v104, v112, 1.0
	v_lshlrev_b32_e32 v104, 16, v105
	v_and_b32_e32 v105, 0xffff0000, v105
	v_pk_add_f32 v[102:103], v[102:103], v[104:105]
	v_pk_mul_f32 v[100:101], v[100:101], v[112:113]
	v_mul_f32_e32 v104, 0x3d372713, v102
	v_mul_f32_e32 v105, 0x3d372713, v103
	v_mul_f32_e32 v104, v102, v104
	v_mul_f32_e32 v105, v103, v105
	v_fma_f32 v104, v102, v104, v102
	v_fma_f32 v105, v103, v105, v103
	v_mul_f32_e32 v104, 0x3fcc422a, v104
	v_mul_f32_e32 v105, 0x3fcc422a, v105
	v_mul_f32_e32 v104, 0xbfb8aa3b, v104
	v_mul_f32_e32 v105, 0xbfb8aa3b, v105
	v_exp_f32_e32 v104, v104
	v_exp_f32_e32 v105, v105
	s_nop 0
	v_pk_add_f32 v[104:105], v[104:105], 1.0 op_sel_hi:[1,0]
	s_nop 0
	v_div_scale_f32 v112, s[46:47], v105, v105, 1.0
	v_rcp_f32_e32 v113, v112
	s_nop 0
	v_fma_f32 v114, -v112, v113, 1.0
	v_fmac_f32_e32 v113, v114, v113
	v_div_scale_f32 v114, vcc, 1.0, v105, 1.0
	v_mul_f32_e32 v115, v114, v113
	v_fma_f32 v118, -v112, v115, v114
	v_fmac_f32_e32 v115, v118, v113
	v_fma_f32 v112, -v112, v115, v114
	v_div_fmas_f32 v112, v112, v113, v115
	v_div_fixup_f32 v105, v112, v105, 1.0
	v_div_scale_f32 v112, s[46:47], v104, v104, 1.0
	v_rcp_f32_e32 v113, v112
	s_nop 0
	v_fma_f32 v114, -v112, v113, 1.0
	v_fmac_f32_e32 v113, v114, v113
	v_div_scale_f32 v114, vcc, 1.0, v104, 1.0
	v_mul_f32_e32 v115, v114, v113
	v_fma_f32 v118, -v112, v115, v114
	v_fmac_f32_e32 v115, v118, v113
	v_fma_f32 v112, -v112, v115, v114
	v_div_fmas_f32 v112, v112, v113, v115
	v_div_fixup_f32 v104, v112, v104, 1.0
	v_pk_mul_f32 v[102:103], v[102:103], v[104:105]
	v_lshlrev_b32_e32 v104, 16, v106
	v_and_b32_e32 v105, 0xffff0000, v106
	v_pk_add_f32 v[96:97], v[96:97], v[104:105]
	s_nop 0
	v_mul_f32_e32 v104, 0x3d372713, v96
	v_mul_f32_e32 v105, 0x3d372713, v97
	v_mul_f32_e32 v104, v96, v104
	v_mul_f32_e32 v105, v97, v105
	v_fma_f32 v104, v96, v104, v96
	v_fma_f32 v105, v97, v105, v97
	v_mul_f32_e32 v104, 0x3fcc422a, v104
	v_mul_f32_e32 v105, 0x3fcc422a, v105
	v_mul_f32_e32 v104, 0xbfb8aa3b, v104
	v_mul_f32_e32 v105, 0xbfb8aa3b, v105
	v_exp_f32_e32 v104, v104
	v_exp_f32_e32 v105, v105
	s_nop 0
	v_pk_add_f32 v[104:105], v[104:105], 1.0 op_sel_hi:[1,0]
	s_nop 0
	v_div_scale_f32 v106, s[46:47], v105, v105, 1.0
	v_rcp_f32_e32 v112, v106
	s_nop 0
	v_fma_f32 v113, -v106, v112, 1.0
	v_fmac_f32_e32 v112, v113, v112
	v_div_scale_f32 v113, vcc, 1.0, v105, 1.0
	v_mul_f32_e32 v114, v113, v112
	v_fma_f32 v115, -v106, v114, v113
	v_fmac_f32_e32 v114, v115, v112
	v_fma_f32 v106, -v106, v114, v113
	v_div_fmas_f32 v106, v106, v112, v114
	v_div_fixup_f32 v105, v106, v105, 1.0
	v_div_scale_f32 v106, s[46:47], v104, v104, 1.0
	v_rcp_f32_e32 v112, v106
	s_nop 0
	v_fma_f32 v113, -v106, v112, 1.0
	v_fmac_f32_e32 v112, v113, v112
	v_div_scale_f32 v113, vcc, 1.0, v104, 1.0
	v_mul_f32_e32 v114, v113, v112
	v_fma_f32 v115, -v106, v114, v113
	v_fmac_f32_e32 v114, v115, v112
	v_fma_f32 v106, -v106, v114, v113
	v_div_fmas_f32 v106, v106, v112, v114
	v_div_fixup_f32 v104, v106, v104, 1.0
	v_pk_mul_f32 v[104:105], v[96:97], v[104:105]
	v_lshlrev_b32_e32 v96, 16, v107
	v_and_b32_e32 v97, 0xffff0000, v107
	v_pk_add_f32 v[96:97], v[98:99], v[96:97]
	s_nop 0
	v_mul_f32_e32 v98, 0x3d372713, v96
	v_mul_f32_e32 v99, 0x3d372713, v97
	v_mul_f32_e32 v98, v96, v98
	v_mul_f32_e32 v99, v97, v99
	v_fma_f32 v98, v96, v98, v96
	v_fma_f32 v99, v97, v99, v97
	v_mul_f32_e32 v98, 0x3fcc422a, v98
	v_mul_f32_e32 v99, 0x3fcc422a, v99
	v_mul_f32_e32 v98, 0xbfb8aa3b, v98
	v_mul_f32_e32 v99, 0xbfb8aa3b, v99
	v_exp_f32_e32 v98, v98
	v_exp_f32_e32 v99, v99
	s_nop 0
	v_pk_add_f32 v[98:99], v[98:99], 1.0 op_sel_hi:[1,0]
	s_nop 0
	v_div_scale_f32 v106, s[46:47], v99, v99, 1.0
	v_rcp_f32_e32 v107, v106
	s_nop 0
	v_fma_f32 v112, -v106, v107, 1.0
	v_fmac_f32_e32 v107, v112, v107
	v_div_scale_f32 v112, vcc, 1.0, v99, 1.0
	v_mul_f32_e32 v113, v112, v107
	v_fma_f32 v114, -v106, v113, v112
	v_fmac_f32_e32 v113, v114, v107
	v_fma_f32 v106, -v106, v113, v112
	v_div_fmas_f32 v106, v106, v107, v113
	v_div_fixup_f32 v99, v106, v99, 1.0
	v_div_scale_f32 v106, s[46:47], v98, v98, 1.0
	v_rcp_f32_e32 v107, v106
	s_nop 0
	v_fma_f32 v112, -v106, v107, 1.0
	v_fmac_f32_e32 v107, v112, v107
	v_div_scale_f32 v112, vcc, 1.0, v98, 1.0
	v_mul_f32_e32 v113, v112, v107
	v_fma_f32 v114, -v106, v113, v112
	v_fmac_f32_e32 v113, v114, v107
	v_fma_f32 v106, -v106, v113, v112
	v_div_fmas_f32 v106, v106, v107, v113
	v_div_fixup_f32 v98, v106, v98, 1.0
	v_pk_mul_f32 v[106:107], v[96:97], v[98:99]
	v_cvt_pk_bf16_f32 v96, v100, v101
	v_lshl_add_u64 v[100:101], v[108:109], 0, v[116:117]
	v_lshl_add_u64 v[100:101], v[100:101], 0, v[110:111]
	v_cvt_pk_bf16_f32 v97, v102, v103
	v_cvt_pk_bf16_f32 v98, v104, v105
	v_cvt_pk_bf16_f32 v99, v106, v107
	v_lshl_add_u64 v[100:101], v[100:101], 0, v[140:141]
	global_store_dwordx4 v[100:101], v[96:99], off
	s_nop 1
	v_or_b32_e32 v96, 32, v142
	v_add_u32_e32 v97, v96, v160
	v_ashrrev_i32_e32 v100, 11, v97
	v_mul_i32_i24_e32 v97, 0x800, v100
	v_sub_u32_e32 v98, v96, v97
	v_ashrrev_i32_e32 v97, 31, v96
	v_lshlrev_b64 v[96:97], 10, v[96:97]
	v_lshl_add_u64 v[96:97], s[30:31], 0, v[96:97]
	v_ashrrev_i32_e32 v99, 31, v98
	v_lshl_add_u64 v[104:105], v[96:97], 0, v[144:145]
	v_lshlrev_b64 v[102:103], 15, v[98:99]
	s_nop 1
	v_lshlrev_b32_e32 v100, 4, v100
	v_ashrrev_i32_e32 v101, 31, v100
	s_waitcnt vmcnt(12)
; __device__ __forceinline__ float gelu_tanh(float x) { return x * sigmoidf_(1.5957691216057308f * (x + 0.044715f * x * x * x)); }
; __device__ __forceinline__ unsigned cvt_pk_bf16(float lo, float hi) { const f32x2c v = {lo, hi}; const bf16x2c b = __builtin_convertvector(v, bf16x2c); return __builtin_bit_cast(unsigned, b); }
;     __device__ __forceinline__ void operator()(const f32x4 (&acc)[2][2][4][2], const Unit& u, int wr, int wc, int fr, int fq) const {
;     ...
;             for (int m = 0; m < 4; ++m) { const int row = row0 + ai * HALF + m * 16; const int g = row / S5R, rl = row % S5R;
; #pragma unroll
;                 for (int bj = 0; bj < 2; ++bj) { const int col = col0 + bj * HALF;
;                     const u32x4 yi = *(const u32x4*)(YI + (size_t)row * 512 + col);
;                     const unsigned yw[4] = {yi.x, yi.y, yi.z, yi.w};
;                     const f32x4 v0 = acc[ai][bj][m][0], v1 = acc[ai][bj][m][1];
;                     float o[8];
; #pragma unroll
;                     for (int q = 0; q < 4; ++q) { const float al = (q < 2) ? v0[2 * q] : v1[2 * q - 4], ah = (q < 2) ? v0[2 * q + 1] : v1[2 * q - 3];
;                         o[2 * q] = gelu_tanh(al + __builtin_bit_cast(float, yw[q] << 16)); o[2 * q + 1] = gelu_tanh(ah + __builtin_bit_cast(float, yw[q] & 0xffff0000u)); }
;                     u32x4 w; w.x = cvt_pk_bf16(o[0], o[1]); w.y = cvt_pk_bf16(o[2], o[3]); w.z = cvt_pk_bf16(o[4], o[5]); w.w = cvt_pk_bf16(o[6], o[7]);
;                     const size_t tok = (size_t)rl * S5L + (col >> 4);
;                     *(u32x4*)(Z + tok * 512 + g * 16 + (col & 15)) = w; } }
	v_mov_b32_e32 v96, v186
	v_mov_b32_e32 v97, v187
	v_mov_b32_e32 v98, v188
	v_mov_b32_e32 v99, v189
	global_load_dwordx4 v[186:189], v[168:169], off offset:256
	v_lshlrev_b32_e32 v106, 16, v96
	v_and_b32_e32 v107, 0xffff0000, v96
	v_pk_add_f32 v[92:93], v[92:93], v[106:107]
	s_nop 0
	v_mul_f32_e32 v96, 0x3d372713, v92
	v_mul_f32_e32 v96, v92, v96
	v_fma_f32 v96, v92, v96, v92
	v_mul_f32_e32 v96, 0x3fcc422a, v96
	v_mul_f32_e32 v96, 0xbfb8aa3b, v96
	v_exp_f32_e32 v106, v96
	v_mul_f32_e32 v96, 0x3d372713, v93
	v_mul_f32_e32 v96, v93, v96
	v_fma_f32 v96, v93, v96, v93
	v_mul_f32_e32 v96, 0x3fcc422a, v96
	v_mul_f32_e32 v96, 0xbfb8aa3b, v96
	v_exp_f32_e32 v107, v96
	s_nop 0
	v_pk_add_f32 v[106:107], v[106:107], 1.0 op_sel_hi:[1,0]
	s_nop 0
	v_div_scale_f32 v96, s[46:47], v107, v107, 1.0
	v_rcp_f32_e32 v108, v96
	s_nop 0
	v_fma_f32 v109, -v96, v108, 1.0
	v_fmac_f32_e32 v108, v109, v108
	v_div_scale_f32 v109, vcc, 1.0, v107, 1.0
	v_mul_f32_e32 v110, v109, v108
	v_fma_f32 v111, -v96, v110, v109
	v_fmac_f32_e32 v110, v111, v108
	v_fma_f32 v96, -v96, v110, v109
	v_div_fmas_f32 v96, v96, v108, v110
	v_div_fixup_f32 v107, v96, v107, 1.0
	v_div_scale_f32 v96, s[46:47], v106, v106, 1.0
	v_rcp_f32_e32 v108, v96
	s_nop 0
	v_fma_f32 v109, -v96, v108, 1.0
	v_fmac_f32_e32 v108, v109, v108
	v_div_scale_f32 v109, vcc, 1.0, v106, 1.0
	v_mul_f32_e32 v110, v109, v108
	v_fma_f32 v111, -v96, v110, v109
	v_fmac_f32_e32 v110, v111, v108
	v_fma_f32 v96, -v96, v110, v109
	v_div_fmas_f32 v96, v96, v108, v110
	v_div_fixup_f32 v106, v96, v106, 1.0
	v_lshlrev_b32_e32 v96, 16, v97
	v_and_b32_e32 v97, 0xffff0000, v97
	v_pk_add_f32 v[94:95], v[94:95], v[96:97]
	v_pk_mul_f32 v[92:93], v[92:93], v[106:107]
	v_mul_f32_e32 v96, 0x3d372713, v94
	v_mul_f32_e32 v97, 0x3d372713, v95
	v_mul_f32_e32 v96, v94, v96
	v_mul_f32_e32 v97, v95, v97
	v_fma_f32 v96, v94, v96, v94
	v_fma_f32 v97, v95, v97, v95
	v_mul_f32_e32 v96, 0x3fcc422a, v96
	v_mul_f32_e32 v97, 0x3fcc422a, v97
	v_mul_f32_e32 v96, 0xbfb8aa3b, v96
	v_mul_f32_e32 v97, 0xbfb8aa3b, v97
	v_exp_f32_e32 v96, v96
	v_exp_f32_e32 v97, v97
	s_nop 0
	v_pk_add_f32 v[96:97], v[96:97], 1.0 op_sel_hi:[1,0]
	s_nop 0
	v_div_scale_f32 v106, s[46:47], v97, v97, 1.0
	v_rcp_f32_e32 v107, v106
	s_nop 0
	v_fma_f32 v108, -v106, v107, 1.0
	v_fmac_f32_e32 v107, v108, v107
	v_div_scale_f32 v108, vcc, 1.0, v97, 1.0
	v_mul_f32_e32 v109, v108, v107
	v_fma_f32 v110, -v106, v109, v108
	v_fmac_f32_e32 v109, v110, v107
	v_fma_f32 v106, -v106, v109, v108
	v_div_fmas_f32 v106, v106, v107, v109
	v_div_fixup_f32 v97, v106, v97, 1.0
	v_div_scale_f32 v106, s[46:47], v96, v96, 1.0
	v_rcp_f32_e32 v107, v106
	s_nop 0
	v_fma_f32 v108, -v106, v107, 1.0
	v_fmac_f32_e32 v107, v108, v107
	v_div_scale_f32 v108, vcc, 1.0, v96, 1.0
	v_mul_f32_e32 v109, v108, v107
	v_fma_f32 v110, -v106, v109, v108
	v_fmac_f32_e32 v109, v110, v107
	v_fma_f32 v106, -v106, v109, v108
	v_div_fmas_f32 v106, v106, v107, v109
	v_div_fixup_f32 v96, v106, v96, 1.0
	v_pk_mul_f32 v[94:95], v[94:95], v[96:97]
	v_lshlrev_b32_e32 v96, 16, v98
	v_and_b32_e32 v97, 0xffff0000, v98
	v_pk_add_f32 v[88:89], v[88:89], v[96:97]
	s_nop 0
	v_mul_f32_e32 v96, 0x3d372713, v88
	v_mul_f32_e32 v97, 0x3d372713, v89
	v_mul_f32_e32 v96, v88, v96
	v_mul_f32_e32 v97, v89, v97
	v_fma_f32 v96, v88, v96, v88
	v_fma_f32 v97, v89, v97, v89
	v_mul_f32_e32 v96, 0x3fcc422a, v96
	v_mul_f32_e32 v97, 0x3fcc422a, v97
	v_mul_f32_e32 v96, 0xbfb8aa3b, v96
	v_mul_f32_e32 v97, 0xbfb8aa3b, v97
	v_exp_f32_e32 v96, v96
	v_exp_f32_e32 v97, v97
	s_nop 0
	v_pk_add_f32 v[96:97], v[96:97], 1.0 op_sel_hi:[1,0]
	s_nop 0
	v_div_scale_f32 v98, s[46:47], v97, v97, 1.0
	v_rcp_f32_e32 v106, v98
	s_nop 0
	v_fma_f32 v107, -v98, v106, 1.0
	v_fmac_f32_e32 v106, v107, v106
	v_div_scale_f32 v107, vcc, 1.0, v97, 1.0
	v_mul_f32_e32 v108, v107, v106
	v_fma_f32 v109, -v98, v108, v107
	v_fmac_f32_e32 v108, v109, v106
	v_fma_f32 v98, -v98, v108, v107
	v_div_fmas_f32 v98, v98, v106, v108
	v_div_fixup_f32 v97, v98, v97, 1.0
	v_div_scale_f32 v98, s[46:47], v96, v96, 1.0
	v_rcp_f32_e32 v106, v98
	s_nop 0
	v_fma_f32 v107, -v98, v106, 1.0
	v_fmac_f32_e32 v106, v107, v106
	v_div_scale_f32 v107, vcc, 1.0, v96, 1.0
	v_mul_f32_e32 v108, v107, v106
	v_fma_f32 v109, -v98, v108, v107
	v_fmac_f32_e32 v108, v109, v106
	v_fma_f32 v98, -v98, v108, v107
	v_div_fmas_f32 v98, v98, v106, v108
	v_div_fixup_f32 v96, v98, v96, 1.0
	v_pk_mul_f32 v[96:97], v[88:89], v[96:97]
	v_lshlrev_b32_e32 v88, 16, v99
	v_and_b32_e32 v89, 0xffff0000, v99
	v_pk_add_f32 v[88:89], v[90:91], v[88:89]
	s_nop 0
	v_mul_f32_e32 v90, 0x3d372713, v88
	v_mul_f32_e32 v91, 0x3d372713, v89
	v_mul_f32_e32 v90, v88, v90
	v_mul_f32_e32 v91, v89, v91
	v_fma_f32 v90, v88, v90, v88
	v_fma_f32 v91, v89, v91, v89
	v_mul_f32_e32 v90, 0x3fcc422a, v90
	v_mul_f32_e32 v91, 0x3fcc422a, v91
	v_mul_f32_e32 v90, 0xbfb8aa3b, v90
	v_mul_f32_e32 v91, 0xbfb8aa3b, v91
	v_exp_f32_e32 v90, v90
	v_exp_f32_e32 v91, v91
	s_nop 0
	v_pk_add_f32 v[90:91], v[90:91], 1.0 op_sel_hi:[1,0]
	s_nop 0
	v_div_scale_f32 v98, s[46:47], v91, v91, 1.0
	v_rcp_f32_e32 v99, v98
	s_nop 0
	v_fma_f32 v106, -v98, v99, 1.0
	v_fmac_f32_e32 v99, v106, v99
	v_div_scale_f32 v106, vcc, 1.0, v91, 1.0
	v_mul_f32_e32 v107, v106, v99
	v_fma_f32 v108, -v98, v107, v106
	v_fmac_f32_e32 v107, v108, v99
	v_fma_f32 v98, -v98, v107, v106
	v_div_fmas_f32 v98, v98, v99, v107
	v_div_fixup_f32 v91, v98, v91, 1.0
	v_div_scale_f32 v98, s[46:47], v90, v90, 1.0
	v_rcp_f32_e32 v99, v98
	s_nop 0
	v_fma_f32 v106, -v98, v99, 1.0
	v_fmac_f32_e32 v99, v106, v99
	v_div_scale_f32 v106, vcc, 1.0, v90, 1.0
	v_mul_f32_e32 v107, v106, v99
	v_fma_f32 v108, -v98, v107, v106
	v_fmac_f32_e32 v107, v108, v99
	v_fma_f32 v98, -v98, v107, v106
	v_div_fmas_f32 v98, v98, v99, v107
	v_div_fixup_f32 v90, v98, v90, 1.0
	v_pk_mul_f32 v[98:99], v[88:89], v[90:91]
	v_cvt_pk_bf16_f32 v88, v92, v93
	v_lshl_add_u64 v[92:93], s[36:37], 0, v[102:103]
	v_cvt_pk_bf16_f32 v89, v94, v95
	v_cvt_pk_bf16_f32 v90, v96, v97
	v_lshl_add_u64 v[96:97], v[92:93], 0, v[124:125]
	v_lshlrev_b64 v[94:95], 1, v[100:101]
	v_lshl_add_u64 v[96:97], v[96:97], 0, v[94:95]
	v_cvt_pk_bf16_f32 v91, v98, v99
	v_lshl_add_u64 v[96:97], v[96:97], 0, v[140:141]
	global_store_dwordx4 v[96:97], v[88:91], off
	s_nop 1
	s_waitcnt vmcnt(13)
; __device__ __forceinline__ float gelu_tanh(float x) { return x * sigmoidf_(1.5957691216057308f * (x + 0.044715f * x * x * x)); }
; __device__ __forceinline__ unsigned cvt_pk_bf16(float lo, float hi) { const f32x2c v = {lo, hi}; const bf16x2c b = __builtin_convertvector(v, bf16x2c); return __builtin_bit_cast(unsigned, b); }
;     __device__ __forceinline__ void operator()(const f32x4 (&acc)[2][2][4][2], const Unit& u, int wr, int wc, int fr, int fq) const {
;     ...
;             for (int m = 0; m < 4; ++m) { const int row = row0 + ai * HALF + m * 16; const int g = row / S5R, rl = row % S5R;
; #pragma unroll
;                 for (int bj = 0; bj < 2; ++bj) { const int col = col0 + bj * HALF;
;                     const u32x4 yi = *(const u32x4*)(YI + (size_t)row * 512 + col);
;                     const unsigned yw[4] = {yi.x, yi.y, yi.z, yi.w};
;                     const f32x4 v0 = acc[ai][bj][m][0], v1 = acc[ai][bj][m][1];
;                     float o[8];
; #pragma unroll
;                     for (int q = 0; q < 4; ++q) { const float al = (q < 2) ? v0[2 * q] : v1[2 * q - 4], ah = (q < 2) ? v0[2 * q + 1] : v1[2 * q - 3];
;                         o[2 * q] = gelu_tanh(al + __builtin_bit_cast(float, yw[q] << 16)); o[2 * q + 1] = gelu_tanh(ah + __builtin_bit_cast(float, yw[q] & 0xffff0000u)); }
;                     u32x4 w; w.x = cvt_pk_bf16(o[0], o[1]); w.y = cvt_pk_bf16(o[2], o[3]); w.z = cvt_pk_bf16(o[4], o[5]); w.w = cvt_pk_bf16(o[6], o[7]);
;                     const size_t tok = (size_t)rl * S5L + (col >> 4);
;                     *(u32x4*)(Z + tok * 512 + g * 16 + (col & 15)) = w; } }
	v_mov_b32_e32 v88, v190
	v_mov_b32_e32 v89, v191
	v_mov_b32_e32 v90, v192
	v_mov_b32_e32 v91, v193
	s_mov_b64 s[98:99], 0x2c000
	v_lshl_add_u64 v[168:169], v[166:167], 0, s[98:99]
	global_load_dwordx4 v[190:193], v[168:169], off
	v_lshlrev_b32_e32 v96, 16, v88
	v_and_b32_e32 v97, 0xffff0000, v88
	v_pk_add_f32 v[84:85], v[84:85], v[96:97]
	s_nop 0
	v_mul_f32_e32 v88, 0x3d372713, v84
	v_mul_f32_e32 v88, v84, v88
	v_fma_f32 v88, v84, v88, v84
	v_mul_f32_e32 v88, 0x3fcc422a, v88
	v_mul_f32_e32 v88, 0xbfb8aa3b, v88
	v_exp_f32_e32 v96, v88
	v_mul_f32_e32 v88, 0x3d372713, v85
	v_mul_f32_e32 v88, v85, v88
	v_fma_f32 v88, v85, v88, v85
	v_mul_f32_e32 v88, 0x3fcc422a, v88
	v_mul_f32_e32 v88, 0xbfb8aa3b, v88
	v_exp_f32_e32 v97, v88
	s_nop 0
	v_pk_add_f32 v[96:97], v[96:97], 1.0 op_sel_hi:[1,0]
	s_nop 0
	v_div_scale_f32 v88, s[46:47], v97, v97, 1.0
	v_rcp_f32_e32 v98, v88
	s_nop 0
	v_fma_f32 v99, -v88, v98, 1.0
	v_fmac_f32_e32 v98, v99, v98
	v_div_scale_f32 v99, vcc, 1.0, v97, 1.0
	v_mul_f32_e32 v100, v99, v98
	v_fma_f32 v101, -v88, v100, v99
	v_fmac_f32_e32 v100, v101, v98
	v_fma_f32 v88, -v88, v100, v99
	v_div_fmas_f32 v88, v88, v98, v100
	v_div_fixup_f32 v97, v88, v97, 1.0
	v_div_scale_f32 v88, s[46:47], v96, v96, 1.0
	v_rcp_f32_e32 v98, v88
	s_nop 0
	v_fma_f32 v99, -v88, v98, 1.0
	v_fmac_f32_e32 v98, v99, v98
	v_div_scale_f32 v99, vcc, 1.0, v96, 1.0
	v_mul_f32_e32 v100, v99, v98
	v_fma_f32 v101, -v88, v100, v99
	v_fmac_f32_e32 v100, v101, v98
	v_fma_f32 v88, -v88, v100, v99
	v_div_fmas_f32 v88, v88, v98, v100
	v_div_fixup_f32 v96, v88, v96, 1.0
	v_lshlrev_b32_e32 v88, 16, v89
	v_and_b32_e32 v89, 0xffff0000, v89
	v_pk_add_f32 v[86:87], v[86:87], v[88:89]
	v_pk_mul_f32 v[84:85], v[84:85], v[96:97]
	v_mul_f32_e32 v88, 0x3d372713, v86
	v_mul_f32_e32 v89, 0x3d372713, v87
	v_mul_f32_e32 v88, v86, v88
	v_mul_f32_e32 v89, v87, v89
	v_fma_f32 v88, v86, v88, v86
	v_fma_f32 v89, v87, v89, v87
	v_mul_f32_e32 v88, 0x3fcc422a, v88
	v_mul_f32_e32 v89, 0x3fcc422a, v89
	v_mul_f32_e32 v88, 0xbfb8aa3b, v88
	v_mul_f32_e32 v89, 0xbfb8aa3b, v89
	v_exp_f32_e32 v88, v88
	v_exp_f32_e32 v89, v89
	s_nop 0
	v_pk_add_f32 v[88:89], v[88:89], 1.0 op_sel_hi:[1,0]
	s_nop 0
	v_div_scale_f32 v96, s[46:47], v89, v89, 1.0
	v_rcp_f32_e32 v97, v96
	s_nop 0
	v_fma_f32 v98, -v96, v97, 1.0
	v_fmac_f32_e32 v97, v98, v97
	v_div_scale_f32 v98, vcc, 1.0, v89, 1.0
	v_mul_f32_e32 v99, v98, v97
	v_fma_f32 v100, -v96, v99, v98
	v_fmac_f32_e32 v99, v100, v97
	v_fma_f32 v96, -v96, v99, v98
	v_div_fmas_f32 v96, v96, v97, v99
	v_div_fixup_f32 v89, v96, v89, 1.0
	v_div_scale_f32 v96, s[46:47], v88, v88, 1.0
	v_rcp_f32_e32 v97, v96
	s_nop 0
	v_fma_f32 v98, -v96, v97, 1.0
	v_fmac_f32_e32 v97, v98, v97
	v_div_scale_f32 v98, vcc, 1.0, v88, 1.0
	v_mul_f32_e32 v99, v98, v97
	v_fma_f32 v100, -v96, v99, v98
	v_fmac_f32_e32 v99, v100, v97
	v_fma_f32 v96, -v96, v99, v98
	v_div_fmas_f32 v96, v96, v97, v99
	v_div_fixup_f32 v88, v96, v88, 1.0
	v_pk_mul_f32 v[86:87], v[86:87], v[88:89]
	v_lshlrev_b32_e32 v88, 16, v90
	v_and_b32_e32 v89, 0xffff0000, v90
	v_pk_add_f32 v[80:81], v[80:81], v[88:89]
	s_nop 0
	v_mul_f32_e32 v88, 0x3d372713, v80
	v_mul_f32_e32 v89, 0x3d372713, v81
	v_mul_f32_e32 v88, v80, v88
	v_mul_f32_e32 v89, v81, v89
	v_fma_f32 v88, v80, v88, v80
	v_fma_f32 v89, v81, v89, v81
	v_mul_f32_e32 v88, 0x3fcc422a, v88
	v_mul_f32_e32 v89, 0x3fcc422a, v89
	v_mul_f32_e32 v88, 0xbfb8aa3b, v88
	v_mul_f32_e32 v89, 0xbfb8aa3b, v89
	v_exp_f32_e32 v88, v88
	v_exp_f32_e32 v89, v89
	s_nop 0
	v_pk_add_f32 v[88:89], v[88:89], 1.0 op_sel_hi:[1,0]
	s_nop 0
	v_div_scale_f32 v90, s[46:47], v89, v89, 1.0
	v_rcp_f32_e32 v96, v90
	s_nop 0
	v_fma_f32 v97, -v90, v96, 1.0
	v_fmac_f32_e32 v96, v97, v96
	v_div_scale_f32 v97, vcc, 1.0, v89, 1.0
	v_mul_f32_e32 v98, v97, v96
	v_fma_f32 v99, -v90, v98, v97
	v_fmac_f32_e32 v98, v99, v96
	v_fma_f32 v90, -v90, v98, v97
	v_div_fmas_f32 v90, v90, v96, v98
	v_div_fixup_f32 v89, v90, v89, 1.0
	v_div_scale_f32 v90, s[46:47], v88, v88, 1.0
	v_rcp_f32_e32 v96, v90
	s_nop 0
	v_fma_f32 v97, -v90, v96, 1.0
	v_fmac_f32_e32 v96, v97, v96
	v_div_scale_f32 v97, vcc, 1.0, v88, 1.0
	v_mul_f32_e32 v98, v97, v96
	v_fma_f32 v99, -v90, v98, v97
	v_fmac_f32_e32 v98, v99, v96
	v_fma_f32 v90, -v90, v98, v97
	v_div_fmas_f32 v90, v90, v96, v98
	v_div_fixup_f32 v88, v90, v88, 1.0
	v_pk_mul_f32 v[88:89], v[80:81], v[88:89]
	v_lshlrev_b32_e32 v80, 16, v91
	v_and_b32_e32 v81, 0xffff0000, v91
	v_pk_add_f32 v[80:81], v[82:83], v[80:81]
	s_nop 0
	v_mul_f32_e32 v82, 0x3d372713, v80
	v_mul_f32_e32 v83, 0x3d372713, v81
	v_mul_f32_e32 v82, v80, v82
	v_mul_f32_e32 v83, v81, v83
	v_fma_f32 v82, v80, v82, v80
	v_fma_f32 v83, v81, v83, v81
	v_mul_f32_e32 v82, 0x3fcc422a, v82
	v_mul_f32_e32 v83, 0x3fcc422a, v83
	v_mul_f32_e32 v82, 0xbfb8aa3b, v82
	v_mul_f32_e32 v83, 0xbfb8aa3b, v83
	v_exp_f32_e32 v82, v82
	v_exp_f32_e32 v83, v83
	s_nop 0
	v_pk_add_f32 v[82:83], v[82:83], 1.0 op_sel_hi:[1,0]
	s_nop 0
	v_div_scale_f32 v90, s[46:47], v83, v83, 1.0
	v_rcp_f32_e32 v91, v90
	s_nop 0
	v_fma_f32 v96, -v90, v91, 1.0
	v_fmac_f32_e32 v91, v96, v91
	v_div_scale_f32 v96, vcc, 1.0, v83, 1.0
	v_mul_f32_e32 v97, v96, v91
	v_fma_f32 v98, -v90, v97, v96
	v_fmac_f32_e32 v97, v98, v91
	v_fma_f32 v90, -v90, v97, v96
	v_div_fmas_f32 v90, v90, v91, v97
	v_div_fixup_f32 v83, v90, v83, 1.0
	v_div_scale_f32 v90, s[46:47], v82, v82, 1.0
	v_rcp_f32_e32 v91, v90
	s_nop 0
	v_fma_f32 v96, -v90, v91, 1.0
	v_fmac_f32_e32 v91, v96, v91
	v_div_scale_f32 v96, vcc, 1.0, v82, 1.0
	v_mul_f32_e32 v97, v96, v91
	v_fma_f32 v98, -v90, v97, v96
	v_fmac_f32_e32 v97, v98, v91
	v_fma_f32 v90, -v90, v97, v96
	v_div_fmas_f32 v90, v90, v91, v97
	v_div_fixup_f32 v82, v90, v82, 1.0
	v_pk_mul_f32 v[90:91], v[80:81], v[82:83]
	v_cvt_pk_bf16_f32 v80, v84, v85
	v_lshl_add_u64 v[84:85], v[92:93], 0, v[116:117]
	v_lshl_add_u64 v[84:85], v[84:85], 0, v[94:95]
	v_cvt_pk_bf16_f32 v81, v86, v87
	v_cvt_pk_bf16_f32 v82, v88, v89
	v_cvt_pk_bf16_f32 v83, v90, v91
	v_lshl_add_u64 v[84:85], v[84:85], 0, v[140:141]
	global_store_dwordx4 v[84:85], v[80:83], off
	s_nop 1
	v_or_b32_e32 v80, 48, v142
	v_add_u32_e32 v81, v80, v160
	v_ashrrev_i32_e32 v84, 11, v81
	v_mul_i32_i24_e32 v81, 0x800, v84
	v_sub_u32_e32 v82, v80, v81
	v_ashrrev_i32_e32 v81, 31, v80
	v_lshlrev_b64 v[80:81], 10, v[80:81]
	v_lshl_add_u64 v[80:81], s[30:31], 0, v[80:81]
	v_ashrrev_i32_e32 v83, 31, v82
	v_lshl_add_u64 v[88:89], v[80:81], 0, v[144:145]
	v_lshlrev_b64 v[86:87], 15, v[82:83]
	s_nop 1
	v_lshlrev_b32_e32 v84, 4, v84
	v_ashrrev_i32_e32 v85, 31, v84
	s_waitcnt vmcnt(14)
; __device__ __forceinline__ float gelu_tanh(float x) { return x * sigmoidf_(1.5957691216057308f * (x + 0.044715f * x * x * x)); }
; __device__ __forceinline__ unsigned cvt_pk_bf16(float lo, float hi) { const f32x2c v = {lo, hi}; const bf16x2c b = __builtin_convertvector(v, bf16x2c); return __builtin_bit_cast(unsigned, b); }
;     __device__ __forceinline__ void operator()(const f32x4 (&acc)[2][2][4][2], const Unit& u, int wr, int wc, int fr, int fq) const {
;     ...
;             for (int m = 0; m < 4; ++m) { const int row = row0 + ai * HALF + m * 16; const int g = row / S5R, rl = row % S5R;
; #pragma unroll
;                 for (int bj = 0; bj < 2; ++bj) { const int col = col0 + bj * HALF;
;                     const u32x4 yi = *(const u32x4*)(YI + (size_t)row * 512 + col);
;                     const unsigned yw[4] = {yi.x, yi.y, yi.z, yi.w};
;                     const f32x4 v0 = acc[ai][bj][m][0], v1 = acc[ai][bj][m][1];
;                     float o[8];
; #pragma unroll
;                     for (int q = 0; q < 4; ++q) { const float al = (q < 2) ? v0[2 * q] : v1[2 * q - 4], ah = (q < 2) ? v0[2 * q + 1] : v1[2 * q - 3];
;                         o[2 * q] = gelu_tanh(al + __builtin_bit_cast(float, yw[q] << 16)); o[2 * q + 1] = gelu_tanh(ah + __builtin_bit_cast(float, yw[q] & 0xffff0000u)); }
;                     u32x4 w; w.x = cvt_pk_bf16(o[0], o[1]); w.y = cvt_pk_bf16(o[2], o[3]); w.z = cvt_pk_bf16(o[4], o[5]); w.w = cvt_pk_bf16(o[6], o[7]);
;                     const size_t tok = (size_t)rl * S5L + (col >> 4);
;                     *(u32x4*)(Z + tok * 512 + g * 16 + (col & 15)) = w; } }
	v_mov_b32_e32 v80, v194
	v_mov_b32_e32 v81, v195
	v_mov_b32_e32 v82, v196
	v_mov_b32_e32 v83, v197
	global_load_dwordx4 v[194:197], v[168:169], off offset:256
	v_lshlrev_b32_e32 v90, 16, v80
	v_and_b32_e32 v91, 0xffff0000, v80
	v_pk_add_f32 v[76:77], v[76:77], v[90:91]
	s_nop 0
	v_mul_f32_e32 v80, 0x3d372713, v76
	v_mul_f32_e32 v80, v76, v80
	v_fma_f32 v80, v76, v80, v76
	v_mul_f32_e32 v80, 0x3fcc422a, v80
	v_mul_f32_e32 v80, 0xbfb8aa3b, v80
	v_exp_f32_e32 v90, v80
	v_mul_f32_e32 v80, 0x3d372713, v77
	v_mul_f32_e32 v80, v77, v80
	v_fma_f32 v80, v77, v80, v77
	v_mul_f32_e32 v80, 0x3fcc422a, v80
	v_mul_f32_e32 v80, 0xbfb8aa3b, v80
	v_exp_f32_e32 v91, v80
	s_nop 0
	v_pk_add_f32 v[90:91], v[90:91], 1.0 op_sel_hi:[1,0]
	s_nop 0
	v_div_scale_f32 v80, s[46:47], v91, v91, 1.0
	v_rcp_f32_e32 v92, v80
	s_nop 0
	v_fma_f32 v93, -v80, v92, 1.0
	v_fmac_f32_e32 v92, v93, v92
	v_div_scale_f32 v93, vcc, 1.0, v91, 1.0
	v_mul_f32_e32 v94, v93, v92
	v_fma_f32 v95, -v80, v94, v93
	v_fmac_f32_e32 v94, v95, v92
	v_fma_f32 v80, -v80, v94, v93
	v_div_fmas_f32 v80, v80, v92, v94
	v_div_fixup_f32 v91, v80, v91, 1.0
	v_div_scale_f32 v80, s[46:47], v90, v90, 1.0
	v_rcp_f32_e32 v92, v80
	s_nop 0
	v_fma_f32 v93, -v80, v92, 1.0
	v_fmac_f32_e32 v92, v93, v92
	v_div_scale_f32 v93, vcc, 1.0, v90, 1.0
	v_mul_f32_e32 v94, v93, v92
	v_fma_f32 v95, -v80, v94, v93
	v_fmac_f32_e32 v94, v95, v92
	v_fma_f32 v80, -v80, v94, v93
	v_div_fmas_f32 v80, v80, v92, v94
	v_div_fixup_f32 v90, v80, v90, 1.0
	v_lshlrev_b32_e32 v80, 16, v81
	v_and_b32_e32 v81, 0xffff0000, v81
	v_pk_add_f32 v[78:79], v[78:79], v[80:81]
	v_pk_mul_f32 v[76:77], v[76:77], v[90:91]
	v_mul_f32_e32 v80, 0x3d372713, v78
	v_mul_f32_e32 v81, 0x3d372713, v79
	v_mul_f32_e32 v80, v78, v80
	v_mul_f32_e32 v81, v79, v81
	v_fma_f32 v80, v78, v80, v78
	v_fma_f32 v81, v79, v81, v79
	v_mul_f32_e32 v80, 0x3fcc422a, v80
	v_mul_f32_e32 v81, 0x3fcc422a, v81
	v_mul_f32_e32 v80, 0xbfb8aa3b, v80
	v_mul_f32_e32 v81, 0xbfb8aa3b, v81
	v_exp_f32_e32 v80, v80
	v_exp_f32_e32 v81, v81
	s_nop 0
	v_pk_add_f32 v[80:81], v[80:81], 1.0 op_sel_hi:[1,0]
	s_nop 0
	v_div_scale_f32 v90, s[46:47], v81, v81, 1.0
	v_rcp_f32_e32 v91, v90
	s_nop 0
	v_fma_f32 v92, -v90, v91, 1.0
	v_fmac_f32_e32 v91, v92, v91
	v_div_scale_f32 v92, vcc, 1.0, v81, 1.0
	v_mul_f32_e32 v93, v92, v91
	v_fma_f32 v94, -v90, v93, v92
	v_fmac_f32_e32 v93, v94, v91
	v_fma_f32 v90, -v90, v93, v92
	v_div_fmas_f32 v90, v90, v91, v93
	v_div_fixup_f32 v81, v90, v81, 1.0
	v_div_scale_f32 v90, s[46:47], v80, v80, 1.0
	v_rcp_f32_e32 v91, v90
	s_nop 0
	v_fma_f32 v92, -v90, v91, 1.0
	v_fmac_f32_e32 v91, v92, v91
	v_div_scale_f32 v92, vcc, 1.0, v80, 1.0
	v_mul_f32_e32 v93, v92, v91
	v_fma_f32 v94, -v90, v93, v92
	v_fmac_f32_e32 v93, v94, v91
	v_fma_f32 v90, -v90, v93, v92
	v_div_fmas_f32 v90, v90, v91, v93
	v_div_fixup_f32 v80, v90, v80, 1.0
	v_pk_mul_f32 v[78:79], v[78:79], v[80:81]
	v_lshlrev_b32_e32 v80, 16, v82
	v_and_b32_e32 v81, 0xffff0000, v82
	v_pk_add_f32 v[72:73], v[72:73], v[80:81]
	s_nop 0
	v_mul_f32_e32 v80, 0x3d372713, v72
	v_mul_f32_e32 v81, 0x3d372713, v73
	v_mul_f32_e32 v80, v72, v80
	v_mul_f32_e32 v81, v73, v81
	v_fma_f32 v80, v72, v80, v72
	v_fma_f32 v81, v73, v81, v73
	v_mul_f32_e32 v80, 0x3fcc422a, v80
	v_mul_f32_e32 v81, 0x3fcc422a, v81
	v_mul_f32_e32 v80, 0xbfb8aa3b, v80
	v_mul_f32_e32 v81, 0xbfb8aa3b, v81
	v_exp_f32_e32 v80, v80
	v_exp_f32_e32 v81, v81
	s_nop 0
	v_pk_add_f32 v[80:81], v[80:81], 1.0 op_sel_hi:[1,0]
	s_nop 0
	v_div_scale_f32 v82, s[46:47], v81, v81, 1.0
	v_rcp_f32_e32 v90, v82
	s_nop 0
	v_fma_f32 v91, -v82, v90, 1.0
	v_fmac_f32_e32 v90, v91, v90
	v_div_scale_f32 v91, vcc, 1.0, v81, 1.0
	v_mul_f32_e32 v92, v91, v90
	v_fma_f32 v93, -v82, v92, v91
	v_fmac_f32_e32 v92, v93, v90
	v_fma_f32 v82, -v82, v92, v91
	v_div_fmas_f32 v82, v82, v90, v92
	v_div_fixup_f32 v81, v82, v81, 1.0
	v_div_scale_f32 v82, s[46:47], v80, v80, 1.0
	v_rcp_f32_e32 v90, v82
	s_nop 0
	v_fma_f32 v91, -v82, v90, 1.0
	v_fmac_f32_e32 v90, v91, v90
	v_div_scale_f32 v91, vcc, 1.0, v80, 1.0
	v_mul_f32_e32 v92, v91, v90
	v_fma_f32 v93, -v82, v92, v91
	v_fmac_f32_e32 v92, v93, v90
	v_fma_f32 v82, -v82, v92, v91
	v_div_fmas_f32 v82, v82, v90, v92
	v_div_fixup_f32 v80, v82, v80, 1.0
	v_pk_mul_f32 v[80:81], v[72:73], v[80:81]
	v_lshlrev_b32_e32 v72, 16, v83
	v_and_b32_e32 v73, 0xffff0000, v83
	v_pk_add_f32 v[72:73], v[74:75], v[72:73]
	s_nop 0
	v_mul_f32_e32 v74, 0x3d372713, v72
	v_mul_f32_e32 v75, 0x3d372713, v73
	v_mul_f32_e32 v74, v72, v74
	v_mul_f32_e32 v75, v73, v75
	v_fma_f32 v74, v72, v74, v72
	v_fma_f32 v75, v73, v75, v73
	v_mul_f32_e32 v74, 0x3fcc422a, v74
	v_mul_f32_e32 v75, 0x3fcc422a, v75
	v_mul_f32_e32 v74, 0xbfb8aa3b, v74
	v_mul_f32_e32 v75, 0xbfb8aa3b, v75
	v_exp_f32_e32 v74, v74
	v_exp_f32_e32 v75, v75
	s_nop 0
	v_pk_add_f32 v[74:75], v[74:75], 1.0 op_sel_hi:[1,0]
	s_nop 0
	v_div_scale_f32 v82, s[46:47], v75, v75, 1.0
	v_rcp_f32_e32 v83, v82
	s_nop 0
	v_fma_f32 v90, -v82, v83, 1.0
	v_fmac_f32_e32 v83, v90, v83
	v_div_scale_f32 v90, vcc, 1.0, v75, 1.0
	v_mul_f32_e32 v91, v90, v83
	v_fma_f32 v92, -v82, v91, v90
	v_fmac_f32_e32 v91, v92, v83
	v_fma_f32 v82, -v82, v91, v90
	v_div_fmas_f32 v82, v82, v83, v91
	v_div_fixup_f32 v75, v82, v75, 1.0
	v_div_scale_f32 v82, s[46:47], v74, v74, 1.0
	v_rcp_f32_e32 v83, v82
	s_nop 0
	v_fma_f32 v90, -v82, v83, 1.0
	v_fmac_f32_e32 v83, v90, v83
	v_div_scale_f32 v90, vcc, 1.0, v74, 1.0
	v_mul_f32_e32 v91, v90, v83
	v_fma_f32 v92, -v82, v91, v90
	v_fmac_f32_e32 v91, v92, v83
	v_fma_f32 v82, -v82, v91, v90
	v_div_fmas_f32 v82, v82, v83, v91
	v_div_fixup_f32 v74, v82, v74, 1.0
	v_pk_mul_f32 v[82:83], v[72:73], v[74:75]
	v_cvt_pk_bf16_f32 v72, v76, v77
	v_lshl_add_u64 v[76:77], s[36:37], 0, v[86:87]
	v_cvt_pk_bf16_f32 v73, v78, v79
	v_cvt_pk_bf16_f32 v74, v80, v81
	v_lshl_add_u64 v[80:81], v[76:77], 0, v[124:125]
	v_lshlrev_b64 v[78:79], 1, v[84:85]
	v_lshl_add_u64 v[80:81], v[80:81], 0, v[78:79]
	v_cvt_pk_bf16_f32 v75, v82, v83
	v_lshl_add_u64 v[80:81], v[80:81], 0, v[140:141]
	global_store_dwordx4 v[80:81], v[72:75], off
	s_nop 1
	s_waitcnt vmcnt(15)
; __device__ __forceinline__ float gelu_tanh(float x) { return x * sigmoidf_(1.5957691216057308f * (x + 0.044715f * x * x * x)); }
; __device__ __forceinline__ unsigned cvt_pk_bf16(float lo, float hi) { const f32x2c v = {lo, hi}; const bf16x2c b = __builtin_convertvector(v, bf16x2c); return __builtin_bit_cast(unsigned, b); }
;     __device__ __forceinline__ void operator()(const f32x4 (&acc)[2][2][4][2], const Unit& u, int wr, int wc, int fr, int fq) const {
;     ...
;             for (int m = 0; m < 4; ++m) { const int row = row0 + ai * HALF + m * 16; const int g = row / S5R, rl = row % S5R;
; #pragma unroll
;                 for (int bj = 0; bj < 2; ++bj) { const int col = col0 + bj * HALF;
;                     const u32x4 yi = *(const u32x4*)(YI + (size_t)row * 512 + col);
;                     const unsigned yw[4] = {yi.x, yi.y, yi.z, yi.w};
;                     const f32x4 v0 = acc[ai][bj][m][0], v1 = acc[ai][bj][m][1];
;                     float o[8];
; #pragma unroll
;                     for (int q = 0; q < 4; ++q) { const float al = (q < 2) ? v0[2 * q] : v1[2 * q - 4], ah = (q < 2) ? v0[2 * q + 1] : v1[2 * q - 3];
;                         o[2 * q] = gelu_tanh(al + __builtin_bit_cast(float, yw[q] << 16)); o[2 * q + 1] = gelu_tanh(ah + __builtin_bit_cast(float, yw[q] & 0xffff0000u)); }
;                     u32x4 w; w.x = cvt_pk_bf16(o[0], o[1]); w.y = cvt_pk_bf16(o[2], o[3]); w.z = cvt_pk_bf16(o[4], o[5]); w.w = cvt_pk_bf16(o[6], o[7]);
;                     const size_t tok = (size_t)rl * S5L + (col >> 4);
;                     *(u32x4*)(Z + tok * 512 + g * 16 + (col & 15)) = w; } }
	v_mov_b32_e32 v72, v198
	v_mov_b32_e32 v73, v199
	v_mov_b32_e32 v74, v200
	v_mov_b32_e32 v75, v201
	v_lshlrev_b32_e32 v80, 16, v72
	v_and_b32_e32 v81, 0xffff0000, v72
	v_pk_add_f32 v[68:69], v[68:69], v[80:81]
	s_nop 0
	v_mul_f32_e32 v72, 0x3d372713, v68
	v_mul_f32_e32 v72, v68, v72
	v_fma_f32 v72, v68, v72, v68
	v_mul_f32_e32 v72, 0x3fcc422a, v72
	v_mul_f32_e32 v72, 0xbfb8aa3b, v72
	v_exp_f32_e32 v80, v72
	v_mul_f32_e32 v72, 0x3d372713, v69
	v_mul_f32_e32 v72, v69, v72
	v_fma_f32 v72, v69, v72, v69
	v_mul_f32_e32 v72, 0x3fcc422a, v72
	v_mul_f32_e32 v72, 0xbfb8aa3b, v72
	v_exp_f32_e32 v81, v72
	s_nop 0
	v_pk_add_f32 v[80:81], v[80:81], 1.0 op_sel_hi:[1,0]
	s_nop 0
	v_div_scale_f32 v72, s[46:47], v81, v81, 1.0
	v_rcp_f32_e32 v82, v72
	s_nop 0
	v_fma_f32 v83, -v72, v82, 1.0
	v_fmac_f32_e32 v82, v83, v82
	v_div_scale_f32 v83, vcc, 1.0, v81, 1.0
	v_mul_f32_e32 v84, v83, v82
	v_fma_f32 v85, -v72, v84, v83
	v_fmac_f32_e32 v84, v85, v82
	v_fma_f32 v72, -v72, v84, v83
	v_div_fmas_f32 v72, v72, v82, v84
	v_div_fixup_f32 v81, v72, v81, 1.0
	v_div_scale_f32 v72, s[46:47], v80, v80, 1.0
	v_rcp_f32_e32 v82, v72
	s_nop 0
	v_fma_f32 v83, -v72, v82, 1.0
	v_fmac_f32_e32 v82, v83, v82
	v_div_scale_f32 v83, vcc, 1.0, v80, 1.0
	v_mul_f32_e32 v84, v83, v82
	v_fma_f32 v85, -v72, v84, v83
	v_fmac_f32_e32 v84, v85, v82
	v_fma_f32 v72, -v72, v84, v83
	v_div_fmas_f32 v72, v72, v82, v84
	v_div_fixup_f32 v80, v72, v80, 1.0
	v_lshlrev_b32_e32 v72, 16, v73
	v_and_b32_e32 v73, 0xffff0000, v73
	v_pk_add_f32 v[70:71], v[70:71], v[72:73]
	v_pk_mul_f32 v[68:69], v[68:69], v[80:81]
	v_mul_f32_e32 v72, 0x3d372713, v70
	v_mul_f32_e32 v73, 0x3d372713, v71
	v_mul_f32_e32 v72, v70, v72
	v_mul_f32_e32 v73, v71, v73
	v_fma_f32 v72, v70, v72, v70
	v_fma_f32 v73, v71, v73, v71
	v_mul_f32_e32 v72, 0x3fcc422a, v72
	v_mul_f32_e32 v73, 0x3fcc422a, v73
	v_mul_f32_e32 v72, 0xbfb8aa3b, v72
	v_mul_f32_e32 v73, 0xbfb8aa3b, v73
	v_exp_f32_e32 v72, v72
	v_exp_f32_e32 v73, v73
	s_nop 0
	v_pk_add_f32 v[72:73], v[72:73], 1.0 op_sel_hi:[1,0]
	s_nop 0
	v_div_scale_f32 v80, s[46:47], v73, v73, 1.0
	v_rcp_f32_e32 v81, v80
	s_nop 0
	v_fma_f32 v82, -v80, v81, 1.0
	v_fmac_f32_e32 v81, v82, v81
	v_div_scale_f32 v82, vcc, 1.0, v73, 1.0
	v_mul_f32_e32 v83, v82, v81
	v_fma_f32 v84, -v80, v83, v82
	v_fmac_f32_e32 v83, v84, v81
	v_fma_f32 v80, -v80, v83, v82
	v_div_fmas_f32 v80, v80, v81, v83
	v_div_fixup_f32 v73, v80, v73, 1.0
	v_div_scale_f32 v80, s[46:47], v72, v72, 1.0
	v_rcp_f32_e32 v81, v80
	s_nop 0
	v_fma_f32 v82, -v80, v81, 1.0
	v_fmac_f32_e32 v81, v82, v81
	v_div_scale_f32 v82, vcc, 1.0, v72, 1.0
	v_mul_f32_e32 v83, v82, v81
	v_fma_f32 v84, -v80, v83, v82
	v_fmac_f32_e32 v83, v84, v81
	v_fma_f32 v80, -v80, v83, v82
	v_div_fmas_f32 v80, v80, v81, v83
	v_div_fixup_f32 v72, v80, v72, 1.0
	v_pk_mul_f32 v[70:71], v[70:71], v[72:73]
	v_lshlrev_b32_e32 v72, 16, v74
	v_and_b32_e32 v73, 0xffff0000, v74
	v_pk_add_f32 v[64:65], v[64:65], v[72:73]
	s_nop 0
	v_mul_f32_e32 v72, 0x3d372713, v64
	v_mul_f32_e32 v73, 0x3d372713, v65
	v_mul_f32_e32 v72, v64, v72
	v_mul_f32_e32 v73, v65, v73
	v_fma_f32 v72, v64, v72, v64
	v_fma_f32 v73, v65, v73, v65
	v_mul_f32_e32 v72, 0x3fcc422a, v72
	v_mul_f32_e32 v73, 0x3fcc422a, v73
	v_mul_f32_e32 v72, 0xbfb8aa3b, v72
	v_mul_f32_e32 v73, 0xbfb8aa3b, v73
	v_exp_f32_e32 v72, v72
	v_exp_f32_e32 v73, v73
	s_nop 0
	v_pk_add_f32 v[72:73], v[72:73], 1.0 op_sel_hi:[1,0]
	s_nop 0
	v_div_scale_f32 v74, s[46:47], v73, v73, 1.0
	v_rcp_f32_e32 v80, v74
	s_nop 0
	v_fma_f32 v81, -v74, v80, 1.0
	v_fmac_f32_e32 v80, v81, v80
	v_div_scale_f32 v81, vcc, 1.0, v73, 1.0
	v_mul_f32_e32 v82, v81, v80
	v_fma_f32 v83, -v74, v82, v81
	v_fmac_f32_e32 v82, v83, v80
	v_fma_f32 v74, -v74, v82, v81
	v_div_fmas_f32 v74, v74, v80, v82
	v_div_fixup_f32 v73, v74, v73, 1.0
	v_div_scale_f32 v74, s[46:47], v72, v72, 1.0
	v_rcp_f32_e32 v80, v74
	s_nop 0
	v_fma_f32 v81, -v74, v80, 1.0
	v_fmac_f32_e32 v80, v81, v80
	v_div_scale_f32 v81, vcc, 1.0, v72, 1.0
	v_mul_f32_e32 v82, v81, v80
	v_fma_f32 v83, -v74, v82, v81
	v_fmac_f32_e32 v82, v83, v80
	v_fma_f32 v74, -v74, v82, v81
	v_div_fmas_f32 v74, v74, v80, v82
	v_div_fixup_f32 v72, v74, v72, 1.0
	v_pk_mul_f32 v[72:73], v[64:65], v[72:73]
	v_lshlrev_b32_e32 v64, 16, v75
	v_and_b32_e32 v65, 0xffff0000, v75
	v_pk_add_f32 v[64:65], v[66:67], v[64:65]
	s_nop 0
	v_mul_f32_e32 v66, 0x3d372713, v64
	v_mul_f32_e32 v67, 0x3d372713, v65
	v_mul_f32_e32 v66, v64, v66
	v_mul_f32_e32 v67, v65, v67
	v_fma_f32 v66, v64, v66, v64
	v_fma_f32 v67, v65, v67, v65
	v_mul_f32_e32 v66, 0x3fcc422a, v66
	v_mul_f32_e32 v67, 0x3fcc422a, v67
	v_mul_f32_e32 v66, 0xbfb8aa3b, v66
	v_mul_f32_e32 v67, 0xbfb8aa3b, v67
	v_exp_f32_e32 v66, v66
	v_exp_f32_e32 v67, v67
	s_nop 0
	v_pk_add_f32 v[66:67], v[66:67], 1.0 op_sel_hi:[1,0]
	s_nop 0
	v_div_scale_f32 v74, s[46:47], v67, v67, 1.0
	v_rcp_f32_e32 v75, v74
	s_nop 0
	v_fma_f32 v80, -v74, v75, 1.0
	v_fmac_f32_e32 v75, v80, v75
	v_div_scale_f32 v80, vcc, 1.0, v67, 1.0
	v_mul_f32_e32 v81, v80, v75
	v_fma_f32 v82, -v74, v81, v80
	v_fmac_f32_e32 v81, v82, v75
	v_fma_f32 v74, -v74, v81, v80
	v_div_fmas_f32 v74, v74, v75, v81
	v_div_fixup_f32 v67, v74, v67, 1.0
	v_div_scale_f32 v74, s[46:47], v66, v66, 1.0
	v_rcp_f32_e32 v75, v74
	s_nop 0
	v_fma_f32 v80, -v74, v75, 1.0
	v_fmac_f32_e32 v75, v80, v75
	v_div_scale_f32 v80, vcc, 1.0, v66, 1.0
	v_mul_f32_e32 v81, v80, v75
	v_fma_f32 v82, -v74, v81, v80
	v_fmac_f32_e32 v81, v82, v75
	v_fma_f32 v74, -v74, v81, v80
	v_div_fmas_f32 v74, v74, v75, v81
	v_div_fixup_f32 v66, v74, v66, 1.0
	v_pk_mul_f32 v[74:75], v[64:65], v[66:67]
	v_cvt_pk_bf16_f32 v64, v68, v69
	v_lshl_add_u64 v[68:69], v[76:77], 0, v[116:117]
	v_lshl_add_u64 v[68:69], v[68:69], 0, v[78:79]
	v_cvt_pk_bf16_f32 v65, v70, v71
	v_cvt_pk_bf16_f32 v66, v72, v73
	v_cvt_pk_bf16_f32 v67, v74, v75
	v_lshl_add_u64 v[68:69], v[68:69], 0, v[140:141]
	global_store_dwordx4 v[68:69], v[64:67], off
	s_nop 1
	v_add_u32_e32 v64, 0x80, v142
	v_ashrrev_i32_e32 v65, 31, v64
	v_lshrrev_b32_e32 v66, 21, v65
	v_add_u32_e32 v66, v64, v66
	v_ashrrev_i32_e32 v68, 11, v66
	v_mul_i32_i24_e32 v66, 0x800, v68
	v_sub_u32_e32 v66, v64, v66
	v_lshlrev_b64 v[64:65], 10, v[64:65]
	v_lshl_add_u64 v[64:65], s[30:31], 0, v[64:65]
	v_ashrrev_i32_e32 v67, 31, v66
	v_lshl_add_u64 v[72:73], v[64:65], 0, v[144:145]
	v_lshlrev_b64 v[70:71], 15, v[66:67]
	s_nop 1
	v_lshlrev_b32_e32 v68, 4, v68
	v_ashrrev_i32_e32 v69, 31, v68
	s_waitcnt vmcnt(15)
; __device__ __forceinline__ float gelu_tanh(float x) { return x * sigmoidf_(1.5957691216057308f * (x + 0.044715f * x * x * x)); }
; __device__ __forceinline__ unsigned cvt_pk_bf16(float lo, float hi) { const f32x2c v = {lo, hi}; const bf16x2c b = __builtin_convertvector(v, bf16x2c); return __builtin_bit_cast(unsigned, b); }
;     __device__ __forceinline__ void operator()(const f32x4 (&acc)[2][2][4][2], const Unit& u, int wr, int wc, int fr, int fq) const {
;     ...
;             for (int m = 0; m < 4; ++m) { const int row = row0 + ai * HALF + m * 16; const int g = row / S5R, rl = row % S5R;
; #pragma unroll
;                 for (int bj = 0; bj < 2; ++bj) { const int col = col0 + bj * HALF;
;                     const u32x4 yi = *(const u32x4*)(YI + (size_t)row * 512 + col);
;                     const unsigned yw[4] = {yi.x, yi.y, yi.z, yi.w};
;                     const f32x4 v0 = acc[ai][bj][m][0], v1 = acc[ai][bj][m][1];
;                     float o[8];
; #pragma unroll
;                     for (int q = 0; q < 4; ++q) { const float al = (q < 2) ? v0[2 * q] : v1[2 * q - 4], ah = (q < 2) ? v0[2 * q + 1] : v1[2 * q - 3];
;                         o[2 * q] = gelu_tanh(al + __builtin_bit_cast(float, yw[q] << 16)); o[2 * q + 1] = gelu_tanh(ah + __builtin_bit_cast(float, yw[q] & 0xffff0000u)); }
;                     u32x4 w; w.x = cvt_pk_bf16(o[0], o[1]); w.y = cvt_pk_bf16(o[2], o[3]); w.z = cvt_pk_bf16(o[4], o[5]); w.w = cvt_pk_bf16(o[6], o[7]);
;                     const size_t tok = (size_t)rl * S5L + (col >> 4);
;                     *(u32x4*)(Z + tok * 512 + g * 16 + (col & 15)) = w; } }
	v_mov_b32_e32 v64, v202
	v_mov_b32_e32 v65, v203
	v_mov_b32_e32 v66, v204
	v_mov_b32_e32 v67, v205
	v_lshlrev_b32_e32 v74, 16, v64
	v_and_b32_e32 v75, 0xffff0000, v64
	v_pk_add_f32 v[60:61], v[60:61], v[74:75]
	s_nop 0
	v_mul_f32_e32 v64, 0x3d372713, v60
	v_mul_f32_e32 v64, v60, v64
	v_fma_f32 v64, v60, v64, v60
	v_mul_f32_e32 v64, 0x3fcc422a, v64
	v_mul_f32_e32 v64, 0xbfb8aa3b, v64
	v_exp_f32_e32 v74, v64
	v_mul_f32_e32 v64, 0x3d372713, v61
	v_mul_f32_e32 v64, v61, v64
	v_fma_f32 v64, v61, v64, v61
	v_mul_f32_e32 v64, 0x3fcc422a, v64
	v_mul_f32_e32 v64, 0xbfb8aa3b, v64
	v_exp_f32_e32 v75, v64
	s_nop 0
	v_pk_add_f32 v[74:75], v[74:75], 1.0 op_sel_hi:[1,0]
	s_nop 0
	v_div_scale_f32 v64, s[46:47], v75, v75, 1.0
	v_rcp_f32_e32 v76, v64
	s_nop 0
	v_fma_f32 v77, -v64, v76, 1.0
	v_fmac_f32_e32 v76, v77, v76
	v_div_scale_f32 v77, vcc, 1.0, v75, 1.0
	v_mul_f32_e32 v78, v77, v76
	v_fma_f32 v79, -v64, v78, v77
	v_fmac_f32_e32 v78, v79, v76
	v_fma_f32 v64, -v64, v78, v77
	v_div_fmas_f32 v64, v64, v76, v78
	v_div_fixup_f32 v75, v64, v75, 1.0
	v_div_scale_f32 v64, s[46:47], v74, v74, 1.0
	v_rcp_f32_e32 v76, v64
	s_nop 0
	v_fma_f32 v77, -v64, v76, 1.0
	v_fmac_f32_e32 v76, v77, v76
	v_div_scale_f32 v77, vcc, 1.0, v74, 1.0
	v_mul_f32_e32 v78, v77, v76
	v_fma_f32 v79, -v64, v78, v77
	v_fmac_f32_e32 v78, v79, v76
	v_fma_f32 v64, -v64, v78, v77
	v_div_fmas_f32 v64, v64, v76, v78
	v_div_fixup_f32 v74, v64, v74, 1.0
	v_lshlrev_b32_e32 v64, 16, v65
	v_and_b32_e32 v65, 0xffff0000, v65
	v_pk_add_f32 v[62:63], v[62:63], v[64:65]
	v_pk_mul_f32 v[60:61], v[60:61], v[74:75]
	v_mul_f32_e32 v64, 0x3d372713, v62
	v_mul_f32_e32 v65, 0x3d372713, v63
	v_mul_f32_e32 v64, v62, v64
	v_mul_f32_e32 v65, v63, v65
	v_fma_f32 v64, v62, v64, v62
	v_fma_f32 v65, v63, v65, v63
	v_mul_f32_e32 v64, 0x3fcc422a, v64
	v_mul_f32_e32 v65, 0x3fcc422a, v65
	v_mul_f32_e32 v64, 0xbfb8aa3b, v64
	v_mul_f32_e32 v65, 0xbfb8aa3b, v65
	v_exp_f32_e32 v64, v64
	v_exp_f32_e32 v65, v65
	s_nop 0
	v_pk_add_f32 v[64:65], v[64:65], 1.0 op_sel_hi:[1,0]
	s_nop 0
	v_div_scale_f32 v74, s[46:47], v65, v65, 1.0
	v_rcp_f32_e32 v75, v74
	s_nop 0
	v_fma_f32 v76, -v74, v75, 1.0
	v_fmac_f32_e32 v75, v76, v75
	v_div_scale_f32 v76, vcc, 1.0, v65, 1.0
	v_mul_f32_e32 v77, v76, v75
	v_fma_f32 v78, -v74, v77, v76
	v_fmac_f32_e32 v77, v78, v75
	v_fma_f32 v74, -v74, v77, v76
	v_div_fmas_f32 v74, v74, v75, v77
	v_div_fixup_f32 v65, v74, v65, 1.0
	v_div_scale_f32 v74, s[46:47], v64, v64, 1.0
	v_rcp_f32_e32 v75, v74
	s_nop 0
	v_fma_f32 v76, -v74, v75, 1.0
	v_fmac_f32_e32 v75, v76, v75
	v_div_scale_f32 v76, vcc, 1.0, v64, 1.0
	v_mul_f32_e32 v77, v76, v75
	v_fma_f32 v78, -v74, v77, v76
	v_fmac_f32_e32 v77, v78, v75
	v_fma_f32 v74, -v74, v77, v76
	v_div_fmas_f32 v74, v74, v75, v77
	v_div_fixup_f32 v64, v74, v64, 1.0
	v_pk_mul_f32 v[62:63], v[62:63], v[64:65]
	v_lshlrev_b32_e32 v64, 16, v66
	v_and_b32_e32 v65, 0xffff0000, v66
	v_pk_add_f32 v[56:57], v[56:57], v[64:65]
	s_nop 0
	v_mul_f32_e32 v64, 0x3d372713, v56
	v_mul_f32_e32 v65, 0x3d372713, v57
	v_mul_f32_e32 v64, v56, v64
	v_mul_f32_e32 v65, v57, v65
	v_fma_f32 v64, v56, v64, v56
	v_fma_f32 v65, v57, v65, v57
	v_mul_f32_e32 v64, 0x3fcc422a, v64
	v_mul_f32_e32 v65, 0x3fcc422a, v65
	v_mul_f32_e32 v64, 0xbfb8aa3b, v64
	v_mul_f32_e32 v65, 0xbfb8aa3b, v65
	v_exp_f32_e32 v64, v64
	v_exp_f32_e32 v65, v65
	s_nop 0
	v_pk_add_f32 v[64:65], v[64:65], 1.0 op_sel_hi:[1,0]
	s_nop 0
	v_div_scale_f32 v66, s[46:47], v65, v65, 1.0
	v_rcp_f32_e32 v74, v66
	s_nop 0
	v_fma_f32 v75, -v66, v74, 1.0
	v_fmac_f32_e32 v74, v75, v74
	v_div_scale_f32 v75, vcc, 1.0, v65, 1.0
	v_mul_f32_e32 v76, v75, v74
	v_fma_f32 v77, -v66, v76, v75
	v_fmac_f32_e32 v76, v77, v74
	v_fma_f32 v66, -v66, v76, v75
	v_div_fmas_f32 v66, v66, v74, v76
	v_div_fixup_f32 v65, v66, v65, 1.0
	v_div_scale_f32 v66, s[46:47], v64, v64, 1.0
	v_rcp_f32_e32 v74, v66
	s_nop 0
	v_fma_f32 v75, -v66, v74, 1.0
	v_fmac_f32_e32 v74, v75, v74
	v_div_scale_f32 v75, vcc, 1.0, v64, 1.0
	v_mul_f32_e32 v76, v75, v74
	v_fma_f32 v77, -v66, v76, v75
	v_fmac_f32_e32 v76, v77, v74
	v_fma_f32 v66, -v66, v76, v75
	v_div_fmas_f32 v66, v66, v74, v76
	v_div_fixup_f32 v64, v66, v64, 1.0
	v_pk_mul_f32 v[64:65], v[56:57], v[64:65]
	v_lshlrev_b32_e32 v56, 16, v67
	v_and_b32_e32 v57, 0xffff0000, v67
	v_pk_add_f32 v[56:57], v[58:59], v[56:57]
	s_nop 0
	v_mul_f32_e32 v58, 0x3d372713, v56
	v_mul_f32_e32 v59, 0x3d372713, v57
	v_mul_f32_e32 v58, v56, v58
	v_mul_f32_e32 v59, v57, v59
	v_fma_f32 v58, v56, v58, v56
	v_fma_f32 v59, v57, v59, v57
	v_mul_f32_e32 v58, 0x3fcc422a, v58
	v_mul_f32_e32 v59, 0x3fcc422a, v59
	v_mul_f32_e32 v58, 0xbfb8aa3b, v58
	v_mul_f32_e32 v59, 0xbfb8aa3b, v59
	v_exp_f32_e32 v58, v58
	v_exp_f32_e32 v59, v59
	s_nop 0
	v_pk_add_f32 v[58:59], v[58:59], 1.0 op_sel_hi:[1,0]
	s_nop 0
	v_div_scale_f32 v66, s[46:47], v59, v59, 1.0
	v_rcp_f32_e32 v67, v66
	s_nop 0
	v_fma_f32 v74, -v66, v67, 1.0
	v_fmac_f32_e32 v67, v74, v67
	v_div_scale_f32 v74, vcc, 1.0, v59, 1.0
	v_mul_f32_e32 v75, v74, v67
	v_fma_f32 v76, -v66, v75, v74
	v_fmac_f32_e32 v75, v76, v67
	v_fma_f32 v66, -v66, v75, v74
	v_div_fmas_f32 v66, v66, v67, v75
	v_div_fixup_f32 v59, v66, v59, 1.0
	v_div_scale_f32 v66, s[46:47], v58, v58, 1.0
	v_rcp_f32_e32 v67, v66
	s_nop 0
	v_fma_f32 v74, -v66, v67, 1.0
	v_fmac_f32_e32 v67, v74, v67
	v_div_scale_f32 v74, vcc, 1.0, v58, 1.0
	v_mul_f32_e32 v75, v74, v67
	v_fma_f32 v76, -v66, v75, v74
	v_fmac_f32_e32 v75, v76, v67
	v_fma_f32 v66, -v66, v75, v74
	v_div_fmas_f32 v66, v66, v67, v75
	v_div_fixup_f32 v58, v66, v58, 1.0
	v_pk_mul_f32 v[66:67], v[56:57], v[58:59]
	v_cvt_pk_bf16_f32 v56, v60, v61
	v_lshl_add_u64 v[60:61], s[36:37], 0, v[70:71]
	v_cvt_pk_bf16_f32 v57, v62, v63
	v_cvt_pk_bf16_f32 v58, v64, v65
	v_lshl_add_u64 v[64:65], v[60:61], 0, v[124:125]
	v_lshlrev_b64 v[62:63], 1, v[68:69]
	v_lshl_add_u64 v[64:65], v[64:65], 0, v[62:63]
	v_cvt_pk_bf16_f32 v59, v66, v67
	v_lshl_add_u64 v[64:65], v[64:65], 0, v[140:141]
	global_store_dwordx4 v[64:65], v[56:59], off
	s_nop 1
	s_waitcnt vmcnt(15)
; __device__ __forceinline__ float gelu_tanh(float x) { return x * sigmoidf_(1.5957691216057308f * (x + 0.044715f * x * x * x)); }
; __device__ __forceinline__ unsigned cvt_pk_bf16(float lo, float hi) { const f32x2c v = {lo, hi}; const bf16x2c b = __builtin_convertvector(v, bf16x2c); return __builtin_bit_cast(unsigned, b); }
;     __device__ __forceinline__ void operator()(const f32x4 (&acc)[2][2][4][2], const Unit& u, int wr, int wc, int fr, int fq) const {
;     ...
;             for (int m = 0; m < 4; ++m) { const int row = row0 + ai * HALF + m * 16; const int g = row / S5R, rl = row % S5R;
; #pragma unroll
;                 for (int bj = 0; bj < 2; ++bj) { const int col = col0 + bj * HALF;
;                     const u32x4 yi = *(const u32x4*)(YI + (size_t)row * 512 + col);
;                     const unsigned yw[4] = {yi.x, yi.y, yi.z, yi.w};
;                     const f32x4 v0 = acc[ai][bj][m][0], v1 = acc[ai][bj][m][1];
;                     float o[8];
; #pragma unroll
;                     for (int q = 0; q < 4; ++q) { const float al = (q < 2) ? v0[2 * q] : v1[2 * q - 4], ah = (q < 2) ? v0[2 * q + 1] : v1[2 * q - 3];
;                         o[2 * q] = gelu_tanh(al + __builtin_bit_cast(float, yw[q] << 16)); o[2 * q + 1] = gelu_tanh(ah + __builtin_bit_cast(float, yw[q] & 0xffff0000u)); }
;                     u32x4 w; w.x = cvt_pk_bf16(o[0], o[1]); w.y = cvt_pk_bf16(o[2], o[3]); w.z = cvt_pk_bf16(o[4], o[5]); w.w = cvt_pk_bf16(o[6], o[7]);
;                     const size_t tok = (size_t)rl * S5L + (col >> 4);
;                     *(u32x4*)(Z + tok * 512 + g * 16 + (col & 15)) = w; } }
	v_mov_b32_e32 v56, v170
	v_mov_b32_e32 v57, v171
	v_mov_b32_e32 v58, v172
	v_mov_b32_e32 v59, v173
	v_lshlrev_b32_e32 v64, 16, v56
	v_and_b32_e32 v65, 0xffff0000, v56
	v_pk_add_f32 v[52:53], v[52:53], v[64:65]
	s_nop 0
	v_mul_f32_e32 v56, 0x3d372713, v52
	v_mul_f32_e32 v56, v52, v56
	v_fma_f32 v56, v52, v56, v52
	v_mul_f32_e32 v56, 0x3fcc422a, v56
	v_mul_f32_e32 v56, 0xbfb8aa3b, v56
	v_exp_f32_e32 v64, v56
	v_mul_f32_e32 v56, 0x3d372713, v53
	v_mul_f32_e32 v56, v53, v56
	v_fma_f32 v56, v53, v56, v53
	v_mul_f32_e32 v56, 0x3fcc422a, v56
	v_mul_f32_e32 v56, 0xbfb8aa3b, v56
	v_exp_f32_e32 v65, v56
	s_nop 0
	v_pk_add_f32 v[64:65], v[64:65], 1.0 op_sel_hi:[1,0]
	s_nop 0
	v_div_scale_f32 v56, s[46:47], v65, v65, 1.0
	v_rcp_f32_e32 v66, v56
	s_nop 0
	v_fma_f32 v67, -v56, v66, 1.0
	v_fmac_f32_e32 v66, v67, v66
	v_div_scale_f32 v67, vcc, 1.0, v65, 1.0
	v_mul_f32_e32 v68, v67, v66
	v_fma_f32 v69, -v56, v68, v67
	v_fmac_f32_e32 v68, v69, v66
	v_fma_f32 v56, -v56, v68, v67
	v_div_fmas_f32 v56, v56, v66, v68
	v_div_fixup_f32 v65, v56, v65, 1.0
	v_div_scale_f32 v56, s[46:47], v64, v64, 1.0
	v_rcp_f32_e32 v66, v56
	s_nop 0
	v_fma_f32 v67, -v56, v66, 1.0
	v_fmac_f32_e32 v66, v67, v66
	v_div_scale_f32 v67, vcc, 1.0, v64, 1.0
	v_mul_f32_e32 v68, v67, v66
	v_fma_f32 v69, -v56, v68, v67
	v_fmac_f32_e32 v68, v69, v66
	v_fma_f32 v56, -v56, v68, v67
	v_div_fmas_f32 v56, v56, v66, v68
	v_div_fixup_f32 v64, v56, v64, 1.0
	v_lshlrev_b32_e32 v56, 16, v57
	v_and_b32_e32 v57, 0xffff0000, v57
	v_pk_add_f32 v[54:55], v[54:55], v[56:57]
	v_pk_mul_f32 v[52:53], v[52:53], v[64:65]
	v_mul_f32_e32 v56, 0x3d372713, v54
	v_mul_f32_e32 v57, 0x3d372713, v55
	v_mul_f32_e32 v56, v54, v56
	v_mul_f32_e32 v57, v55, v57
	v_fma_f32 v56, v54, v56, v54
	v_fma_f32 v57, v55, v57, v55
	v_mul_f32_e32 v56, 0x3fcc422a, v56
	v_mul_f32_e32 v57, 0x3fcc422a, v57
	v_mul_f32_e32 v56, 0xbfb8aa3b, v56
	v_mul_f32_e32 v57, 0xbfb8aa3b, v57
	v_exp_f32_e32 v56, v56
	v_exp_f32_e32 v57, v57
	s_nop 0
	v_pk_add_f32 v[56:57], v[56:57], 1.0 op_sel_hi:[1,0]
	s_nop 0
	v_div_scale_f32 v64, s[46:47], v57, v57, 1.0
	v_rcp_f32_e32 v65, v64
	s_nop 0
	v_fma_f32 v66, -v64, v65, 1.0
	v_fmac_f32_e32 v65, v66, v65
	v_div_scale_f32 v66, vcc, 1.0, v57, 1.0
	v_mul_f32_e32 v67, v66, v65
	v_fma_f32 v68, -v64, v67, v66
	v_fmac_f32_e32 v67, v68, v65
	v_fma_f32 v64, -v64, v67, v66
	v_div_fmas_f32 v64, v64, v65, v67
	v_div_fixup_f32 v57, v64, v57, 1.0
	v_div_scale_f32 v64, s[46:47], v56, v56, 1.0
	v_rcp_f32_e32 v65, v64
	s_nop 0
	v_fma_f32 v66, -v64, v65, 1.0
	v_fmac_f32_e32 v65, v66, v65
	v_div_scale_f32 v66, vcc, 1.0, v56, 1.0
	v_mul_f32_e32 v67, v66, v65
	v_fma_f32 v68, -v64, v67, v66
	v_fmac_f32_e32 v67, v68, v65
	v_fma_f32 v64, -v64, v67, v66
	v_div_fmas_f32 v64, v64, v65, v67
	v_div_fixup_f32 v56, v64, v56, 1.0
	v_pk_mul_f32 v[54:55], v[54:55], v[56:57]
	v_lshlrev_b32_e32 v56, 16, v58
	v_and_b32_e32 v57, 0xffff0000, v58
	v_pk_add_f32 v[48:49], v[48:49], v[56:57]
	s_nop 0
	v_mul_f32_e32 v56, 0x3d372713, v48
	v_mul_f32_e32 v57, 0x3d372713, v49
	v_mul_f32_e32 v56, v48, v56
	v_mul_f32_e32 v57, v49, v57
	v_fma_f32 v56, v48, v56, v48
	v_fma_f32 v57, v49, v57, v49
	v_mul_f32_e32 v56, 0x3fcc422a, v56
	v_mul_f32_e32 v57, 0x3fcc422a, v57
	v_mul_f32_e32 v56, 0xbfb8aa3b, v56
	v_mul_f32_e32 v57, 0xbfb8aa3b, v57
	v_exp_f32_e32 v56, v56
	v_exp_f32_e32 v57, v57
	s_nop 0
	v_pk_add_f32 v[56:57], v[56:57], 1.0 op_sel_hi:[1,0]
	s_nop 0
	v_div_scale_f32 v58, s[46:47], v57, v57, 1.0
	v_rcp_f32_e32 v64, v58
	s_nop 0
	v_fma_f32 v65, -v58, v64, 1.0
	v_fmac_f32_e32 v64, v65, v64
	v_div_scale_f32 v65, vcc, 1.0, v57, 1.0
	v_mul_f32_e32 v66, v65, v64
	v_fma_f32 v67, -v58, v66, v65
	v_fmac_f32_e32 v66, v67, v64
	v_fma_f32 v58, -v58, v66, v65
	v_div_fmas_f32 v58, v58, v64, v66
	v_div_fixup_f32 v57, v58, v57, 1.0
	v_div_scale_f32 v58, s[46:47], v56, v56, 1.0
	v_rcp_f32_e32 v64, v58
	s_nop 0
	v_fma_f32 v65, -v58, v64, 1.0
	v_fmac_f32_e32 v64, v65, v64
	v_div_scale_f32 v65, vcc, 1.0, v56, 1.0
	v_mul_f32_e32 v66, v65, v64
	v_fma_f32 v67, -v58, v66, v65
	v_fmac_f32_e32 v66, v67, v64
	v_fma_f32 v58, -v58, v66, v65
	v_div_fmas_f32 v58, v58, v64, v66
	v_div_fixup_f32 v56, v58, v56, 1.0
	v_pk_mul_f32 v[56:57], v[48:49], v[56:57]
	v_lshlrev_b32_e32 v48, 16, v59
	v_and_b32_e32 v49, 0xffff0000, v59
	v_pk_add_f32 v[48:49], v[50:51], v[48:49]
	s_nop 0
	v_mul_f32_e32 v50, 0x3d372713, v48
	v_mul_f32_e32 v51, 0x3d372713, v49
	v_mul_f32_e32 v50, v48, v50
	v_mul_f32_e32 v51, v49, v51
	v_fma_f32 v50, v48, v50, v48
	v_fma_f32 v51, v49, v51, v49
	v_mul_f32_e32 v50, 0x3fcc422a, v50
	v_mul_f32_e32 v51, 0x3fcc422a, v51
	v_mul_f32_e32 v50, 0xbfb8aa3b, v50
	v_mul_f32_e32 v51, 0xbfb8aa3b, v51
	v_exp_f32_e32 v50, v50
	v_exp_f32_e32 v51, v51
	s_nop 0
	v_pk_add_f32 v[50:51], v[50:51], 1.0 op_sel_hi:[1,0]
	s_nop 0
	v_div_scale_f32 v58, s[46:47], v51, v51, 1.0
	v_rcp_f32_e32 v59, v58
	s_nop 0
	v_fma_f32 v64, -v58, v59, 1.0
	v_fmac_f32_e32 v59, v64, v59
	v_div_scale_f32 v64, vcc, 1.0, v51, 1.0
	v_mul_f32_e32 v65, v64, v59
	v_fma_f32 v66, -v58, v65, v64
	v_fmac_f32_e32 v65, v66, v59
	v_fma_f32 v58, -v58, v65, v64
	v_div_fmas_f32 v58, v58, v59, v65
	v_div_fixup_f32 v51, v58, v51, 1.0
	v_div_scale_f32 v58, s[46:47], v50, v50, 1.0
	v_rcp_f32_e32 v59, v58
	s_nop 0
	v_fma_f32 v64, -v58, v59, 1.0
	v_fmac_f32_e32 v59, v64, v59
	v_div_scale_f32 v64, vcc, 1.0, v50, 1.0
	v_mul_f32_e32 v65, v64, v59
	v_fma_f32 v66, -v58, v65, v64
	v_fmac_f32_e32 v65, v66, v59
	v_fma_f32 v58, -v58, v65, v64
	v_div_fmas_f32 v58, v58, v59, v65
	v_div_fixup_f32 v50, v58, v50, 1.0
	v_pk_mul_f32 v[58:59], v[48:49], v[50:51]
	v_cvt_pk_bf16_f32 v48, v52, v53
	v_lshl_add_u64 v[52:53], v[60:61], 0, v[116:117]
	v_lshl_add_u64 v[52:53], v[52:53], 0, v[62:63]
	v_cvt_pk_bf16_f32 v49, v54, v55
	v_cvt_pk_bf16_f32 v50, v56, v57
	v_cvt_pk_bf16_f32 v51, v58, v59
	v_lshl_add_u64 v[52:53], v[52:53], 0, v[140:141]
	global_store_dwordx4 v[52:53], v[48:51], off
	s_nop 1
	v_add_u32_e32 v48, 0x90, v142
	v_ashrrev_i32_e32 v49, 31, v48
	v_lshrrev_b32_e32 v50, 21, v49
	v_add_u32_e32 v50, v48, v50
	v_ashrrev_i32_e32 v52, 11, v50
	v_mul_i32_i24_e32 v50, 0x800, v52
	v_sub_u32_e32 v50, v48, v50
	v_lshlrev_b64 v[48:49], 10, v[48:49]
	v_lshl_add_u64 v[48:49], s[30:31], 0, v[48:49]
	v_ashrrev_i32_e32 v51, 31, v50
	v_lshl_add_u64 v[56:57], v[48:49], 0, v[144:145]
	v_lshlrev_b64 v[54:55], 15, v[50:51]
	s_nop 1
	v_lshlrev_b32_e32 v52, 4, v52
	v_ashrrev_i32_e32 v53, 31, v52
	s_waitcnt vmcnt(14)
; __device__ __forceinline__ float gelu_tanh(float x) { return x * sigmoidf_(1.5957691216057308f * (x + 0.044715f * x * x * x)); }
; __device__ __forceinline__ unsigned cvt_pk_bf16(float lo, float hi) { const f32x2c v = {lo, hi}; const bf16x2c b = __builtin_convertvector(v, bf16x2c); return __builtin_bit_cast(unsigned, b); }
;     __device__ __forceinline__ void operator()(const f32x4 (&acc)[2][2][4][2], const Unit& u, int wr, int wc, int fr, int fq) const {
;     ...
;             for (int m = 0; m < 4; ++m) { const int row = row0 + ai * HALF + m * 16; const int g = row / S5R, rl = row % S5R;
; #pragma unroll
;                 for (int bj = 0; bj < 2; ++bj) { const int col = col0 + bj * HALF;
;                     const u32x4 yi = *(const u32x4*)(YI + (size_t)row * 512 + col);
;                     const unsigned yw[4] = {yi.x, yi.y, yi.z, yi.w};
;                     const f32x4 v0 = acc[ai][bj][m][0], v1 = acc[ai][bj][m][1];
;                     float o[8];
; #pragma unroll
;                     for (int q = 0; q < 4; ++q) { const float al = (q < 2) ? v0[2 * q] : v1[2 * q - 4], ah = (q < 2) ? v0[2 * q + 1] : v1[2 * q - 3];
;                         o[2 * q] = gelu_tanh(al + __builtin_bit_cast(float, yw[q] << 16)); o[2 * q + 1] = gelu_tanh(ah + __builtin_bit_cast(float, yw[q] & 0xffff0000u)); }
;                     u32x4 w; w.x = cvt_pk_bf16(o[0], o[1]); w.y = cvt_pk_bf16(o[2], o[3]); w.z = cvt_pk_bf16(o[4], o[5]); w.w = cvt_pk_bf16(o[6], o[7]);
;                     const size_t tok = (size_t)rl * S5L + (col >> 4);
;                     *(u32x4*)(Z + tok * 512 + g * 16 + (col & 15)) = w; } }
	v_mov_b32_e32 v48, v174
	v_mov_b32_e32 v49, v175
	v_mov_b32_e32 v50, v176
	v_mov_b32_e32 v51, v177
	v_lshlrev_b32_e32 v58, 16, v48
	v_and_b32_e32 v59, 0xffff0000, v48
	v_pk_add_f32 v[44:45], v[44:45], v[58:59]
	s_nop 0
	v_mul_f32_e32 v48, 0x3d372713, v44
	v_mul_f32_e32 v48, v44, v48
	v_fma_f32 v48, v44, v48, v44
	v_mul_f32_e32 v48, 0x3fcc422a, v48
	v_mul_f32_e32 v48, 0xbfb8aa3b, v48
	v_exp_f32_e32 v58, v48
	v_mul_f32_e32 v48, 0x3d372713, v45
	v_mul_f32_e32 v48, v45, v48
	v_fma_f32 v48, v45, v48, v45
	v_mul_f32_e32 v48, 0x3fcc422a, v48
	v_mul_f32_e32 v48, 0xbfb8aa3b, v48
	v_exp_f32_e32 v59, v48
	s_nop 0
	v_pk_add_f32 v[58:59], v[58:59], 1.0 op_sel_hi:[1,0]
	s_nop 0
	v_div_scale_f32 v48, s[46:47], v59, v59, 1.0
	v_rcp_f32_e32 v60, v48
	s_nop 0
	v_fma_f32 v61, -v48, v60, 1.0
	v_fmac_f32_e32 v60, v61, v60
	v_div_scale_f32 v61, vcc, 1.0, v59, 1.0
	v_mul_f32_e32 v62, v61, v60
	v_fma_f32 v63, -v48, v62, v61
	v_fmac_f32_e32 v62, v63, v60
	v_fma_f32 v48, -v48, v62, v61
	v_div_fmas_f32 v48, v48, v60, v62
	v_div_fixup_f32 v59, v48, v59, 1.0
	v_div_scale_f32 v48, s[46:47], v58, v58, 1.0
	v_rcp_f32_e32 v60, v48
	s_nop 0
	v_fma_f32 v61, -v48, v60, 1.0
	v_fmac_f32_e32 v60, v61, v60
	v_div_scale_f32 v61, vcc, 1.0, v58, 1.0
	v_mul_f32_e32 v62, v61, v60
	v_fma_f32 v63, -v48, v62, v61
	v_fmac_f32_e32 v62, v63, v60
	v_fma_f32 v48, -v48, v62, v61
	v_div_fmas_f32 v48, v48, v60, v62
	v_div_fixup_f32 v58, v48, v58, 1.0
	v_lshlrev_b32_e32 v48, 16, v49
	v_and_b32_e32 v49, 0xffff0000, v49
	v_pk_add_f32 v[46:47], v[46:47], v[48:49]
	v_pk_mul_f32 v[44:45], v[44:45], v[58:59]
	v_mul_f32_e32 v48, 0x3d372713, v46
	v_mul_f32_e32 v49, 0x3d372713, v47
	v_mul_f32_e32 v48, v46, v48
	v_mul_f32_e32 v49, v47, v49
	v_fma_f32 v48, v46, v48, v46
	v_fma_f32 v49, v47, v49, v47
	v_mul_f32_e32 v48, 0x3fcc422a, v48
	v_mul_f32_e32 v49, 0x3fcc422a, v49
	v_mul_f32_e32 v48, 0xbfb8aa3b, v48
	v_mul_f32_e32 v49, 0xbfb8aa3b, v49
	v_exp_f32_e32 v48, v48
	v_exp_f32_e32 v49, v49
	s_nop 0
	v_pk_add_f32 v[48:49], v[48:49], 1.0 op_sel_hi:[1,0]
	s_nop 0
	v_div_scale_f32 v58, s[46:47], v49, v49, 1.0
	v_rcp_f32_e32 v59, v58
	s_nop 0
	v_fma_f32 v60, -v58, v59, 1.0
	v_fmac_f32_e32 v59, v60, v59
	v_div_scale_f32 v60, vcc, 1.0, v49, 1.0
	v_mul_f32_e32 v61, v60, v59
	v_fma_f32 v62, -v58, v61, v60
	v_fmac_f32_e32 v61, v62, v59
	v_fma_f32 v58, -v58, v61, v60
	v_div_fmas_f32 v58, v58, v59, v61
	v_div_fixup_f32 v49, v58, v49, 1.0
	v_div_scale_f32 v58, s[46:47], v48, v48, 1.0
	v_rcp_f32_e32 v59, v58
	s_nop 0
	v_fma_f32 v60, -v58, v59, 1.0
	v_fmac_f32_e32 v59, v60, v59
	v_div_scale_f32 v60, vcc, 1.0, v48, 1.0
	v_mul_f32_e32 v61, v60, v59
	v_fma_f32 v62, -v58, v61, v60
	v_fmac_f32_e32 v61, v62, v59
	v_fma_f32 v58, -v58, v61, v60
	v_div_fmas_f32 v58, v58, v59, v61
	v_div_fixup_f32 v48, v58, v48, 1.0
	v_pk_mul_f32 v[46:47], v[46:47], v[48:49]
	v_lshlrev_b32_e32 v48, 16, v50
	v_and_b32_e32 v49, 0xffff0000, v50
	v_pk_add_f32 v[40:41], v[40:41], v[48:49]
	s_nop 0
	v_mul_f32_e32 v48, 0x3d372713, v40
	v_mul_f32_e32 v49, 0x3d372713, v41
	v_mul_f32_e32 v48, v40, v48
	v_mul_f32_e32 v49, v41, v49
	v_fma_f32 v48, v40, v48, v40
	v_fma_f32 v49, v41, v49, v41
	v_mul_f32_e32 v48, 0x3fcc422a, v48
	v_mul_f32_e32 v49, 0x3fcc422a, v49
	v_mul_f32_e32 v48, 0xbfb8aa3b, v48
	v_mul_f32_e32 v49, 0xbfb8aa3b, v49
	v_exp_f32_e32 v48, v48
	v_exp_f32_e32 v49, v49
	s_nop 0
	v_pk_add_f32 v[48:49], v[48:49], 1.0 op_sel_hi:[1,0]
	s_nop 0
	v_div_scale_f32 v50, s[46:47], v49, v49, 1.0
	v_rcp_f32_e32 v58, v50
	s_nop 0
	v_fma_f32 v59, -v50, v58, 1.0
	v_fmac_f32_e32 v58, v59, v58
	v_div_scale_f32 v59, vcc, 1.0, v49, 1.0
	v_mul_f32_e32 v60, v59, v58
	v_fma_f32 v61, -v50, v60, v59
	v_fmac_f32_e32 v60, v61, v58
	v_fma_f32 v50, -v50, v60, v59
	v_div_fmas_f32 v50, v50, v58, v60
	v_div_fixup_f32 v49, v50, v49, 1.0
	v_div_scale_f32 v50, s[46:47], v48, v48, 1.0
	v_rcp_f32_e32 v58, v50
	s_nop 0
	v_fma_f32 v59, -v50, v58, 1.0
	v_fmac_f32_e32 v58, v59, v58
	v_div_scale_f32 v59, vcc, 1.0, v48, 1.0
	v_mul_f32_e32 v60, v59, v58
	v_fma_f32 v61, -v50, v60, v59
	v_fmac_f32_e32 v60, v61, v58
	v_fma_f32 v50, -v50, v60, v59
	v_div_fmas_f32 v50, v50, v58, v60
	v_div_fixup_f32 v48, v50, v48, 1.0
	v_pk_mul_f32 v[48:49], v[40:41], v[48:49]
	v_lshlrev_b32_e32 v40, 16, v51
	v_and_b32_e32 v41, 0xffff0000, v51
	v_pk_add_f32 v[40:41], v[42:43], v[40:41]
	s_nop 0
	v_mul_f32_e32 v42, 0x3d372713, v40
	v_mul_f32_e32 v43, 0x3d372713, v41
	v_mul_f32_e32 v42, v40, v42
	v_mul_f32_e32 v43, v41, v43
	v_fma_f32 v42, v40, v42, v40
	v_fma_f32 v43, v41, v43, v41
	v_mul_f32_e32 v42, 0x3fcc422a, v42
	v_mul_f32_e32 v43, 0x3fcc422a, v43
	v_mul_f32_e32 v42, 0xbfb8aa3b, v42
	v_mul_f32_e32 v43, 0xbfb8aa3b, v43
	v_exp_f32_e32 v42, v42
	v_exp_f32_e32 v43, v43
	s_nop 0
	v_pk_add_f32 v[42:43], v[42:43], 1.0 op_sel_hi:[1,0]
	s_nop 0
	v_div_scale_f32 v50, s[46:47], v43, v43, 1.0
	v_rcp_f32_e32 v51, v50
	s_nop 0
	v_fma_f32 v58, -v50, v51, 1.0
	v_fmac_f32_e32 v51, v58, v51
	v_div_scale_f32 v58, vcc, 1.0, v43, 1.0
	v_mul_f32_e32 v59, v58, v51
	v_fma_f32 v60, -v50, v59, v58
	v_fmac_f32_e32 v59, v60, v51
	v_fma_f32 v50, -v50, v59, v58
	v_div_fmas_f32 v50, v50, v51, v59
	v_div_fixup_f32 v43, v50, v43, 1.0
	v_div_scale_f32 v50, s[46:47], v42, v42, 1.0
	v_rcp_f32_e32 v51, v50
	s_nop 0
	v_fma_f32 v58, -v50, v51, 1.0
	v_fmac_f32_e32 v51, v58, v51
	v_div_scale_f32 v58, vcc, 1.0, v42, 1.0
	v_mul_f32_e32 v59, v58, v51
	v_fma_f32 v60, -v50, v59, v58
	v_fmac_f32_e32 v59, v60, v51
	v_fma_f32 v50, -v50, v59, v58
	v_div_fmas_f32 v50, v50, v51, v59
	v_div_fixup_f32 v42, v50, v42, 1.0
	v_pk_mul_f32 v[50:51], v[40:41], v[42:43]
	v_cvt_pk_bf16_f32 v40, v44, v45
	v_lshl_add_u64 v[44:45], s[36:37], 0, v[54:55]
	v_cvt_pk_bf16_f32 v41, v46, v47
	v_cvt_pk_bf16_f32 v42, v48, v49
	v_lshl_add_u64 v[48:49], v[44:45], 0, v[124:125]
	v_lshlrev_b64 v[46:47], 1, v[52:53]
	v_lshl_add_u64 v[48:49], v[48:49], 0, v[46:47]
	v_cvt_pk_bf16_f32 v43, v50, v51
	v_lshl_add_u64 v[48:49], v[48:49], 0, v[140:141]
	global_store_dwordx4 v[48:49], v[40:43], off
	s_nop 1
	s_waitcnt vmcnt(13)
; __device__ __forceinline__ float gelu_tanh(float x) { return x * sigmoidf_(1.5957691216057308f * (x + 0.044715f * x * x * x)); }
; __device__ __forceinline__ unsigned cvt_pk_bf16(float lo, float hi) { const f32x2c v = {lo, hi}; const bf16x2c b = __builtin_convertvector(v, bf16x2c); return __builtin_bit_cast(unsigned, b); }
;     __device__ __forceinline__ void operator()(const f32x4 (&acc)[2][2][4][2], const Unit& u, int wr, int wc, int fr, int fq) const {
;     ...
;             for (int m = 0; m < 4; ++m) { const int row = row0 + ai * HALF + m * 16; const int g = row / S5R, rl = row % S5R;
; #pragma unroll
;                 for (int bj = 0; bj < 2; ++bj) { const int col = col0 + bj * HALF;
;                     const u32x4 yi = *(const u32x4*)(YI + (size_t)row * 512 + col);
;                     const unsigned yw[4] = {yi.x, yi.y, yi.z, yi.w};
;                     const f32x4 v0 = acc[ai][bj][m][0], v1 = acc[ai][bj][m][1];
;                     float o[8];
; #pragma unroll
;                     for (int q = 0; q < 4; ++q) { const float al = (q < 2) ? v0[2 * q] : v1[2 * q - 4], ah = (q < 2) ? v0[2 * q + 1] : v1[2 * q - 3];
;                         o[2 * q] = gelu_tanh(al + __builtin_bit_cast(float, yw[q] << 16)); o[2 * q + 1] = gelu_tanh(ah + __builtin_bit_cast(float, yw[q] & 0xffff0000u)); }
;                     u32x4 w; w.x = cvt_pk_bf16(o[0], o[1]); w.y = cvt_pk_bf16(o[2], o[3]); w.z = cvt_pk_bf16(o[4], o[5]); w.w = cvt_pk_bf16(o[6], o[7]);
;                     const size_t tok = (size_t)rl * S5L + (col >> 4);
;                     *(u32x4*)(Z + tok * 512 + g * 16 + (col & 15)) = w; } }
	v_mov_b32_e32 v40, v178
	v_mov_b32_e32 v41, v179
	v_mov_b32_e32 v42, v180
	v_mov_b32_e32 v43, v181
	v_lshlrev_b32_e32 v48, 16, v40
	v_and_b32_e32 v49, 0xffff0000, v40
	v_pk_add_f32 v[36:37], v[36:37], v[48:49]
	s_nop 0
	v_mul_f32_e32 v40, 0x3d372713, v36
	v_mul_f32_e32 v40, v36, v40
	v_fma_f32 v40, v36, v40, v36
	v_mul_f32_e32 v40, 0x3fcc422a, v40
	v_mul_f32_e32 v40, 0xbfb8aa3b, v40
	v_exp_f32_e32 v48, v40
	v_mul_f32_e32 v40, 0x3d372713, v37
	v_mul_f32_e32 v40, v37, v40
	v_fma_f32 v40, v37, v40, v37
	v_mul_f32_e32 v40, 0x3fcc422a, v40
	v_mul_f32_e32 v40, 0xbfb8aa3b, v40
	v_exp_f32_e32 v49, v40
	s_nop 0
	v_pk_add_f32 v[48:49], v[48:49], 1.0 op_sel_hi:[1,0]
	s_nop 0
	v_div_scale_f32 v40, s[46:47], v49, v49, 1.0
	v_rcp_f32_e32 v50, v40
	s_nop 0
	v_fma_f32 v51, -v40, v50, 1.0
	v_fmac_f32_e32 v50, v51, v50
	v_div_scale_f32 v51, vcc, 1.0, v49, 1.0
	v_mul_f32_e32 v52, v51, v50
	v_fma_f32 v53, -v40, v52, v51
	v_fmac_f32_e32 v52, v53, v50
	v_fma_f32 v40, -v40, v52, v51
	v_div_fmas_f32 v40, v40, v50, v52
	v_div_fixup_f32 v49, v40, v49, 1.0
	v_div_scale_f32 v40, s[46:47], v48, v48, 1.0
	v_rcp_f32_e32 v50, v40
	s_nop 0
	v_fma_f32 v51, -v40, v50, 1.0
	v_fmac_f32_e32 v50, v51, v50
	v_div_scale_f32 v51, vcc, 1.0, v48, 1.0
	v_mul_f32_e32 v52, v51, v50
	v_fma_f32 v53, -v40, v52, v51
	v_fmac_f32_e32 v52, v53, v50
	v_fma_f32 v40, -v40, v52, v51
	v_div_fmas_f32 v40, v40, v50, v52
	v_div_fixup_f32 v48, v40, v48, 1.0
	v_lshlrev_b32_e32 v40, 16, v41
	v_and_b32_e32 v41, 0xffff0000, v41
	v_pk_add_f32 v[38:39], v[38:39], v[40:41]
	v_pk_mul_f32 v[36:37], v[36:37], v[48:49]
	v_mul_f32_e32 v40, 0x3d372713, v38
	v_mul_f32_e32 v41, 0x3d372713, v39
	v_mul_f32_e32 v40, v38, v40
	v_mul_f32_e32 v41, v39, v41
	v_fma_f32 v40, v38, v40, v38
	v_fma_f32 v41, v39, v41, v39
	v_mul_f32_e32 v40, 0x3fcc422a, v40
	v_mul_f32_e32 v41, 0x3fcc422a, v41
	v_mul_f32_e32 v40, 0xbfb8aa3b, v40
	v_mul_f32_e32 v41, 0xbfb8aa3b, v41
	v_exp_f32_e32 v40, v40
	v_exp_f32_e32 v41, v41
	s_nop 0
	v_pk_add_f32 v[40:41], v[40:41], 1.0 op_sel_hi:[1,0]
	s_nop 0
	v_div_scale_f32 v48, s[46:47], v41, v41, 1.0
	v_rcp_f32_e32 v49, v48
	s_nop 0
	v_fma_f32 v50, -v48, v49, 1.0
	v_fmac_f32_e32 v49, v50, v49
	v_div_scale_f32 v50, vcc, 1.0, v41, 1.0
	v_mul_f32_e32 v51, v50, v49
	v_fma_f32 v52, -v48, v51, v50
	v_fmac_f32_e32 v51, v52, v49
	v_fma_f32 v48, -v48, v51, v50
	v_div_fmas_f32 v48, v48, v49, v51
	v_div_fixup_f32 v41, v48, v41, 1.0
	v_div_scale_f32 v48, s[46:47], v40, v40, 1.0
	v_rcp_f32_e32 v49, v48
	s_nop 0
	v_fma_f32 v50, -v48, v49, 1.0
	v_fmac_f32_e32 v49, v50, v49
	v_div_scale_f32 v50, vcc, 1.0, v40, 1.0
	v_mul_f32_e32 v51, v50, v49
	v_fma_f32 v52, -v48, v51, v50
	v_fmac_f32_e32 v51, v52, v49
	v_fma_f32 v48, -v48, v51, v50
	v_div_fmas_f32 v48, v48, v49, v51
	v_div_fixup_f32 v40, v48, v40, 1.0
	v_pk_mul_f32 v[38:39], v[38:39], v[40:41]
	v_lshlrev_b32_e32 v40, 16, v42
	v_and_b32_e32 v41, 0xffff0000, v42
	v_pk_add_f32 v[32:33], v[32:33], v[40:41]
	s_nop 0
	v_mul_f32_e32 v40, 0x3d372713, v32
	v_mul_f32_e32 v41, 0x3d372713, v33
	v_mul_f32_e32 v40, v32, v40
	v_mul_f32_e32 v41, v33, v41
	v_fma_f32 v40, v32, v40, v32
	v_fma_f32 v41, v33, v41, v33
	v_mul_f32_e32 v40, 0x3fcc422a, v40
	v_mul_f32_e32 v41, 0x3fcc422a, v41
	v_mul_f32_e32 v40, 0xbfb8aa3b, v40
	v_mul_f32_e32 v41, 0xbfb8aa3b, v41
	v_exp_f32_e32 v40, v40
	v_exp_f32_e32 v41, v41
	s_nop 0
	v_pk_add_f32 v[40:41], v[40:41], 1.0 op_sel_hi:[1,0]
	s_nop 0
	v_div_scale_f32 v42, s[46:47], v41, v41, 1.0
	v_rcp_f32_e32 v48, v42
	s_nop 0
	v_fma_f32 v49, -v42, v48, 1.0
	v_fmac_f32_e32 v48, v49, v48
	v_div_scale_f32 v49, vcc, 1.0, v41, 1.0
	v_mul_f32_e32 v50, v49, v48
	v_fma_f32 v51, -v42, v50, v49
	v_fmac_f32_e32 v50, v51, v48
	v_fma_f32 v42, -v42, v50, v49
	v_div_fmas_f32 v42, v42, v48, v50
	v_div_fixup_f32 v41, v42, v41, 1.0
	v_div_scale_f32 v42, s[46:47], v40, v40, 1.0
	v_rcp_f32_e32 v48, v42
	s_nop 0
	v_fma_f32 v49, -v42, v48, 1.0
	v_fmac_f32_e32 v48, v49, v48
	v_div_scale_f32 v49, vcc, 1.0, v40, 1.0
	v_mul_f32_e32 v50, v49, v48
	v_fma_f32 v51, -v42, v50, v49
	v_fmac_f32_e32 v50, v51, v48
	v_fma_f32 v42, -v42, v50, v49
	v_div_fmas_f32 v42, v42, v48, v50
	v_div_fixup_f32 v40, v42, v40, 1.0
	v_pk_mul_f32 v[40:41], v[32:33], v[40:41]
	v_lshlrev_b32_e32 v32, 16, v43
	v_and_b32_e32 v33, 0xffff0000, v43
	v_pk_add_f32 v[32:33], v[34:35], v[32:33]
	s_nop 0
	v_mul_f32_e32 v34, 0x3d372713, v32
	v_mul_f32_e32 v35, 0x3d372713, v33
	v_mul_f32_e32 v34, v32, v34
	v_mul_f32_e32 v35, v33, v35
	v_fma_f32 v34, v32, v34, v32
	v_fma_f32 v35, v33, v35, v33
	v_mul_f32_e32 v34, 0x3fcc422a, v34
	v_mul_f32_e32 v35, 0x3fcc422a, v35
	v_mul_f32_e32 v34, 0xbfb8aa3b, v34
	v_mul_f32_e32 v35, 0xbfb8aa3b, v35
	v_exp_f32_e32 v34, v34
	v_exp_f32_e32 v35, v35
	s_nop 0
	v_pk_add_f32 v[34:35], v[34:35], 1.0 op_sel_hi:[1,0]
	s_nop 0
	v_div_scale_f32 v42, s[46:47], v35, v35, 1.0
	v_rcp_f32_e32 v43, v42
	s_nop 0
	v_fma_f32 v48, -v42, v43, 1.0
	v_fmac_f32_e32 v43, v48, v43
	v_div_scale_f32 v48, vcc, 1.0, v35, 1.0
	v_mul_f32_e32 v49, v48, v43
	v_fma_f32 v50, -v42, v49, v48
	v_fmac_f32_e32 v49, v50, v43
	v_fma_f32 v42, -v42, v49, v48
	v_div_fmas_f32 v42, v42, v43, v49
	v_div_fixup_f32 v35, v42, v35, 1.0
	v_div_scale_f32 v42, s[46:47], v34, v34, 1.0
	v_rcp_f32_e32 v43, v42
	s_nop 0
	v_fma_f32 v48, -v42, v43, 1.0
	v_fmac_f32_e32 v43, v48, v43
	v_div_scale_f32 v48, vcc, 1.0, v34, 1.0
	v_mul_f32_e32 v49, v48, v43
	v_fma_f32 v50, -v42, v49, v48
	v_fmac_f32_e32 v49, v50, v43
	v_fma_f32 v42, -v42, v49, v48
	v_div_fmas_f32 v42, v42, v43, v49
	v_div_fixup_f32 v34, v42, v34, 1.0
	v_pk_mul_f32 v[42:43], v[32:33], v[34:35]
	v_cvt_pk_bf16_f32 v32, v36, v37
	v_lshl_add_u64 v[36:37], v[44:45], 0, v[116:117]
	v_lshl_add_u64 v[36:37], v[36:37], 0, v[46:47]
	v_cvt_pk_bf16_f32 v33, v38, v39
	v_cvt_pk_bf16_f32 v34, v40, v41
	v_cvt_pk_bf16_f32 v35, v42, v43
	v_lshl_add_u64 v[36:37], v[36:37], 0, v[140:141]
	global_store_dwordx4 v[36:37], v[32:35], off
	s_nop 1
	v_add_u32_e32 v32, 0xa0, v142
	v_ashrrev_i32_e32 v33, 31, v32
	v_lshrrev_b32_e32 v34, 21, v33
	v_add_u32_e32 v34, v32, v34
	v_ashrrev_i32_e32 v36, 11, v34
	v_mul_i32_i24_e32 v34, 0x800, v36
	v_sub_u32_e32 v34, v32, v34
	v_lshlrev_b64 v[32:33], 10, v[32:33]
	v_lshl_add_u64 v[32:33], s[30:31], 0, v[32:33]
	v_ashrrev_i32_e32 v35, 31, v34
	v_lshl_add_u64 v[40:41], v[32:33], 0, v[144:145]
	v_lshlrev_b64 v[38:39], 15, v[34:35]
	s_nop 1
	v_lshlrev_b32_e32 v36, 4, v36
	v_ashrrev_i32_e32 v37, 31, v36
	s_waitcnt vmcnt(12)
; __device__ __forceinline__ float gelu_tanh(float x) { return x * sigmoidf_(1.5957691216057308f * (x + 0.044715f * x * x * x)); }
; __device__ __forceinline__ unsigned cvt_pk_bf16(float lo, float hi) { const f32x2c v = {lo, hi}; const bf16x2c b = __builtin_convertvector(v, bf16x2c); return __builtin_bit_cast(unsigned, b); }
;     __device__ __forceinline__ void operator()(const f32x4 (&acc)[2][2][4][2], const Unit& u, int wr, int wc, int fr, int fq) const {
;     ...
;             for (int m = 0; m < 4; ++m) { const int row = row0 + ai * HALF + m * 16; const int g = row / S5R, rl = row % S5R;
; #pragma unroll
;                 for (int bj = 0; bj < 2; ++bj) { const int col = col0 + bj * HALF;
;                     const u32x4 yi = *(const u32x4*)(YI + (size_t)row * 512 + col);
;                     const unsigned yw[4] = {yi.x, yi.y, yi.z, yi.w};
;                     const f32x4 v0 = acc[ai][bj][m][0], v1 = acc[ai][bj][m][1];
;                     float o[8];
; #pragma unroll
;                     for (int q = 0; q < 4; ++q) { const float al = (q < 2) ? v0[2 * q] : v1[2 * q - 4], ah = (q < 2) ? v0[2 * q + 1] : v1[2 * q - 3];
;                         o[2 * q] = gelu_tanh(al + __builtin_bit_cast(float, yw[q] << 16)); o[2 * q + 1] = gelu_tanh(ah + __builtin_bit_cast(float, yw[q] & 0xffff0000u)); }
;                     u32x4 w; w.x = cvt_pk_bf16(o[0], o[1]); w.y = cvt_pk_bf16(o[2], o[3]); w.z = cvt_pk_bf16(o[4], o[5]); w.w = cvt_pk_bf16(o[6], o[7]);
;                     const size_t tok = (size_t)rl * S5L + (col >> 4);
;                     *(u32x4*)(Z + tok * 512 + g * 16 + (col & 15)) = w; } }
	v_mov_b32_e32 v32, v182
	v_mov_b32_e32 v33, v183
	v_mov_b32_e32 v34, v184
	v_mov_b32_e32 v35, v185
	v_lshlrev_b32_e32 v42, 16, v32
	v_and_b32_e32 v43, 0xffff0000, v32
	v_pk_add_f32 v[28:29], v[28:29], v[42:43]
	s_nop 0
	v_mul_f32_e32 v32, 0x3d372713, v28
	v_mul_f32_e32 v32, v28, v32
	v_fma_f32 v32, v28, v32, v28
	v_mul_f32_e32 v32, 0x3fcc422a, v32
	v_mul_f32_e32 v32, 0xbfb8aa3b, v32
	v_exp_f32_e32 v42, v32
	v_mul_f32_e32 v32, 0x3d372713, v29
	v_mul_f32_e32 v32, v29, v32
	v_fma_f32 v32, v29, v32, v29
	v_mul_f32_e32 v32, 0x3fcc422a, v32
	v_mul_f32_e32 v32, 0xbfb8aa3b, v32
	v_exp_f32_e32 v43, v32
	s_nop 0
	v_pk_add_f32 v[42:43], v[42:43], 1.0 op_sel_hi:[1,0]
	s_nop 0
	v_div_scale_f32 v32, s[46:47], v43, v43, 1.0
	v_rcp_f32_e32 v44, v32
	s_nop 0
	v_fma_f32 v45, -v32, v44, 1.0
	v_fmac_f32_e32 v44, v45, v44
	v_div_scale_f32 v45, vcc, 1.0, v43, 1.0
	v_mul_f32_e32 v46, v45, v44
	v_fma_f32 v47, -v32, v46, v45
	v_fmac_f32_e32 v46, v47, v44
	v_fma_f32 v32, -v32, v46, v45
	v_div_fmas_f32 v32, v32, v44, v46
	v_div_fixup_f32 v43, v32, v43, 1.0
	v_div_scale_f32 v32, s[46:47], v42, v42, 1.0
	v_rcp_f32_e32 v44, v32
	s_nop 0
	v_fma_f32 v45, -v32, v44, 1.0
	v_fmac_f32_e32 v44, v45, v44
	v_div_scale_f32 v45, vcc, 1.0, v42, 1.0
	v_mul_f32_e32 v46, v45, v44
	v_fma_f32 v47, -v32, v46, v45
	v_fmac_f32_e32 v46, v47, v44
	v_fma_f32 v32, -v32, v46, v45
	v_div_fmas_f32 v32, v32, v44, v46
	v_div_fixup_f32 v42, v32, v42, 1.0
	v_lshlrev_b32_e32 v32, 16, v33
	v_and_b32_e32 v33, 0xffff0000, v33
	v_pk_add_f32 v[30:31], v[30:31], v[32:33]
	v_pk_mul_f32 v[28:29], v[28:29], v[42:43]
	v_mul_f32_e32 v32, 0x3d372713, v30
	v_mul_f32_e32 v33, 0x3d372713, v31
	v_mul_f32_e32 v32, v30, v32
	v_mul_f32_e32 v33, v31, v33
	v_fma_f32 v32, v30, v32, v30
	v_fma_f32 v33, v31, v33, v31
	v_mul_f32_e32 v32, 0x3fcc422a, v32
	v_mul_f32_e32 v33, 0x3fcc422a, v33
	v_mul_f32_e32 v32, 0xbfb8aa3b, v32
	v_mul_f32_e32 v33, 0xbfb8aa3b, v33
	v_exp_f32_e32 v32, v32
	v_exp_f32_e32 v33, v33
	s_nop 0
	v_pk_add_f32 v[32:33], v[32:33], 1.0 op_sel_hi:[1,0]
	s_nop 0
	v_div_scale_f32 v42, s[46:47], v33, v33, 1.0
	v_rcp_f32_e32 v43, v42
	s_nop 0
	v_fma_f32 v44, -v42, v43, 1.0
	v_fmac_f32_e32 v43, v44, v43
	v_div_scale_f32 v44, vcc, 1.0, v33, 1.0
	v_mul_f32_e32 v45, v44, v43
	v_fma_f32 v46, -v42, v45, v44
	v_fmac_f32_e32 v45, v46, v43
	v_fma_f32 v42, -v42, v45, v44
	v_div_fmas_f32 v42, v42, v43, v45
	v_div_fixup_f32 v33, v42, v33, 1.0
	v_div_scale_f32 v42, s[46:47], v32, v32, 1.0
	v_rcp_f32_e32 v43, v42
	s_nop 0
	v_fma_f32 v44, -v42, v43, 1.0
	v_fmac_f32_e32 v43, v44, v43
	v_div_scale_f32 v44, vcc, 1.0, v32, 1.0
	v_mul_f32_e32 v45, v44, v43
	v_fma_f32 v46, -v42, v45, v44
	v_fmac_f32_e32 v45, v46, v43
	v_fma_f32 v42, -v42, v45, v44
	v_div_fmas_f32 v42, v42, v43, v45
	v_div_fixup_f32 v32, v42, v32, 1.0
	v_pk_mul_f32 v[30:31], v[30:31], v[32:33]
	v_lshlrev_b32_e32 v32, 16, v34
	v_and_b32_e32 v33, 0xffff0000, v34
	v_pk_add_f32 v[24:25], v[24:25], v[32:33]
	s_nop 0
	v_mul_f32_e32 v32, 0x3d372713, v24
	v_mul_f32_e32 v33, 0x3d372713, v25
	v_mul_f32_e32 v32, v24, v32
	v_mul_f32_e32 v33, v25, v33
	v_fma_f32 v32, v24, v32, v24
	v_fma_f32 v33, v25, v33, v25
	v_mul_f32_e32 v32, 0x3fcc422a, v32
	v_mul_f32_e32 v33, 0x3fcc422a, v33
	v_mul_f32_e32 v32, 0xbfb8aa3b, v32
	v_mul_f32_e32 v33, 0xbfb8aa3b, v33
	v_exp_f32_e32 v32, v32
	v_exp_f32_e32 v33, v33
	s_nop 0
	v_pk_add_f32 v[32:33], v[32:33], 1.0 op_sel_hi:[1,0]
	s_nop 0
	v_div_scale_f32 v34, s[46:47], v33, v33, 1.0
	v_rcp_f32_e32 v42, v34
	s_nop 0
	v_fma_f32 v43, -v34, v42, 1.0
	v_fmac_f32_e32 v42, v43, v42
	v_div_scale_f32 v43, vcc, 1.0, v33, 1.0
	v_mul_f32_e32 v44, v43, v42
	v_fma_f32 v45, -v34, v44, v43
	v_fmac_f32_e32 v44, v45, v42
	v_fma_f32 v34, -v34, v44, v43
	v_div_fmas_f32 v34, v34, v42, v44
	v_div_fixup_f32 v33, v34, v33, 1.0
	v_div_scale_f32 v34, s[46:47], v32, v32, 1.0
	v_rcp_f32_e32 v42, v34
	s_nop 0
	v_fma_f32 v43, -v34, v42, 1.0
	v_fmac_f32_e32 v42, v43, v42
	v_div_scale_f32 v43, vcc, 1.0, v32, 1.0
	v_mul_f32_e32 v44, v43, v42
	v_fma_f32 v45, -v34, v44, v43
	v_fmac_f32_e32 v44, v45, v42
	v_fma_f32 v34, -v34, v44, v43
	v_div_fmas_f32 v34, v34, v42, v44
	v_div_fixup_f32 v32, v34, v32, 1.0
	v_pk_mul_f32 v[32:33], v[24:25], v[32:33]
	v_lshlrev_b32_e32 v24, 16, v35
	v_and_b32_e32 v25, 0xffff0000, v35
	v_pk_add_f32 v[24:25], v[26:27], v[24:25]
	s_nop 0
	v_mul_f32_e32 v26, 0x3d372713, v24
	v_mul_f32_e32 v27, 0x3d372713, v25
	v_mul_f32_e32 v26, v24, v26
	v_mul_f32_e32 v27, v25, v27
	v_fma_f32 v26, v24, v26, v24
	v_fma_f32 v27, v25, v27, v25
	v_mul_f32_e32 v26, 0x3fcc422a, v26
	v_mul_f32_e32 v27, 0x3fcc422a, v27
	v_mul_f32_e32 v26, 0xbfb8aa3b, v26
	v_mul_f32_e32 v27, 0xbfb8aa3b, v27
	v_exp_f32_e32 v26, v26
	v_exp_f32_e32 v27, v27
	s_nop 0
	v_pk_add_f32 v[26:27], v[26:27], 1.0 op_sel_hi:[1,0]
	s_nop 0
	v_div_scale_f32 v34, s[46:47], v27, v27, 1.0
	v_rcp_f32_e32 v35, v34
	s_nop 0
	v_fma_f32 v42, -v34, v35, 1.0
	v_fmac_f32_e32 v35, v42, v35
	v_div_scale_f32 v42, vcc, 1.0, v27, 1.0
	v_mul_f32_e32 v43, v42, v35
	v_fma_f32 v44, -v34, v43, v42
	v_fmac_f32_e32 v43, v44, v35
	v_fma_f32 v34, -v34, v43, v42
	v_div_fmas_f32 v34, v34, v35, v43
	v_div_fixup_f32 v27, v34, v27, 1.0
	v_div_scale_f32 v34, s[46:47], v26, v26, 1.0
	v_rcp_f32_e32 v35, v34
	s_nop 0
	v_fma_f32 v42, -v34, v35, 1.0
	v_fmac_f32_e32 v35, v42, v35
	v_div_scale_f32 v42, vcc, 1.0, v26, 1.0
	v_mul_f32_e32 v43, v42, v35
	v_fma_f32 v44, -v34, v43, v42
	v_fmac_f32_e32 v43, v44, v35
	v_fma_f32 v34, -v34, v43, v42
	v_div_fmas_f32 v34, v34, v35, v43
	v_div_fixup_f32 v26, v34, v26, 1.0
	v_pk_mul_f32 v[34:35], v[24:25], v[26:27]
	v_cvt_pk_bf16_f32 v24, v28, v29
	v_lshl_add_u64 v[28:29], s[36:37], 0, v[38:39]
	v_cvt_pk_bf16_f32 v25, v30, v31
	v_cvt_pk_bf16_f32 v26, v32, v33
	v_lshl_add_u64 v[32:33], v[28:29], 0, v[124:125]
	v_lshlrev_b64 v[30:31], 1, v[36:37]
	v_lshl_add_u64 v[32:33], v[32:33], 0, v[30:31]
	v_cvt_pk_bf16_f32 v27, v34, v35
	v_lshl_add_u64 v[32:33], v[32:33], 0, v[140:141]
	global_store_dwordx4 v[32:33], v[24:27], off
	s_nop 1
	s_waitcnt vmcnt(11)
; __device__ __forceinline__ float gelu_tanh(float x) { return x * sigmoidf_(1.5957691216057308f * (x + 0.044715f * x * x * x)); }
; __device__ __forceinline__ unsigned cvt_pk_bf16(float lo, float hi) { const f32x2c v = {lo, hi}; const bf16x2c b = __builtin_convertvector(v, bf16x2c); return __builtin_bit_cast(unsigned, b); }
;     __device__ __forceinline__ void operator()(const f32x4 (&acc)[2][2][4][2], const Unit& u, int wr, int wc, int fr, int fq) const {
;     ...
;             for (int m = 0; m < 4; ++m) { const int row = row0 + ai * HALF + m * 16; const int g = row / S5R, rl = row % S5R;
; #pragma unroll
;                 for (int bj = 0; bj < 2; ++bj) { const int col = col0 + bj * HALF;
;                     const u32x4 yi = *(const u32x4*)(YI + (size_t)row * 512 + col);
;                     const unsigned yw[4] = {yi.x, yi.y, yi.z, yi.w};
;                     const f32x4 v0 = acc[ai][bj][m][0], v1 = acc[ai][bj][m][1];
;                     float o[8];
; #pragma unroll
;                     for (int q = 0; q < 4; ++q) { const float al = (q < 2) ? v0[2 * q] : v1[2 * q - 4], ah = (q < 2) ? v0[2 * q + 1] : v1[2 * q - 3];
;                         o[2 * q] = gelu_tanh(al + __builtin_bit_cast(float, yw[q] << 16)); o[2 * q + 1] = gelu_tanh(ah + __builtin_bit_cast(float, yw[q] & 0xffff0000u)); }
;                     u32x4 w; w.x = cvt_pk_bf16(o[0], o[1]); w.y = cvt_pk_bf16(o[2], o[3]); w.z = cvt_pk_bf16(o[4], o[5]); w.w = cvt_pk_bf16(o[6], o[7]);
;                     const size_t tok = (size_t)rl * S5L + (col >> 4);
;                     *(u32x4*)(Z + tok * 512 + g * 16 + (col & 15)) = w; } }
	v_mov_b32_e32 v24, v186
	v_mov_b32_e32 v25, v187
	v_mov_b32_e32 v26, v188
	v_mov_b32_e32 v27, v189
	v_lshlrev_b32_e32 v32, 16, v24
	v_and_b32_e32 v33, 0xffff0000, v24
	v_pk_add_f32 v[20:21], v[20:21], v[32:33]
	s_nop 0
	v_mul_f32_e32 v24, 0x3d372713, v20
	v_mul_f32_e32 v24, v20, v24
	v_fma_f32 v24, v20, v24, v20
	v_mul_f32_e32 v24, 0x3fcc422a, v24
	v_mul_f32_e32 v24, 0xbfb8aa3b, v24
	v_exp_f32_e32 v32, v24
	v_mul_f32_e32 v24, 0x3d372713, v21
	v_mul_f32_e32 v24, v21, v24
	v_fma_f32 v24, v21, v24, v21
	v_mul_f32_e32 v24, 0x3fcc422a, v24
	v_mul_f32_e32 v24, 0xbfb8aa3b, v24
	v_exp_f32_e32 v33, v24
	s_nop 0
	v_pk_add_f32 v[32:33], v[32:33], 1.0 op_sel_hi:[1,0]
	s_nop 0
	v_div_scale_f32 v24, s[46:47], v33, v33, 1.0
	v_rcp_f32_e32 v34, v24
	s_nop 0
	v_fma_f32 v35, -v24, v34, 1.0
	v_fmac_f32_e32 v34, v35, v34
	v_div_scale_f32 v35, vcc, 1.0, v33, 1.0
	v_mul_f32_e32 v36, v35, v34
	v_fma_f32 v37, -v24, v36, v35
	v_fmac_f32_e32 v36, v37, v34
	v_fma_f32 v24, -v24, v36, v35
	v_div_fmas_f32 v24, v24, v34, v36
	v_div_fixup_f32 v33, v24, v33, 1.0
	v_div_scale_f32 v24, s[46:47], v32, v32, 1.0
	v_rcp_f32_e32 v34, v24
	s_nop 0
	v_fma_f32 v35, -v24, v34, 1.0
	v_fmac_f32_e32 v34, v35, v34
	v_div_scale_f32 v35, vcc, 1.0, v32, 1.0
	v_mul_f32_e32 v36, v35, v34
	v_fma_f32 v37, -v24, v36, v35
	v_fmac_f32_e32 v36, v37, v34
	v_fma_f32 v24, -v24, v36, v35
	v_div_fmas_f32 v24, v24, v34, v36
	v_div_fixup_f32 v32, v24, v32, 1.0
	v_lshlrev_b32_e32 v24, 16, v25
	v_and_b32_e32 v25, 0xffff0000, v25
	v_pk_add_f32 v[22:23], v[22:23], v[24:25]
	v_pk_mul_f32 v[20:21], v[20:21], v[32:33]
	v_mul_f32_e32 v24, 0x3d372713, v22
	v_mul_f32_e32 v25, 0x3d372713, v23
	v_mul_f32_e32 v24, v22, v24
	v_mul_f32_e32 v25, v23, v25
	v_fma_f32 v24, v22, v24, v22
	v_fma_f32 v25, v23, v25, v23
	v_mul_f32_e32 v24, 0x3fcc422a, v24
	v_mul_f32_e32 v25, 0x3fcc422a, v25
	v_mul_f32_e32 v24, 0xbfb8aa3b, v24
	v_mul_f32_e32 v25, 0xbfb8aa3b, v25
	v_exp_f32_e32 v24, v24
	v_exp_f32_e32 v25, v25
	s_nop 0
	v_pk_add_f32 v[24:25], v[24:25], 1.0 op_sel_hi:[1,0]
	s_nop 0
	v_div_scale_f32 v32, s[46:47], v25, v25, 1.0
	v_rcp_f32_e32 v33, v32
	s_nop 0
	v_fma_f32 v34, -v32, v33, 1.0
	v_fmac_f32_e32 v33, v34, v33
	v_div_scale_f32 v34, vcc, 1.0, v25, 1.0
	v_mul_f32_e32 v35, v34, v33
	v_fma_f32 v36, -v32, v35, v34
	v_fmac_f32_e32 v35, v36, v33
	v_fma_f32 v32, -v32, v35, v34
	v_div_fmas_f32 v32, v32, v33, v35
	v_div_fixup_f32 v25, v32, v25, 1.0
	v_div_scale_f32 v32, s[46:47], v24, v24, 1.0
	v_rcp_f32_e32 v33, v32
	s_nop 0
	v_fma_f32 v34, -v32, v33, 1.0
	v_fmac_f32_e32 v33, v34, v33
	v_div_scale_f32 v34, vcc, 1.0, v24, 1.0
	v_mul_f32_e32 v35, v34, v33
	v_fma_f32 v36, -v32, v35, v34
	v_fmac_f32_e32 v35, v36, v33
	v_fma_f32 v32, -v32, v35, v34
	v_div_fmas_f32 v32, v32, v33, v35
	v_div_fixup_f32 v24, v32, v24, 1.0
	v_pk_mul_f32 v[22:23], v[22:23], v[24:25]
	v_lshlrev_b32_e32 v24, 16, v26
	v_and_b32_e32 v25, 0xffff0000, v26
	v_pk_add_f32 v[16:17], v[16:17], v[24:25]
	s_nop 0
	v_mul_f32_e32 v24, 0x3d372713, v16
	v_mul_f32_e32 v25, 0x3d372713, v17
	v_mul_f32_e32 v24, v16, v24
	v_mul_f32_e32 v25, v17, v25
	v_fma_f32 v24, v16, v24, v16
	v_fma_f32 v25, v17, v25, v17
	v_mul_f32_e32 v24, 0x3fcc422a, v24
	v_mul_f32_e32 v25, 0x3fcc422a, v25
	v_mul_f32_e32 v24, 0xbfb8aa3b, v24
	v_mul_f32_e32 v25, 0xbfb8aa3b, v25
	v_exp_f32_e32 v24, v24
	v_exp_f32_e32 v25, v25
	s_nop 0
	v_pk_add_f32 v[24:25], v[24:25], 1.0 op_sel_hi:[1,0]
	s_nop 0
	v_div_scale_f32 v26, s[46:47], v25, v25, 1.0
	v_rcp_f32_e32 v32, v26
	s_nop 0
	v_fma_f32 v33, -v26, v32, 1.0
	v_fmac_f32_e32 v32, v33, v32
	v_div_scale_f32 v33, vcc, 1.0, v25, 1.0
	v_mul_f32_e32 v34, v33, v32
	v_fma_f32 v35, -v26, v34, v33
	v_fmac_f32_e32 v34, v35, v32
	v_fma_f32 v26, -v26, v34, v33
	v_div_fmas_f32 v26, v26, v32, v34
	v_div_fixup_f32 v25, v26, v25, 1.0
	v_div_scale_f32 v26, s[46:47], v24, v24, 1.0
	v_rcp_f32_e32 v32, v26
	s_nop 0
	v_fma_f32 v33, -v26, v32, 1.0
	v_fmac_f32_e32 v32, v33, v32
	v_div_scale_f32 v33, vcc, 1.0, v24, 1.0
	v_mul_f32_e32 v34, v33, v32
	v_fma_f32 v35, -v26, v34, v33
	v_fmac_f32_e32 v34, v35, v32
	v_fma_f32 v26, -v26, v34, v33
	v_div_fmas_f32 v26, v26, v32, v34
	v_div_fixup_f32 v24, v26, v24, 1.0
	v_pk_mul_f32 v[24:25], v[16:17], v[24:25]
	v_lshlrev_b32_e32 v16, 16, v27
	v_and_b32_e32 v17, 0xffff0000, v27
	v_pk_add_f32 v[16:17], v[18:19], v[16:17]
	s_nop 0
	v_mul_f32_e32 v18, 0x3d372713, v16
	v_mul_f32_e32 v19, 0x3d372713, v17
	v_mul_f32_e32 v18, v16, v18
	v_mul_f32_e32 v19, v17, v19
	v_fma_f32 v18, v16, v18, v16
	v_fma_f32 v19, v17, v19, v17
	v_mul_f32_e32 v18, 0x3fcc422a, v18
	v_mul_f32_e32 v19, 0x3fcc422a, v19
	v_mul_f32_e32 v18, 0xbfb8aa3b, v18
	v_mul_f32_e32 v19, 0xbfb8aa3b, v19
	v_exp_f32_e32 v18, v18
	v_exp_f32_e32 v19, v19
	s_nop 0
	v_pk_add_f32 v[18:19], v[18:19], 1.0 op_sel_hi:[1,0]
	s_nop 0
	v_div_scale_f32 v26, s[46:47], v19, v19, 1.0
	v_rcp_f32_e32 v27, v26
	s_nop 0
	v_fma_f32 v32, -v26, v27, 1.0
	v_fmac_f32_e32 v27, v32, v27
	v_div_scale_f32 v32, vcc, 1.0, v19, 1.0
	v_mul_f32_e32 v33, v32, v27
	v_fma_f32 v34, -v26, v33, v32
	v_fmac_f32_e32 v33, v34, v27
	v_fma_f32 v26, -v26, v33, v32
	v_div_fmas_f32 v26, v26, v27, v33
	v_div_fixup_f32 v19, v26, v19, 1.0
	v_div_scale_f32 v26, s[46:47], v18, v18, 1.0
	v_rcp_f32_e32 v27, v26
	s_nop 0
	v_fma_f32 v32, -v26, v27, 1.0
	v_fmac_f32_e32 v27, v32, v27
	v_div_scale_f32 v32, vcc, 1.0, v18, 1.0
	v_mul_f32_e32 v33, v32, v27
	v_fma_f32 v34, -v26, v33, v32
	v_fmac_f32_e32 v33, v34, v27
	v_fma_f32 v26, -v26, v33, v32
	v_div_fmas_f32 v26, v26, v27, v33
	v_div_fixup_f32 v18, v26, v18, 1.0
	v_pk_mul_f32 v[26:27], v[16:17], v[18:19]
	v_cvt_pk_bf16_f32 v16, v20, v21
	v_lshl_add_u64 v[20:21], v[28:29], 0, v[116:117]
	v_lshl_add_u64 v[20:21], v[20:21], 0, v[30:31]
	v_cvt_pk_bf16_f32 v17, v22, v23
	v_cvt_pk_bf16_f32 v18, v24, v25
	v_cvt_pk_bf16_f32 v19, v26, v27
	v_lshl_add_u64 v[20:21], v[20:21], 0, v[140:141]
	global_store_dwordx4 v[20:21], v[16:19], off
	s_nop 1
	v_add_u32_e32 v16, 0xb0, v142
	v_ashrrev_i32_e32 v17, 31, v16
	v_lshrrev_b32_e32 v18, 21, v17
	v_add_u32_e32 v18, v16, v18
	v_ashrrev_i32_e32 v20, 11, v18
	v_mul_i32_i24_e32 v18, 0x800, v20
	v_sub_u32_e32 v18, v16, v18
	v_lshlrev_b64 v[16:17], 10, v[16:17]
	v_lshl_add_u64 v[16:17], s[30:31], 0, v[16:17]
	v_ashrrev_i32_e32 v19, 31, v18
	v_lshl_add_u64 v[24:25], v[16:17], 0, v[144:145]
	v_lshlrev_b64 v[22:23], 15, v[18:19]
	s_nop 1
	v_lshlrev_b32_e32 v20, 4, v20
	v_ashrrev_i32_e32 v21, 31, v20
	s_waitcnt vmcnt(10)
; __device__ __forceinline__ float gelu_tanh(float x) { return x * sigmoidf_(1.5957691216057308f * (x + 0.044715f * x * x * x)); }
; __device__ __forceinline__ unsigned cvt_pk_bf16(float lo, float hi) { const f32x2c v = {lo, hi}; const bf16x2c b = __builtin_convertvector(v, bf16x2c); return __builtin_bit_cast(unsigned, b); }
;     __device__ __forceinline__ void operator()(const f32x4 (&acc)[2][2][4][2], const Unit& u, int wr, int wc, int fr, int fq) const {
;     ...
;             for (int m = 0; m < 4; ++m) { const int row = row0 + ai * HALF + m * 16; const int g = row / S5R, rl = row % S5R;
; #pragma unroll
;                 for (int bj = 0; bj < 2; ++bj) { const int col = col0 + bj * HALF;
;                     const u32x4 yi = *(const u32x4*)(YI + (size_t)row * 512 + col);
;                     const unsigned yw[4] = {yi.x, yi.y, yi.z, yi.w};
;                     const f32x4 v0 = acc[ai][bj][m][0], v1 = acc[ai][bj][m][1];
;                     float o[8];
; #pragma unroll
;                     for (int q = 0; q < 4; ++q) { const float al = (q < 2) ? v0[2 * q] : v1[2 * q - 4], ah = (q < 2) ? v0[2 * q + 1] : v1[2 * q - 3];
;                         o[2 * q] = gelu_tanh(al + __builtin_bit_cast(float, yw[q] << 16)); o[2 * q + 1] = gelu_tanh(ah + __builtin_bit_cast(float, yw[q] & 0xffff0000u)); }
;                     u32x4 w; w.x = cvt_pk_bf16(o[0], o[1]); w.y = cvt_pk_bf16(o[2], o[3]); w.z = cvt_pk_bf16(o[4], o[5]); w.w = cvt_pk_bf16(o[6], o[7]);
;                     const size_t tok = (size_t)rl * S5L + (col >> 4);
;                     *(u32x4*)(Z + tok * 512 + g * 16 + (col & 15)) = w; } }
	v_mov_b32_e32 v16, v190
	v_mov_b32_e32 v17, v191
	v_mov_b32_e32 v18, v192
	v_mov_b32_e32 v19, v193
	v_lshlrev_b32_e32 v26, 16, v16
	v_and_b32_e32 v27, 0xffff0000, v16
	v_pk_add_f32 v[12:13], v[12:13], v[26:27]
	s_nop 0
	v_mul_f32_e32 v16, 0x3d372713, v12
	v_mul_f32_e32 v16, v12, v16
	v_fma_f32 v16, v12, v16, v12
	v_mul_f32_e32 v16, 0x3fcc422a, v16
	v_mul_f32_e32 v16, 0xbfb8aa3b, v16
	v_exp_f32_e32 v26, v16
	v_mul_f32_e32 v16, 0x3d372713, v13
	v_mul_f32_e32 v16, v13, v16
	v_fma_f32 v16, v13, v16, v13
	v_mul_f32_e32 v16, 0x3fcc422a, v16
	v_mul_f32_e32 v16, 0xbfb8aa3b, v16
	v_exp_f32_e32 v27, v16
	s_nop 0
	v_pk_add_f32 v[26:27], v[26:27], 1.0 op_sel_hi:[1,0]
	s_nop 0
	v_div_scale_f32 v16, s[46:47], v27, v27, 1.0
	v_rcp_f32_e32 v28, v16
	s_nop 0
	v_fma_f32 v29, -v16, v28, 1.0
	v_fmac_f32_e32 v28, v29, v28
	v_div_scale_f32 v29, vcc, 1.0, v27, 1.0
	v_mul_f32_e32 v30, v29, v28
	v_fma_f32 v31, -v16, v30, v29
	v_fmac_f32_e32 v30, v31, v28
	v_fma_f32 v16, -v16, v30, v29
	v_div_fmas_f32 v16, v16, v28, v30
	v_div_fixup_f32 v27, v16, v27, 1.0
	v_div_scale_f32 v16, s[46:47], v26, v26, 1.0
	v_rcp_f32_e32 v28, v16
	s_nop 0
	v_fma_f32 v29, -v16, v28, 1.0
	v_fmac_f32_e32 v28, v29, v28
	v_div_scale_f32 v29, vcc, 1.0, v26, 1.0
	v_mul_f32_e32 v30, v29, v28
	v_fma_f32 v31, -v16, v30, v29
	v_fmac_f32_e32 v30, v31, v28
	v_fma_f32 v16, -v16, v30, v29
	v_div_fmas_f32 v16, v16, v28, v30
	v_div_fixup_f32 v26, v16, v26, 1.0
	v_lshlrev_b32_e32 v16, 16, v17
	v_and_b32_e32 v17, 0xffff0000, v17
	v_pk_add_f32 v[14:15], v[14:15], v[16:17]
	v_pk_mul_f32 v[12:13], v[12:13], v[26:27]
	v_mul_f32_e32 v16, 0x3d372713, v14
	v_mul_f32_e32 v17, 0x3d372713, v15
	v_mul_f32_e32 v16, v14, v16
	v_mul_f32_e32 v17, v15, v17
	v_fma_f32 v16, v14, v16, v14
	v_fma_f32 v17, v15, v17, v15
	v_mul_f32_e32 v16, 0x3fcc422a, v16
	v_mul_f32_e32 v17, 0x3fcc422a, v17
	v_mul_f32_e32 v16, 0xbfb8aa3b, v16
	v_mul_f32_e32 v17, 0xbfb8aa3b, v17
	v_exp_f32_e32 v16, v16
	v_exp_f32_e32 v17, v17
	s_nop 0
	v_pk_add_f32 v[16:17], v[16:17], 1.0 op_sel_hi:[1,0]
	s_nop 0
	v_div_scale_f32 v26, s[46:47], v17, v17, 1.0
	v_rcp_f32_e32 v27, v26
	s_nop 0
	v_fma_f32 v28, -v26, v27, 1.0
	v_fmac_f32_e32 v27, v28, v27
	v_div_scale_f32 v28, vcc, 1.0, v17, 1.0
	v_mul_f32_e32 v29, v28, v27
	v_fma_f32 v30, -v26, v29, v28
	v_fmac_f32_e32 v29, v30, v27
	v_fma_f32 v26, -v26, v29, v28
	v_div_fmas_f32 v26, v26, v27, v29
	v_div_fixup_f32 v17, v26, v17, 1.0
	v_div_scale_f32 v26, s[46:47], v16, v16, 1.0
	v_rcp_f32_e32 v27, v26
	s_nop 0
	v_fma_f32 v28, -v26, v27, 1.0
	v_fmac_f32_e32 v27, v28, v27
	v_div_scale_f32 v28, vcc, 1.0, v16, 1.0
	v_mul_f32_e32 v29, v28, v27
	v_fma_f32 v30, -v26, v29, v28
	v_fmac_f32_e32 v29, v30, v27
	v_fma_f32 v26, -v26, v29, v28
	v_div_fmas_f32 v26, v26, v27, v29
	v_div_fixup_f32 v16, v26, v16, 1.0
	v_pk_mul_f32 v[14:15], v[14:15], v[16:17]
	v_lshlrev_b32_e32 v16, 16, v18
	v_and_b32_e32 v17, 0xffff0000, v18
	v_pk_add_f32 v[8:9], v[8:9], v[16:17]
	s_nop 0
	v_mul_f32_e32 v16, 0x3d372713, v8
	v_mul_f32_e32 v17, 0x3d372713, v9
	v_mul_f32_e32 v16, v8, v16
	v_mul_f32_e32 v17, v9, v17
	v_fma_f32 v16, v8, v16, v8
	v_fma_f32 v17, v9, v17, v9
	v_mul_f32_e32 v16, 0x3fcc422a, v16
	v_mul_f32_e32 v17, 0x3fcc422a, v17
	v_mul_f32_e32 v16, 0xbfb8aa3b, v16
	v_mul_f32_e32 v17, 0xbfb8aa3b, v17
	v_exp_f32_e32 v16, v16
	v_exp_f32_e32 v17, v17
	s_nop 0
	v_pk_add_f32 v[16:17], v[16:17], 1.0 op_sel_hi:[1,0]
	s_nop 0
	v_div_scale_f32 v18, s[46:47], v17, v17, 1.0
	v_rcp_f32_e32 v26, v18
	s_nop 0
	v_fma_f32 v27, -v18, v26, 1.0
	v_fmac_f32_e32 v26, v27, v26
	v_div_scale_f32 v27, vcc, 1.0, v17, 1.0
	v_mul_f32_e32 v28, v27, v26
	v_fma_f32 v29, -v18, v28, v27
	v_fmac_f32_e32 v28, v29, v26
	v_fma_f32 v18, -v18, v28, v27
	v_div_fmas_f32 v18, v18, v26, v28
	v_div_fixup_f32 v17, v18, v17, 1.0
	v_div_scale_f32 v18, s[46:47], v16, v16, 1.0
	v_rcp_f32_e32 v26, v18
	s_nop 0
	v_fma_f32 v27, -v18, v26, 1.0
	v_fmac_f32_e32 v26, v27, v26
	v_div_scale_f32 v27, vcc, 1.0, v16, 1.0
	v_mul_f32_e32 v28, v27, v26
	v_fma_f32 v29, -v18, v28, v27
	v_fmac_f32_e32 v28, v29, v26
	v_fma_f32 v18, -v18, v28, v27
	v_div_fmas_f32 v18, v18, v26, v28
	v_div_fixup_f32 v16, v18, v16, 1.0
	v_pk_mul_f32 v[16:17], v[8:9], v[16:17]
	v_lshlrev_b32_e32 v8, 16, v19
	v_and_b32_e32 v9, 0xffff0000, v19
	v_pk_add_f32 v[8:9], v[10:11], v[8:9]
	s_nop 0
	v_mul_f32_e32 v10, 0x3d372713, v8
	v_mul_f32_e32 v11, 0x3d372713, v9
	v_mul_f32_e32 v10, v8, v10
	v_mul_f32_e32 v11, v9, v11
	v_fma_f32 v10, v8, v10, v8
	v_fma_f32 v11, v9, v11, v9
	v_mul_f32_e32 v10, 0x3fcc422a, v10
	v_mul_f32_e32 v11, 0x3fcc422a, v11
	v_mul_f32_e32 v10, 0xbfb8aa3b, v10
	v_mul_f32_e32 v11, 0xbfb8aa3b, v11
	v_exp_f32_e32 v10, v10
	v_exp_f32_e32 v11, v11
	s_nop 0
	v_pk_add_f32 v[10:11], v[10:11], 1.0 op_sel_hi:[1,0]
	s_nop 0
	v_div_scale_f32 v18, s[46:47], v11, v11, 1.0
	v_rcp_f32_e32 v19, v18
	s_nop 0
	v_fma_f32 v26, -v18, v19, 1.0
	v_fmac_f32_e32 v19, v26, v19
	v_div_scale_f32 v26, vcc, 1.0, v11, 1.0
	v_mul_f32_e32 v27, v26, v19
	v_fma_f32 v28, -v18, v27, v26
	v_fmac_f32_e32 v27, v28, v19
	v_fma_f32 v18, -v18, v27, v26
	v_div_fmas_f32 v18, v18, v19, v27
	v_div_fixup_f32 v11, v18, v11, 1.0
	v_div_scale_f32 v18, s[46:47], v10, v10, 1.0
	v_rcp_f32_e32 v19, v18
	s_nop 0
	v_fma_f32 v26, -v18, v19, 1.0
	v_fmac_f32_e32 v19, v26, v19
	v_div_scale_f32 v26, vcc, 1.0, v10, 1.0
	v_mul_f32_e32 v27, v26, v19
	v_fma_f32 v28, -v18, v27, v26
	v_fmac_f32_e32 v27, v28, v19
	v_fma_f32 v18, -v18, v27, v26
	v_div_fmas_f32 v18, v18, v19, v27
	v_div_fixup_f32 v10, v18, v10, 1.0
	v_pk_mul_f32 v[18:19], v[8:9], v[10:11]
	v_cvt_pk_bf16_f32 v8, v12, v13
	v_lshl_add_u64 v[12:13], s[36:37], 0, v[22:23]
	v_cvt_pk_bf16_f32 v9, v14, v15
	v_cvt_pk_bf16_f32 v10, v16, v17
	v_lshl_add_u64 v[16:17], v[12:13], 0, v[124:125]
	v_lshlrev_b64 v[14:15], 1, v[20:21]
	v_lshl_add_u64 v[16:17], v[16:17], 0, v[14:15]
	v_cvt_pk_bf16_f32 v11, v18, v19
	v_lshl_add_u64 v[16:17], v[16:17], 0, v[140:141]
	global_store_dwordx4 v[16:17], v[8:11], off
	s_nop 1
	s_waitcnt vmcnt(9)
; __device__ __forceinline__ unsigned cvt_pk_bf16(float lo, float hi) { const f32x2c v = {lo, hi}; const bf16x2c b = __builtin_convertvector(v, bf16x2c); return __builtin_bit_cast(unsigned, b); }
; __device__ __forceinline__ float sigmoidf_(float x) { return 1.f / (1.f + __expf(-x)); }
; __device__ __forceinline__ float gelu_tanh(float x) { return x * sigmoidf_(1.5957691216057308f * (x + 0.044715f * x * x * x)); }
;     __device__ __forceinline__ void operator()(const f32x4 (&acc)[2][2][4][2], const Unit& u, int wr, int wc, int fr, int fq) const {
;     ...
;             for (int m = 0; m < 4; ++m) { const int row = row0 + ai * HALF + m * 16; const int g = row / S5R, rl = row % S5R;
; #pragma unroll
;                 for (int bj = 0; bj < 2; ++bj) { const int col = col0 + bj * HALF;
;                     const u32x4 yi = *(const u32x4*)(YI + (size_t)row * 512 + col);
;                     const unsigned yw[4] = {yi.x, yi.y, yi.z, yi.w};
;                     const f32x4 v0 = acc[ai][bj][m][0], v1 = acc[ai][bj][m][1];
;                     float o[8];
; #pragma unroll
;                     for (int q = 0; q < 4; ++q) { const float al = (q < 2) ? v0[2 * q] : v1[2 * q - 4], ah = (q < 2) ? v0[2 * q + 1] : v1[2 * q - 3];
;                         o[2 * q] = gelu_tanh(al + __builtin_bit_cast(float, yw[q] << 16)); o[2 * q + 1] = gelu_tanh(ah + __builtin_bit_cast(float, yw[q] & 0xffff0000u)); }
;                     u32x4 w; w.x = cvt_pk_bf16(o[0], o[1]); w.y = cvt_pk_bf16(o[2], o[3]); w.z = cvt_pk_bf16(o[4], o[5]); w.w = cvt_pk_bf16(o[6], o[7]);
;                     const size_t tok = (size_t)rl * S5L + (col >> 4);
;                     *(u32x4*)(Z + tok * 512 + g * 16 + (col & 15)) = w; } }
	v_mov_b32_e32 v8, v194
	v_mov_b32_e32 v9, v195
	v_mov_b32_e32 v10, v196
	v_mov_b32_e32 v11, v197
	v_lshlrev_b32_e32 v16, 16, v8
	v_and_b32_e32 v17, 0xffff0000, v8
	v_pk_add_f32 v[4:5], v[4:5], v[16:17]
	s_nop 0
	v_mul_f32_e32 v8, 0x3d372713, v4
	v_mul_f32_e32 v8, v4, v8
	v_fma_f32 v8, v4, v8, v4
	v_mul_f32_e32 v8, 0x3fcc422a, v8
	v_mul_f32_e32 v8, 0xbfb8aa3b, v8
	v_exp_f32_e32 v16, v8
	v_mul_f32_e32 v8, 0x3d372713, v5
	v_mul_f32_e32 v8, v5, v8
	v_fma_f32 v8, v5, v8, v5
	v_mul_f32_e32 v8, 0x3fcc422a, v8
	v_mul_f32_e32 v8, 0xbfb8aa3b, v8
	v_exp_f32_e32 v17, v8
	s_nop 0
	v_pk_add_f32 v[16:17], v[16:17], 1.0 op_sel_hi:[1,0]
	s_nop 0
	v_div_scale_f32 v8, s[46:47], v17, v17, 1.0
	v_rcp_f32_e32 v18, v8
	s_nop 0
	v_fma_f32 v19, -v8, v18, 1.0
	v_fmac_f32_e32 v18, v19, v18
	v_div_scale_f32 v19, vcc, 1.0, v17, 1.0
	v_mul_f32_e32 v20, v19, v18
	v_fma_f32 v21, -v8, v20, v19
	v_fmac_f32_e32 v20, v21, v18
	v_fma_f32 v8, -v8, v20, v19
	v_div_fmas_f32 v8, v8, v18, v20
	v_div_fixup_f32 v17, v8, v17, 1.0
	v_div_scale_f32 v8, s[46:47], v16, v16, 1.0
	v_rcp_f32_e32 v18, v8
	s_nop 0
	v_fma_f32 v19, -v8, v18, 1.0
	v_fmac_f32_e32 v18, v19, v18
	v_div_scale_f32 v19, vcc, 1.0, v16, 1.0
	v_mul_f32_e32 v20, v19, v18
	v_fma_f32 v21, -v8, v20, v19
	v_fmac_f32_e32 v20, v21, v18
	v_fma_f32 v8, -v8, v20, v19
	v_div_fmas_f32 v8, v8, v18, v20
	v_div_fixup_f32 v16, v8, v16, 1.0
	v_lshlrev_b32_e32 v8, 16, v9
	v_and_b32_e32 v9, 0xffff0000, v9
	v_pk_add_f32 v[6:7], v[6:7], v[8:9]
	v_pk_mul_f32 v[4:5], v[4:5], v[16:17]
	v_mul_f32_e32 v8, 0x3d372713, v6
	v_mul_f32_e32 v9, 0x3d372713, v7
	v_mul_f32_e32 v8, v6, v8
	v_mul_f32_e32 v9, v7, v9
	v_fma_f32 v8, v6, v8, v6
	v_fma_f32 v9, v7, v9, v7
	v_mul_f32_e32 v8, 0x3fcc422a, v8
	v_mul_f32_e32 v9, 0x3fcc422a, v9
	v_mul_f32_e32 v8, 0xbfb8aa3b, v8
	v_mul_f32_e32 v9, 0xbfb8aa3b, v9
	v_exp_f32_e32 v8, v8
	v_exp_f32_e32 v9, v9
	s_nop 0
	v_pk_add_f32 v[8:9], v[8:9], 1.0 op_sel_hi:[1,0]
	s_nop 0
	v_div_scale_f32 v16, s[46:47], v9, v9, 1.0
	v_rcp_f32_e32 v17, v16
	s_nop 0
	v_fma_f32 v18, -v16, v17, 1.0
	v_fmac_f32_e32 v17, v18, v17
	v_div_scale_f32 v18, vcc, 1.0, v9, 1.0
	v_mul_f32_e32 v19, v18, v17
	v_fma_f32 v20, -v16, v19, v18
	v_fmac_f32_e32 v19, v20, v17
	v_fma_f32 v16, -v16, v19, v18
	v_div_fmas_f32 v16, v16, v17, v19
	v_div_fixup_f32 v9, v16, v9, 1.0
	v_div_scale_f32 v16, s[46:47], v8, v8, 1.0
	v_rcp_f32_e32 v17, v16
	s_nop 0
	v_fma_f32 v18, -v16, v17, 1.0
	v_fmac_f32_e32 v17, v18, v17
	v_div_scale_f32 v18, vcc, 1.0, v8, 1.0
	v_mul_f32_e32 v19, v18, v17
	v_fma_f32 v20, -v16, v19, v18
	v_fmac_f32_e32 v19, v20, v17
	v_fma_f32 v16, -v16, v19, v18
	v_div_fmas_f32 v16, v16, v17, v19
	v_div_fixup_f32 v8, v16, v8, 1.0
	v_pk_mul_f32 v[6:7], v[6:7], v[8:9]
	v_lshlrev_b32_e32 v8, 16, v10
	v_and_b32_e32 v9, 0xffff0000, v10
	v_pk_add_f32 v[0:1], v[0:1], v[8:9]
	s_nop 0
	v_mul_f32_e32 v8, 0x3d372713, v0
	v_mul_f32_e32 v9, 0x3d372713, v1
	v_mul_f32_e32 v8, v0, v8
	v_mul_f32_e32 v9, v1, v9
	v_fma_f32 v8, v0, v8, v0
	v_fma_f32 v9, v1, v9, v1
	v_mul_f32_e32 v8, 0x3fcc422a, v8
	v_mul_f32_e32 v9, 0x3fcc422a, v9
	v_mul_f32_e32 v8, 0xbfb8aa3b, v8
	v_mul_f32_e32 v9, 0xbfb8aa3b, v9
	v_exp_f32_e32 v8, v8
	v_exp_f32_e32 v9, v9
	s_nop 0
	v_pk_add_f32 v[8:9], v[8:9], 1.0 op_sel_hi:[1,0]
	s_nop 0
	v_div_scale_f32 v10, s[46:47], v9, v9, 1.0
	v_rcp_f32_e32 v16, v10
	s_nop 0
	v_fma_f32 v17, -v10, v16, 1.0
	v_fmac_f32_e32 v16, v17, v16
	v_div_scale_f32 v17, vcc, 1.0, v9, 1.0
	v_mul_f32_e32 v18, v17, v16
	v_fma_f32 v19, -v10, v18, v17
	v_fmac_f32_e32 v18, v19, v16
	v_fma_f32 v10, -v10, v18, v17
	v_div_fmas_f32 v10, v10, v16, v18
	v_div_fixup_f32 v9, v10, v9, 1.0
	v_div_scale_f32 v10, s[46:47], v8, v8, 1.0
	v_rcp_f32_e32 v16, v10
	s_nop 0
	v_fma_f32 v17, -v10, v16, 1.0
	v_fmac_f32_e32 v16, v17, v16
	v_div_scale_f32 v17, vcc, 1.0, v8, 1.0
	v_mul_f32_e32 v18, v17, v16
	v_fma_f32 v19, -v10, v18, v17
	v_fmac_f32_e32 v18, v19, v16
	v_fma_f32 v10, -v10, v18, v17
	v_div_fmas_f32 v10, v10, v16, v18
	v_div_fixup_f32 v8, v10, v8, 1.0
	v_pk_mul_f32 v[8:9], v[0:1], v[8:9]
	v_lshlrev_b32_e32 v0, 16, v11
	v_and_b32_e32 v1, 0xffff0000, v11
	v_pk_add_f32 v[0:1], v[2:3], v[0:1]
	s_nop 0
	v_mul_f32_e32 v2, 0x3d372713, v0
	v_mul_f32_e32 v3, 0x3d372713, v1
	v_mul_f32_e32 v2, v0, v2
	v_mul_f32_e32 v3, v1, v3
	v_fma_f32 v2, v0, v2, v0
	v_fma_f32 v3, v1, v3, v1
	v_mul_f32_e32 v2, 0x3fcc422a, v2
	v_mul_f32_e32 v3, 0x3fcc422a, v3
	v_mul_f32_e32 v2, 0xbfb8aa3b, v2
	v_mul_f32_e32 v3, 0xbfb8aa3b, v3
	v_exp_f32_e32 v2, v2
	v_exp_f32_e32 v3, v3
	s_nop 0
	v_pk_add_f32 v[2:3], v[2:3], 1.0 op_sel_hi:[1,0]
	s_nop 0
	v_div_scale_f32 v10, s[46:47], v3, v3, 1.0
	v_rcp_f32_e32 v11, v10
	s_nop 0
	v_fma_f32 v16, -v10, v11, 1.0
	v_fmac_f32_e32 v11, v16, v11
	v_div_scale_f32 v16, vcc, 1.0, v3, 1.0
	v_mul_f32_e32 v17, v16, v11
	v_fma_f32 v18, -v10, v17, v16
	v_fmac_f32_e32 v17, v18, v11
	v_fma_f32 v10, -v10, v17, v16
	v_div_fmas_f32 v10, v10, v11, v17
	v_div_fixup_f32 v3, v10, v3, 1.0
	v_div_scale_f32 v10, s[46:47], v2, v2, 1.0
	v_rcp_f32_e32 v11, v10
	s_mov_b64 s[46:47], -1
	v_fma_f32 v16, -v10, v11, 1.0
	v_fmac_f32_e32 v11, v16, v11
	v_div_scale_f32 v16, vcc, 1.0, v2, 1.0
	v_mul_f32_e32 v17, v16, v11
	v_fma_f32 v18, -v10, v17, v16
	v_fmac_f32_e32 v17, v18, v11
	v_fma_f32 v10, -v10, v17, v16
	v_div_fmas_f32 v10, v10, v11, v17
	v_div_fixup_f32 v2, v10, v2, 1.0
	v_pk_mul_f32 v[10:11], v[0:1], v[2:3]
	v_cvt_pk_bf16_f32 v0, v4, v5
	v_lshl_add_u64 v[4:5], v[12:13], 0, v[116:117]
	v_lshl_add_u64 v[4:5], v[4:5], 0, v[14:15]
	v_cvt_pk_bf16_f32 v1, v6, v7
	v_cvt_pk_bf16_f32 v2, v8, v9
	v_cvt_pk_bf16_f32 v3, v10, v11
	v_lshl_add_u64 v[4:5], v[4:5], 0, v[140:141]
	s_and_b64 vcc, exec, s[0:1]
	global_store_dwordx4 v[4:5], v[0:3], off
	s_cbranch_vccnz .LBB0_1884
	s_andn2_b64 vcc, exec, s[2:3]
	s_cbranch_vccnz .LBB0_1883
	s_barrier
	s_branch .LBB0_1883
